# speedup vs baseline: 1.0285x; 1.0024x over previous
_Z4ln_kPKfS0_S0_S0_PfPDF16_:
	v_lshlrev_b32_e32 v59, 4, v0
	s_getpc_b64 s[14:15]
	s_add_u32 s14, s14, 0xa2f8
	s_addc_u32 s15, s15, 0x0
	global_load_dword v60, v59, s[14:15]
	v_add_u32_e32 v59, 0x1000, v59
	global_load_dword v60, v59, s[14:15]
	v_add_u32_e32 v59, 0x1000, v59
	global_load_dword v60, v59, s[14:15]
	v_add_u32_e32 v59, 0x1000, v59
	global_load_dword v60, v59, s[14:15]
	v_lshlrev_b32_e32 v59, 4, v0
	s_load_dwordx8 s[4:11], s[0:1], 0x0
	v_lshrrev_b32_e32 v1, 6, v0
	v_lshl_or_b32 v54, s2, 2, v1
	s_movk_i32 s12, 0xc00
	v_and_b32_e32 v55, 63, v0
	s_waitcnt lgkmcnt(0)
	v_mov_b64_e32 v[2:3], s[4:5]
	v_mad_i64_i32 v[4:5], s[2:3], v54, s12, v[2:3]
	v_mov_b64_e32 v[2:3], s[6:7]
	v_mad_i64_i32 v[6:7], s[2:3], v54, s12, v[2:3]
	v_lshlrev_b32_e32 v2, 4, v55
	v_mov_b32_e32 v3, 0
	v_lshl_add_u64 v[30:31], v[6:7], 0, v[2:3]
	v_lshl_add_u64 v[28:29], v[4:5], 0, v[2:3]
	global_load_dwordx4 v[4:7], v[30:31], off
	global_load_dwordx4 v[8:11], v[28:29], off
	global_load_dwordx4 v[12:15], v[28:29], off offset:1024
	global_load_dwordx4 v[16:19], v[30:31], off offset:1024
	global_load_dwordx4 v[20:23], v[28:29], off offset:2048
	global_load_dwordx4 v[24:27], v[30:31], off offset:2048
	s_nop 0
	global_load_dwordx4 v[28:31], v2, s[8:9]
	global_load_dwordx4 v[32:35], v2, s[10:11]
	global_load_dwordx4 v[36:39], v2, s[8:9] offset:1024
	global_load_dwordx4 v[40:43], v2, s[10:11] offset:1024
	s_load_dwordx4 s[4:7], s[0:1], 0x20
	v_and_b32_e32 v50, 16, v0
	v_cmp_eq_u32_e32 vcc, 0, v50
	v_and_b32_e32 v51, 32, v0
	v_mov_b32_e32 v56, 0x2b8cbccc
	s_waitcnt lgkmcnt(0)
	v_mov_b64_e32 v[0:1], s[4:5]
	v_mad_i64_i32 v[0:1], s[0:1], v54, s12, v[0:1]
	v_cmp_eq_u32_e64 s[0:1], 0, v51
	s_mov_b32 s3, 0xf800000
	s_movk_i32 s2, 0x680
	v_mov_b64_e32 v[44:45], s[6:7]
	v_mov_b32_e32 v57, 0x260
	s_waitcnt vmcnt(8)
	v_pk_add_f32 v[46:47], v[8:9], v[4:5]
	v_pk_add_f32 v[48:49], v[10:11], v[6:7]
	global_load_dwordx4 v[4:7], v2, s[8:9] offset:2048
	global_load_dwordx4 v[8:11], v2, s[10:11] offset:2048
	s_waitcnt vmcnt(8)
	v_pk_add_f32 v[12:13], v[12:13], v[16:17]
	s_waitcnt vmcnt(6)
	v_pk_add_f32 v[16:17], v[20:21], v[24:25]
	v_pk_add_f32 v[14:15], v[14:15], v[18:19]
	v_pk_add_f32 v[18:19], v[22:23], v[26:27]
	v_add_f32_e32 v52, v46, v47
	v_mov_b32_e32 v20, v12
	v_mov_b32_e32 v21, v16
	v_mov_b32_e32 v22, v13
	v_mov_b32_e32 v23, v17
	v_mov_b32_e32 v24, v14
	v_mov_b32_e32 v25, v18
	v_add_f32_e32 v52, v52, v48
	v_pk_add_f32 v[20:21], v[20:21], v[22:23]
	v_mov_b32_e32 v26, v15
	v_mov_b32_e32 v27, v19
	v_add_f32_e32 v22, v52, v49
	v_pk_add_f32 v[20:21], v[20:21], v[24:25]
	v_add_f32_e32 v22, 0, v22
	v_pk_add_f32 v[20:21], v[20:21], v[26:27]
	s_nop 0
	v_add_f32_e32 v20, v22, v20
	v_add_f32_e32 v20, v20, v21
	s_nop 1
	v_add_f32_dpp v20, v20, v20 quad_perm:[1,0,3,2] row_mask:0xf bank_mask:0xf bound_ctrl:1
	s_nop 1
	v_add_f32_dpp v20, v20, v20 quad_perm:[2,3,0,1] row_mask:0xf bank_mask:0xf bound_ctrl:1
	s_nop 1
	v_add_f32_dpp v20, v20, v20 row_half_mirror row_mask:0xf bank_mask:0xf bound_ctrl:1
	s_nop 1
	v_add_f32_dpp v20, v20, v20 row_mirror row_mask:0xf bank_mask:0xf bound_ctrl:1
	v_mov_b32_e32 v21, v20
	v_mov_b32_e32 v22, v20
	s_nop 1
	v_permlane16_swap_b32_e32 v21, v22
	v_cndmask_b32_e32 v21, v21, v22, vcc
	v_add_f32_e32 v20, v20, v21
	v_mov_b32_e32 v21, v20
	v_mov_b32_e32 v22, v20
	s_nop 1
	v_permlane32_swap_b32_e32 v21, v22
	v_cndmask_b32_e64 v21, v21, v22, s[0:1]
	v_add_f32_e32 v20, v20, v21
	v_mul_f32_e32 v20, 0x3aaaaaab, v20
	v_pk_add_f32 v[22:23], v[46:47], v[20:21] op_sel_hi:[1,0] neg_lo:[0,1] neg_hi:[0,1]
	v_pk_add_f32 v[16:17], v[16:17], v[20:21] op_sel_hi:[1,0] neg_lo:[0,1] neg_hi:[0,1]
	v_pk_add_f32 v[24:25], v[48:49], v[20:21] op_sel_hi:[1,0] neg_lo:[0,1] neg_hi:[0,1]
	v_pk_add_f32 v[12:13], v[12:13], v[20:21] op_sel_hi:[1,0] neg_lo:[0,1] neg_hi:[0,1]
	v_mov_b32_e32 v48, v17
	v_mov_b32_e32 v49, v23
	v_pk_add_f32 v[14:15], v[14:15], v[20:21] op_sel_hi:[1,0] neg_lo:[0,1] neg_hi:[0,1]
	v_pk_add_f32 v[18:19], v[18:19], v[20:21] op_sel_hi:[1,0] neg_lo:[0,1] neg_hi:[0,1]
	v_pk_mul_f32 v[20:21], v[12:13], v[12:13]
	v_mov_b32_e32 v46, v16
	v_mov_b32_e32 v47, v22
	v_pk_mul_f32 v[48:49], v[48:49], v[48:49]
	v_pk_mul_f32 v[26:27], v[14:15], v[14:15]
	v_mov_b32_e32 v50, v18
	v_mov_b32_e32 v51, v24
	v_add_f32_e32 v58, v20, v21
	v_pk_fma_f32 v[20:21], v[46:47], v[46:47], v[48:49]
	v_mov_b32_e32 v52, v19
	v_mov_b32_e32 v53, v25
	v_add_f32_e32 v26, v26, v58
	v_pk_fma_f32 v[20:21], v[50:51], v[50:51], v[20:21]
	v_add_f32_e32 v26, v27, v26
	v_pk_fma_f32 v[20:21], v[52:53], v[52:53], v[20:21]
	s_nop 0
	v_add_f32_e32 v21, v21, v26
	v_add_f32_e32 v20, v20, v21
	s_nop 1
	v_add_f32_dpp v20, v20, v20 quad_perm:[1,0,3,2] row_mask:0xf bank_mask:0xf bound_ctrl:1
	s_nop 1
	v_add_f32_dpp v20, v20, v20 quad_perm:[2,3,0,1] row_mask:0xf bank_mask:0xf bound_ctrl:1
	s_nop 1
	v_add_f32_dpp v20, v20, v20 row_half_mirror row_mask:0xf bank_mask:0xf bound_ctrl:1
	s_nop 1
	v_add_f32_dpp v20, v20, v20 row_mirror row_mask:0xf bank_mask:0xf bound_ctrl:1
	v_mov_b32_e32 v21, v20
	v_mov_b32_e32 v26, v20
	s_nop 1
	v_permlane16_swap_b32_e32 v21, v26
	v_cndmask_b32_e32 v21, v21, v26, vcc
	v_add_f32_e32 v20, v20, v21
	v_mov_b32_e32 v21, v20
	v_mov_b32_e32 v26, v20
	s_nop 1
	v_permlane32_swap_b32_e32 v21, v26
	v_cndmask_b32_e64 v21, v21, v26, s[0:1]
	v_add_f32_e32 v20, v20, v21
	v_fmac_f32_e32 v56, 0x3aaaaaab, v20
	v_mul_f32_e32 v20, 0x4f800000, v56
	v_cmp_gt_f32_e32 vcc, s3, v56
	v_lshl_add_u64 v[26:27], v[0:1], 0, v[2:3]
	s_nop 0
	v_cndmask_b32_e32 v46, v56, v20, vcc
	v_sqrt_f32_e32 v47, v46
	v_mad_i64_i32 v[20:21], s[0:1], v54, s2, v[44:45]
	v_add_u32_e32 v0, -1, v47
	v_add_u32_e32 v1, 1, v47
	v_fma_f32 v2, -v0, v47, v46
	v_fma_f32 v44, -v1, v47, v46
	v_cmp_ge_f32_e64 s[0:1], 0, v2
	v_lshlrev_b32_e32 v2, 3, v55
	v_lshl_add_u64 v[20:21], v[20:21], 0, v[2:3]
	v_cndmask_b32_e64 v0, v47, v0, s[0:1]
	v_cmp_lt_f32_e64 s[0:1], 0, v44
	s_nop 1
	v_cndmask_b32_e64 v0, v0, v1, s[0:1]
	v_mul_f32_e32 v1, 0x37800000, v0
	v_cndmask_b32_e32 v0, v0, v1, vcc
	v_cmp_class_f32_e32 vcc, v46, v57
	s_nop 1
	v_cndmask_b32_e32 v0, v0, v46, vcc
	v_div_scale_f32 v1, s[0:1], v0, v0, 1.0
	v_rcp_f32_e32 v44, v1
	s_nop 0
	v_fma_f32 v2, -v1, v44, 1.0
	v_fmac_f32_e32 v44, v2, v44
	v_div_scale_f32 v2, vcc, 1.0, v0, 1.0
	v_mul_f32_e32 v3, v2, v44
	v_fma_f32 v45, -v1, v3, v2
	v_fmac_f32_e32 v3, v45, v44
	v_fma_f32 v1, -v1, v3, v2
	v_div_fmas_f32 v1, v1, v44, v3
	v_div_fixup_f32 v44, v1, v0, 1.0
	v_pk_mul_f32 v[0:1], v[22:23], v[44:45] op_sel_hi:[1,0]
	v_pk_mul_f32 v[2:3], v[24:25], v[44:45] op_sel_hi:[1,0]
	v_pk_mul_f32 v[12:13], v[12:13], v[44:45] op_sel_hi:[1,0]
	v_pk_mul_f32 v[14:15], v[14:15], v[44:45] op_sel_hi:[1,0]
	v_pk_mul_f32 v[16:17], v[16:17], v[44:45] op_sel_hi:[1,0]
	s_waitcnt vmcnt(4)
	v_pk_fma_f32 v[0:1], v[28:29], v[0:1], v[32:33]
	v_pk_fma_f32 v[2:3], v[30:31], v[2:3], v[34:35]
	s_waitcnt vmcnt(2)
	v_pk_fma_f32 v[12:13], v[12:13], v[36:37], v[40:41]
	v_pk_fma_f32 v[14:15], v[14:15], v[38:39], v[42:43]
	s_waitcnt vmcnt(0)
	v_pk_fma_f32 v[4:5], v[16:17], v[4:5], v[8:9]
	v_pk_mul_f32 v[8:9], v[18:19], v[44:45] op_sel_hi:[1,0]
	global_store_dwordx4 v[26:27], v[0:3], off sc1
	v_pk_fma_f32 v[6:7], v[8:9], v[6:7], v[10:11]
	s_nop 0
	v_cvt_pk_f16_f32 v3, v2, v3
	v_cvt_pk_f16_f32 v2, v0, v1
	v_cvt_pk_f16_f32 v1, v14, v15
	v_cvt_pk_f16_f32 v0, v12, v13
	global_store_dwordx2 v[20:21], v[2:3], off sc1
	global_store_dwordx4 v[26:27], v[12:15], off offset:1024 sc1
	global_store_dwordx2 v[20:21], v[0:1], off offset:512 sc1
	global_store_dwordx4 v[26:27], v[4:7], off offset:2048 sc1
	v_cvt_pk_f16_f32 v1, v6, v7
	v_cvt_pk_f16_f32 v0, v4, v5
	global_store_dwordx2 v[20:21], v[0:1], off offset:1024 sc1
	s_endpgm

	.amdhsa_kernel _Z4ln_kPKfS0_S0_S0_PfPDF16_
		.amdhsa_group_segment_fixed_size 0
		.amdhsa_private_segment_fixed_size 0
		.amdhsa_kernarg_size 48
		.amdhsa_user_sgpr_count 2
		.amdhsa_user_sgpr_dispatch_ptr 0
		.amdhsa_user_sgpr_queue_ptr 0
		.amdhsa_user_sgpr_kernarg_segment_ptr 1
		.amdhsa_user_sgpr_dispatch_id 0
		.amdhsa_user_sgpr_kernarg_preload_length 0
		.amdhsa_user_sgpr_kernarg_preload_offset 0
		.amdhsa_user_sgpr_private_segment_size 0
		.amdhsa_uses_dynamic_stack 0
		.amdhsa_enable_private_segment 0
		.amdhsa_system_sgpr_workgroup_id_x 1
		.amdhsa_system_sgpr_workgroup_id_y 0
		.amdhsa_system_sgpr_workgroup_id_z 0
		.amdhsa_system_sgpr_workgroup_info 0
		.amdhsa_system_vgpr_workitem_id 0
		.amdhsa_next_free_vgpr 61
		.amdhsa_next_free_sgpr 16
		.amdhsa_accum_offset 64
		.amdhsa_reserve_vcc 1
		.amdhsa_float_round_mode_32 0
		.amdhsa_float_round_mode_16_64 0
		.amdhsa_float_denorm_mode_32 3
		.amdhsa_float_denorm_mode_16_64 3
		.amdhsa_dx10_clamp 1
		.amdhsa_ieee_mode 1
		.amdhsa_fp16_overflow 0
		.amdhsa_tg_split 0
		.amdhsa_exception_fp_ieee_invalid_op 0
		.amdhsa_exception_fp_denorm_src 0
		.amdhsa_exception_fp_ieee_div_zero 0
		.amdhsa_exception_fp_ieee_overflow 0
		.amdhsa_exception_fp_ieee_underflow 0
		.amdhsa_exception_fp_ieee_inexact 0
		.amdhsa_exception_int_div_zero 0
	.end_amdhsa_kernel

_Z11ln_router_kPKfS0_S0_S0_S0_PfPDF16_PiS1_i:
	v_lshlrev_b32_e32 v56, 4, v0
	s_getpc_b64 s[28:29]
	s_add_u32 s28, s28, 0xef8
	s_addc_u32 s29, s29, 0x0
	global_load_dword v57, v56, s[28:29]
	s_getpc_b64 s[28:29]
	s_add_u32 s28, s28, 0x35e0
	s_addc_u32 s29, s29, 0x0
	global_load_dword v57, v56, s[28:29]
	s_load_dwordx8 s[16:23], s[0:1], 0x0
	v_lshrrev_b32_e32 v1, 6, v0
	v_and_b32_e32 v16, 63, v0
	v_lshl_or_b32 v14, s2, 4, v1
	s_movk_i32 s4, 0xc00
	s_waitcnt lgkmcnt(0)
	v_mov_b64_e32 v[2:3], s[16:17]
	v_mad_i64_i32 v[2:3], s[2:3], v14, s4, v[2:3]
	v_mov_b32_e32 v19, 0
	v_lshlrev_b32_e32 v18, 4, v16
	v_lshl_add_u64 v[20:21], v[2:3], 0, v[18:19]
	global_load_dwordx4 v[10:13], v[20:21], off
	global_load_dwordx4 v[6:9], v[20:21], off offset:1024
	global_load_dwordx4 v[2:5], v[20:21], off offset:2048
	s_load_dwordx2 s[16:17], s[0:1], 0x40
	s_load_dwordx8 s[8:15], s[0:1], 0x20
	v_lshlrev_b32_e32 v18, 4, v0
	v_mad_i64_i32 v[20:21], s[2:3], v14, s4, 0
	v_lshlrev_b32_e32 v17, 1, v0
	v_lshl_add_u64 v[18:19], s[22:23], 0, v[18:19]
	v_ashrrev_i32_e32 v15, 31, v14
	v_or_b32_e32 v1, 0xfffffc00, v0
	v_and_b32_e32 v17, 0x7fc, v17
	v_lshl_add_u64 v[18:19], v[18:19], 0, 8
	v_lshlrev_b32_e32 v22, 2, v0
	s_mov_b64 s[2:3], 0
	s_movk_i32 s6, 0xc10
	s_mov_b64 s[4:5], 0x4000
	s_movk_i32 s7, 0x1ff

	.amdhsa_kernel _Z11ln_router_kPKfS0_S0_S0_S0_PfPDF16_PiS1_i
		.amdhsa_group_segment_fixed_size 24704
		.amdhsa_private_segment_fixed_size 0
		.amdhsa_kernarg_size 76
		.amdhsa_user_sgpr_count 2
		.amdhsa_user_sgpr_dispatch_ptr 0
		.amdhsa_user_sgpr_queue_ptr 0
		.amdhsa_user_sgpr_kernarg_segment_ptr 1
		.amdhsa_user_sgpr_dispatch_id 0
		.amdhsa_user_sgpr_kernarg_preload_length 0
		.amdhsa_user_sgpr_kernarg_preload_offset 0
		.amdhsa_user_sgpr_private_segment_size 0
		.amdhsa_uses_dynamic_stack 0
		.amdhsa_enable_private_segment 0
		.amdhsa_system_sgpr_workgroup_id_x 1
		.amdhsa_system_sgpr_workgroup_id_y 0
		.amdhsa_system_sgpr_workgroup_id_z 0
		.amdhsa_system_sgpr_workgroup_info 0
		.amdhsa_system_vgpr_workitem_id 0
		.amdhsa_next_free_vgpr 58
		.amdhsa_next_free_sgpr 30
		.amdhsa_accum_offset 60
		.amdhsa_reserve_vcc 1
		.amdhsa_float_round_mode_32 0
		.amdhsa_float_round_mode_16_64 0
		.amdhsa_float_denorm_mode_32 3
		.amdhsa_float_denorm_mode_16_64 3
		.amdhsa_dx10_clamp 1
		.amdhsa_ieee_mode 1
		.amdhsa_fp16_overflow 0
		.amdhsa_tg_split 0
		.amdhsa_exception_fp_ieee_invalid_op 0
		.amdhsa_exception_fp_denorm_src 0
		.amdhsa_exception_fp_ieee_div_zero 0
		.amdhsa_exception_fp_ieee_overflow 0
		.amdhsa_exception_fp_ieee_underflow 0
		.amdhsa_exception_fp_ieee_inexact 0
		.amdhsa_exception_int_div_zero 0
	.end_amdhsa_kernel

_Z6sort_kPKiPiS1_:
	v_lshlrev_b32_e32 v48, 4, v0
	s_getpc_b64 s[92:93]
	s_add_u32 s92, s92, 0xdef8
	s_addc_u32 s93, s93, 0x0
	global_load_dword v49, v48, s[92:93]
	s_load_dwordx4 s[4:7], s[0:1], 0x0
	s_load_dwordx2 s[8:9], s[0:1], 0x10
	v_lshrrev_b32_e32 v1, 6, v0
	v_and_b32_e32 v2, 63, v0
	v_lshl_or_b32 v3, v1, 8, v2
	v_lshlrev_b32_e32 v12, 2, v3
	s_waitcnt lgkmcnt(0)
	global_load_dword v4, v12, s[4:5]
	global_load_dword v5, v12, s[4:5] offset:256
	global_load_dword v6, v12, s[4:5] offset:512
	global_load_dword v7, v12, s[4:5] offset:768
	v_readfirstlane_b32 s2, v1
	v_mov_b32_e32 v8, 0
	v_lshl_or_b32 v9, v1, 5, v2
	v_lshlrev_b32_e32 v9, 2, v9
	v_lshlrev_b32_e32 v10, 5, v2
	v_mov_b32_e32 v32, 0
	v_mov_b32_e32 v33, 0
	v_mov_b32_e32 v34, 0
	v_mov_b32_e32 v35, 0
	s_waitcnt vmcnt(3)
	v_cmp_eq_u32_e64 s[10:11], 0, v4
	v_cmp_eq_u32_e64 s[12:13], 1, v4
	v_cmp_eq_u32_e64 s[14:15], 2, v4
	v_cmp_eq_u32_e64 s[16:17], 3, v4
	v_cmp_eq_u32_e64 s[18:19], 4, v4
	v_cmp_eq_u32_e64 s[20:21], 5, v4
	v_cmp_eq_u32_e64 s[22:23], 6, v4
	v_cmp_eq_u32_e64 s[24:25], 7, v4
	s_waitcnt vmcnt(2)
	v_cmp_eq_u32_e64 s[26:27], 0, v5
	v_cmp_eq_u32_e64 s[28:29], 1, v5
	v_cmp_eq_u32_e64 s[30:31], 2, v5
	v_cmp_eq_u32_e64 s[32:33], 3, v5
	v_cmp_eq_u32_e64 s[34:35], 4, v5
	v_cmp_eq_u32_e64 s[36:37], 5, v5
	v_cmp_eq_u32_e64 s[38:39], 6, v5
	v_cmp_eq_u32_e64 s[40:41], 7, v5
	s_waitcnt vmcnt(1)
	v_cmp_eq_u32_e64 s[42:43], 0, v6
	v_cmp_eq_u32_e64 s[44:45], 1, v6
	v_cmp_eq_u32_e64 s[46:47], 2, v6
	v_cmp_eq_u32_e64 s[48:49], 3, v6
	v_cmp_eq_u32_e64 s[50:51], 4, v6
	v_cmp_eq_u32_e64 s[52:53], 5, v6
	v_cmp_eq_u32_e64 s[54:55], 6, v6
	v_cmp_eq_u32_e64 s[56:57], 7, v6
	s_waitcnt vmcnt(0)
	v_cmp_eq_u32_e64 s[58:59], 0, v7
	v_cmp_eq_u32_e64 s[60:61], 1, v7
	v_cmp_eq_u32_e64 s[62:63], 2, v7
	v_cmp_eq_u32_e64 s[64:65], 3, v7
	v_cmp_eq_u32_e64 s[66:67], 4, v7
	v_cmp_eq_u32_e64 s[68:69], 5, v7
	v_cmp_eq_u32_e64 s[70:71], 6, v7
	v_cmp_eq_u32_e64 s[72:73], 7, v7
	s_bcnt1_i32_b64 s74, s[10:11]
	v_writelane_b32 v8, s74, 0
	s_bcnt1_i32_b64 s74, s[12:13]
	v_writelane_b32 v8, s74, 1
	s_bcnt1_i32_b64 s74, s[14:15]
	v_writelane_b32 v8, s74, 2
	s_bcnt1_i32_b64 s74, s[16:17]
	v_writelane_b32 v8, s74, 3
	s_bcnt1_i32_b64 s74, s[18:19]
	v_writelane_b32 v8, s74, 4
	s_bcnt1_i32_b64 s74, s[20:21]
	v_writelane_b32 v8, s74, 5
	s_bcnt1_i32_b64 s74, s[22:23]
	v_writelane_b32 v8, s74, 6
	s_bcnt1_i32_b64 s74, s[24:25]
	v_writelane_b32 v8, s74, 7
	s_bcnt1_i32_b64 s74, s[26:27]
	v_writelane_b32 v8, s74, 8
	s_bcnt1_i32_b64 s74, s[28:29]
	v_writelane_b32 v8, s74, 9
	s_bcnt1_i32_b64 s74, s[30:31]
	v_writelane_b32 v8, s74, 10
	s_bcnt1_i32_b64 s74, s[32:33]
	v_writelane_b32 v8, s74, 11
	s_bcnt1_i32_b64 s74, s[34:35]
	v_writelane_b32 v8, s74, 12
	s_bcnt1_i32_b64 s74, s[36:37]
	v_writelane_b32 v8, s74, 13
	s_bcnt1_i32_b64 s74, s[38:39]
	v_writelane_b32 v8, s74, 14
	s_bcnt1_i32_b64 s74, s[40:41]
	v_writelane_b32 v8, s74, 15
	s_bcnt1_i32_b64 s74, s[42:43]
	v_writelane_b32 v8, s74, 16
	s_bcnt1_i32_b64 s74, s[44:45]
	v_writelane_b32 v8, s74, 17
	s_bcnt1_i32_b64 s74, s[46:47]
	v_writelane_b32 v8, s74, 18
	s_bcnt1_i32_b64 s74, s[48:49]
	v_writelane_b32 v8, s74, 19
	s_bcnt1_i32_b64 s74, s[50:51]
	v_writelane_b32 v8, s74, 20
	s_bcnt1_i32_b64 s74, s[52:53]
	v_writelane_b32 v8, s74, 21
	s_bcnt1_i32_b64 s74, s[54:55]
	v_writelane_b32 v8, s74, 22
	s_bcnt1_i32_b64 s74, s[56:57]
	v_writelane_b32 v8, s74, 23
	s_bcnt1_i32_b64 s74, s[58:59]
	v_writelane_b32 v8, s74, 24
	s_bcnt1_i32_b64 s74, s[60:61]
	v_writelane_b32 v8, s74, 25
	s_bcnt1_i32_b64 s74, s[62:63]
	v_writelane_b32 v8, s74, 26
	s_bcnt1_i32_b64 s74, s[64:65]
	v_writelane_b32 v8, s74, 27
	s_bcnt1_i32_b64 s74, s[66:67]
	v_writelane_b32 v8, s74, 28
	s_bcnt1_i32_b64 s74, s[68:69]
	v_writelane_b32 v8, s74, 29
	s_bcnt1_i32_b64 s74, s[70:71]
	v_writelane_b32 v8, s74, 30
	s_bcnt1_i32_b64 s74, s[72:73]
	v_writelane_b32 v8, s74, 31
	s_mov_b32 exec_lo, -1
	s_mov_b32 exec_hi, 0
	ds_write_b32 v9, v8
	s_mov_b64 exec, -1
	s_waitcnt lgkmcnt(0)
	s_barrier
	ds_read_b128 v[16:19], v10
	ds_read_b128 v[20:23], v10 offset:16
	s_mov_b64 exec, s[10:11]
	v_mbcnt_lo_u32_b32 v32, s10, 0
	v_mbcnt_hi_u32_b32 v32, s11, v32
	s_mov_b64 exec, s[12:13]
	v_mbcnt_lo_u32_b32 v32, s12, 0
	v_mbcnt_hi_u32_b32 v32, s13, v32
	s_mov_b64 exec, s[14:15]
	v_mbcnt_lo_u32_b32 v32, s14, 0
	v_mbcnt_hi_u32_b32 v32, s15, v32
	s_mov_b64 exec, s[16:17]
	v_mbcnt_lo_u32_b32 v32, s16, 0
	v_mbcnt_hi_u32_b32 v32, s17, v32
	s_mov_b64 exec, s[18:19]
	v_mbcnt_lo_u32_b32 v32, s18, 0
	v_mbcnt_hi_u32_b32 v32, s19, v32
	s_mov_b64 exec, s[20:21]
	v_mbcnt_lo_u32_b32 v32, s20, 0
	v_mbcnt_hi_u32_b32 v32, s21, v32
	s_mov_b64 exec, s[22:23]
	v_mbcnt_lo_u32_b32 v32, s22, 0
	v_mbcnt_hi_u32_b32 v32, s23, v32
	s_mov_b64 exec, s[24:25]
	v_mbcnt_lo_u32_b32 v32, s24, 0
	v_mbcnt_hi_u32_b32 v32, s25, v32
	s_mov_b64 exec, s[26:27]
	v_mbcnt_lo_u32_b32 v33, s26, 0
	v_mbcnt_hi_u32_b32 v33, s27, v33
	s_mov_b64 exec, s[28:29]
	v_mbcnt_lo_u32_b32 v33, s28, 0
	v_mbcnt_hi_u32_b32 v33, s29, v33
	s_mov_b64 exec, s[30:31]
	v_mbcnt_lo_u32_b32 v33, s30, 0
	v_mbcnt_hi_u32_b32 v33, s31, v33
	s_mov_b64 exec, s[32:33]
	v_mbcnt_lo_u32_b32 v33, s32, 0
	v_mbcnt_hi_u32_b32 v33, s33, v33
	s_mov_b64 exec, s[34:35]
	v_mbcnt_lo_u32_b32 v33, s34, 0
	v_mbcnt_hi_u32_b32 v33, s35, v33
	s_mov_b64 exec, s[36:37]
	v_mbcnt_lo_u32_b32 v33, s36, 0
	v_mbcnt_hi_u32_b32 v33, s37, v33
	s_mov_b64 exec, s[38:39]
	v_mbcnt_lo_u32_b32 v33, s38, 0
	v_mbcnt_hi_u32_b32 v33, s39, v33
	s_mov_b64 exec, s[40:41]
	v_mbcnt_lo_u32_b32 v33, s40, 0
	v_mbcnt_hi_u32_b32 v33, s41, v33
	s_mov_b64 exec, s[42:43]
	v_mbcnt_lo_u32_b32 v34, s42, 0
	v_mbcnt_hi_u32_b32 v34, s43, v34
	s_mov_b64 exec, s[44:45]
	v_mbcnt_lo_u32_b32 v34, s44, 0
	v_mbcnt_hi_u32_b32 v34, s45, v34
	s_mov_b64 exec, s[46:47]
	v_mbcnt_lo_u32_b32 v34, s46, 0
	v_mbcnt_hi_u32_b32 v34, s47, v34
	s_mov_b64 exec, s[48:49]
	v_mbcnt_lo_u32_b32 v34, s48, 0
	v_mbcnt_hi_u32_b32 v34, s49, v34
	s_mov_b64 exec, s[50:51]
	v_mbcnt_lo_u32_b32 v34, s50, 0
	v_mbcnt_hi_u32_b32 v34, s51, v34
	s_mov_b64 exec, s[52:53]
	v_mbcnt_lo_u32_b32 v34, s52, 0
	v_mbcnt_hi_u32_b32 v34, s53, v34
	s_mov_b64 exec, s[54:55]
	v_mbcnt_lo_u32_b32 v34, s54, 0
	v_mbcnt_hi_u32_b32 v34, s55, v34
	s_mov_b64 exec, s[56:57]
	v_mbcnt_lo_u32_b32 v34, s56, 0
	v_mbcnt_hi_u32_b32 v34, s57, v34
	s_mov_b64 exec, s[58:59]
	v_mbcnt_lo_u32_b32 v35, s58, 0
	v_mbcnt_hi_u32_b32 v35, s59, v35
	s_mov_b64 exec, s[60:61]
	v_mbcnt_lo_u32_b32 v35, s60, 0
	v_mbcnt_hi_u32_b32 v35, s61, v35
	s_mov_b64 exec, s[62:63]
	v_mbcnt_lo_u32_b32 v35, s62, 0
	v_mbcnt_hi_u32_b32 v35, s63, v35
	s_mov_b64 exec, s[64:65]
	v_mbcnt_lo_u32_b32 v35, s64, 0
	v_mbcnt_hi_u32_b32 v35, s65, v35
	s_mov_b64 exec, s[66:67]
	v_mbcnt_lo_u32_b32 v35, s66, 0
	v_mbcnt_hi_u32_b32 v35, s67, v35
	s_mov_b64 exec, s[68:69]
	v_mbcnt_lo_u32_b32 v35, s68, 0
	v_mbcnt_hi_u32_b32 v35, s69, v35
	s_mov_b64 exec, s[70:71]
	v_mbcnt_lo_u32_b32 v35, s70, 0
	v_mbcnt_hi_u32_b32 v35, s71, v35
	s_mov_b64 exec, s[72:73]
	v_mbcnt_lo_u32_b32 v35, s72, 0
	v_mbcnt_hi_u32_b32 v35, s73, v35
	s_mov_b64 exec, -1
	s_waitcnt lgkmcnt(0)
	v_mov_b32_e32 v24, v16
	v_mov_b32_e32 v25, v17
	v_mov_b32_e32 v26, v18
	v_mov_b32_e32 v27, v19
	v_mov_b32_e32 v28, v20
	v_mov_b32_e32 v29, v21
	v_mov_b32_e32 v30, v22
	v_mov_b32_e32 v31, v23
	v_add_u32_dpp v16, v16, v16 row_shr:1 row_mask:0xf bank_mask:0xf
	v_add_u32_dpp v17, v17, v17 row_shr:1 row_mask:0xf bank_mask:0xf
	v_add_u32_dpp v18, v18, v18 row_shr:1 row_mask:0xf bank_mask:0xf
	v_add_u32_dpp v19, v19, v19 row_shr:1 row_mask:0xf bank_mask:0xf
	v_add_u32_dpp v20, v20, v20 row_shr:1 row_mask:0xf bank_mask:0xf
	v_add_u32_dpp v21, v21, v21 row_shr:1 row_mask:0xf bank_mask:0xf
	v_add_u32_dpp v22, v22, v22 row_shr:1 row_mask:0xf bank_mask:0xf
	v_add_u32_dpp v23, v23, v23 row_shr:1 row_mask:0xf bank_mask:0xf
	v_add_u32_dpp v16, v16, v16 row_shr:2 row_mask:0xf bank_mask:0xf
	v_add_u32_dpp v17, v17, v17 row_shr:2 row_mask:0xf bank_mask:0xf
	v_add_u32_dpp v18, v18, v18 row_shr:2 row_mask:0xf bank_mask:0xf
	v_add_u32_dpp v19, v19, v19 row_shr:2 row_mask:0xf bank_mask:0xf
	v_add_u32_dpp v20, v20, v20 row_shr:2 row_mask:0xf bank_mask:0xf
	v_add_u32_dpp v21, v21, v21 row_shr:2 row_mask:0xf bank_mask:0xf
	v_add_u32_dpp v22, v22, v22 row_shr:2 row_mask:0xf bank_mask:0xf
	v_add_u32_dpp v23, v23, v23 row_shr:2 row_mask:0xf bank_mask:0xf
	v_add_u32_dpp v16, v16, v16 row_shr:4 row_mask:0xf bank_mask:0xf
	v_add_u32_dpp v17, v17, v17 row_shr:4 row_mask:0xf bank_mask:0xf
	v_add_u32_dpp v18, v18, v18 row_shr:4 row_mask:0xf bank_mask:0xf
	v_add_u32_dpp v19, v19, v19 row_shr:4 row_mask:0xf bank_mask:0xf
	v_add_u32_dpp v20, v20, v20 row_shr:4 row_mask:0xf bank_mask:0xf
	v_add_u32_dpp v21, v21, v21 row_shr:4 row_mask:0xf bank_mask:0xf
	v_add_u32_dpp v22, v22, v22 row_shr:4 row_mask:0xf bank_mask:0xf
	v_add_u32_dpp v23, v23, v23 row_shr:4 row_mask:0xf bank_mask:0xf
	v_add_u32_dpp v16, v16, v16 row_shr:8 row_mask:0xf bank_mask:0xf
	v_add_u32_dpp v17, v17, v17 row_shr:8 row_mask:0xf bank_mask:0xf
	v_add_u32_dpp v18, v18, v18 row_shr:8 row_mask:0xf bank_mask:0xf
	v_add_u32_dpp v19, v19, v19 row_shr:8 row_mask:0xf bank_mask:0xf
	v_add_u32_dpp v20, v20, v20 row_shr:8 row_mask:0xf bank_mask:0xf
	v_add_u32_dpp v21, v21, v21 row_shr:8 row_mask:0xf bank_mask:0xf
	v_add_u32_dpp v22, v22, v22 row_shr:8 row_mask:0xf bank_mask:0xf
	v_add_u32_dpp v23, v23, v23 row_shr:8 row_mask:0xf bank_mask:0xf
	v_add_u32_dpp v16, v16, v16 row_bcast:15 row_mask:0xa bank_mask:0xf
	v_add_u32_dpp v17, v17, v17 row_bcast:15 row_mask:0xa bank_mask:0xf
	v_add_u32_dpp v18, v18, v18 row_bcast:15 row_mask:0xa bank_mask:0xf
	v_add_u32_dpp v19, v19, v19 row_bcast:15 row_mask:0xa bank_mask:0xf
	v_add_u32_dpp v20, v20, v20 row_bcast:15 row_mask:0xa bank_mask:0xf
	v_add_u32_dpp v21, v21, v21 row_bcast:15 row_mask:0xa bank_mask:0xf
	v_add_u32_dpp v22, v22, v22 row_bcast:15 row_mask:0xa bank_mask:0xf
	v_add_u32_dpp v23, v23, v23 row_bcast:15 row_mask:0xa bank_mask:0xf
	v_add_u32_dpp v16, v16, v16 row_bcast:31 row_mask:0xc bank_mask:0xf
	v_add_u32_dpp v17, v17, v17 row_bcast:31 row_mask:0xc bank_mask:0xf
	v_add_u32_dpp v18, v18, v18 row_bcast:31 row_mask:0xc bank_mask:0xf
	v_add_u32_dpp v19, v19, v19 row_bcast:31 row_mask:0xc bank_mask:0xf
	v_add_u32_dpp v20, v20, v20 row_bcast:31 row_mask:0xc bank_mask:0xf
	v_add_u32_dpp v21, v21, v21 row_bcast:31 row_mask:0xc bank_mask:0xf
	v_add_u32_dpp v22, v22, v22 row_bcast:31 row_mask:0xc bank_mask:0xf
	v_add_u32_dpp v23, v23, v23 row_bcast:31 row_mask:0xc bank_mask:0xf
	v_sub_u32_e32 v24, v16, v24
	v_sub_u32_e32 v25, v17, v25
	v_sub_u32_e32 v26, v18, v26
	v_sub_u32_e32 v27, v19, v27
	v_sub_u32_e32 v28, v20, v28
	v_sub_u32_e32 v29, v21, v29
	v_sub_u32_e32 v30, v22, v30
	v_sub_u32_e32 v31, v23, v31
	v_readlane_b32 s80, v16, 63
	v_readlane_b32 s81, v17, 63
	v_readlane_b32 s82, v18, 63
	v_readlane_b32 s83, v19, 63
	v_readlane_b32 s84, v20, 63
	v_readlane_b32 s85, v21, 63
	v_readlane_b32 s86, v22, 63
	v_readlane_b32 s87, v23, 63
	s_mov_b32 s88, 0
	s_add_i32 s89, s88, s80
	s_add_i32 s90, s89, s81
	s_add_i32 s91, s90, s82
	s_add_i32 s92, s91, s83
	s_add_i32 s93, s92, s84
	s_add_i32 s94, s93, s85
	s_add_i32 s95, s94, s86
	s_lshl_b32 s3, s2, 2
	s_add_i32 s75, s3, 0
	v_mov_b32_e32 v36, 0
	v_readlane_b32 s76, v24, s75
	v_readlane_b32 s77, v25, s75
	s_add_i32 s76, s76, s88
	s_mov_b64 exec, s[10:11]
	v_add_u32_e32 v36, s76, v32
	v_readlane_b32 s76, v26, s75
	s_add_i32 s77, s77, s89
	s_mov_b64 exec, s[12:13]
	v_add_u32_e32 v36, s77, v32
	v_readlane_b32 s77, v27, s75
	s_add_i32 s76, s76, s90
	s_mov_b64 exec, s[14:15]
	v_add_u32_e32 v36, s76, v32
	v_readlane_b32 s76, v28, s75
	s_add_i32 s77, s77, s91
	s_mov_b64 exec, s[16:17]
	v_add_u32_e32 v36, s77, v32
	v_readlane_b32 s77, v29, s75
	s_add_i32 s76, s76, s92
	s_mov_b64 exec, s[18:19]
	v_add_u32_e32 v36, s76, v32
	v_readlane_b32 s76, v30, s75
	s_add_i32 s77, s77, s93
	s_mov_b64 exec, s[20:21]
	v_add_u32_e32 v36, s77, v32
	v_readlane_b32 s77, v31, s75
	s_add_i32 s76, s76, s94
	s_mov_b64 exec, s[22:23]
	v_add_u32_e32 v36, s76, v32
	s_add_i32 s77, s77, s95
	s_mov_b64 exec, s[24:25]
	v_add_u32_e32 v36, s77, v32
	s_mov_b64 exec, -1
	s_add_i32 s75, s3, 1
	v_mov_b32_e32 v37, 0
	v_readlane_b32 s76, v24, s75
	v_readlane_b32 s77, v25, s75
	s_add_i32 s76, s76, s88
	s_mov_b64 exec, s[26:27]
	v_add_u32_e32 v37, s76, v33
	v_readlane_b32 s76, v26, s75
	s_add_i32 s77, s77, s89
	s_mov_b64 exec, s[28:29]
	v_add_u32_e32 v37, s77, v33
	v_readlane_b32 s77, v27, s75
	s_add_i32 s76, s76, s90
	s_mov_b64 exec, s[30:31]
	v_add_u32_e32 v37, s76, v33
	v_readlane_b32 s76, v28, s75
	s_add_i32 s77, s77, s91
	s_mov_b64 exec, s[32:33]
	v_add_u32_e32 v37, s77, v33
	v_readlane_b32 s77, v29, s75
	s_add_i32 s76, s76, s92
	s_mov_b64 exec, s[34:35]
	v_add_u32_e32 v37, s76, v33
	v_readlane_b32 s76, v30, s75
	s_add_i32 s77, s77, s93
	s_mov_b64 exec, s[36:37]
	v_add_u32_e32 v37, s77, v33
	v_readlane_b32 s77, v31, s75
	s_add_i32 s76, s76, s94
	s_mov_b64 exec, s[38:39]
	v_add_u32_e32 v37, s76, v33
	s_add_i32 s77, s77, s95
	s_mov_b64 exec, s[40:41]
	v_add_u32_e32 v37, s77, v33
	s_mov_b64 exec, -1
	s_add_i32 s75, s3, 2
	v_mov_b32_e32 v38, 0
	v_readlane_b32 s76, v24, s75
	v_readlane_b32 s77, v25, s75
	s_add_i32 s76, s76, s88
	s_mov_b64 exec, s[42:43]
	v_add_u32_e32 v38, s76, v34
	v_readlane_b32 s76, v26, s75
	s_add_i32 s77, s77, s89
	s_mov_b64 exec, s[44:45]
	v_add_u32_e32 v38, s77, v34
	v_readlane_b32 s77, v27, s75
	s_add_i32 s76, s76, s90
	s_mov_b64 exec, s[46:47]
	v_add_u32_e32 v38, s76, v34
	v_readlane_b32 s76, v28, s75
	s_add_i32 s77, s77, s91
	s_mov_b64 exec, s[48:49]
	v_add_u32_e32 v38, s77, v34
	v_readlane_b32 s77, v29, s75
	s_add_i32 s76, s76, s92
	s_mov_b64 exec, s[50:51]
	v_add_u32_e32 v38, s76, v34
	v_readlane_b32 s76, v30, s75
	s_add_i32 s77, s77, s93
	s_mov_b64 exec, s[52:53]
	v_add_u32_e32 v38, s77, v34
	v_readlane_b32 s77, v31, s75
	s_add_i32 s76, s76, s94
	s_mov_b64 exec, s[54:55]
	v_add_u32_e32 v38, s76, v34
	s_add_i32 s77, s77, s95
	s_mov_b64 exec, s[56:57]
	v_add_u32_e32 v38, s77, v34
	s_mov_b64 exec, -1
	s_add_i32 s75, s3, 3
	v_mov_b32_e32 v39, 0
	v_readlane_b32 s76, v24, s75
	v_readlane_b32 s77, v25, s75
	s_add_i32 s76, s76, s88
	s_mov_b64 exec, s[58:59]
	v_add_u32_e32 v39, s76, v35
	v_readlane_b32 s76, v26, s75
	s_add_i32 s77, s77, s89
	s_mov_b64 exec, s[60:61]
	v_add_u32_e32 v39, s77, v35
	v_readlane_b32 s77, v27, s75
	s_add_i32 s76, s76, s90
	s_mov_b64 exec, s[62:63]
	v_add_u32_e32 v39, s76, v35
	v_readlane_b32 s76, v28, s75
	s_add_i32 s77, s77, s91
	s_mov_b64 exec, s[64:65]
	v_add_u32_e32 v39, s77, v35
	v_readlane_b32 s77, v29, s75
	s_add_i32 s76, s76, s92
	s_mov_b64 exec, s[66:67]
	v_add_u32_e32 v39, s76, v35
	v_readlane_b32 s76, v30, s75
	s_add_i32 s77, s77, s93
	s_mov_b64 exec, s[68:69]
	v_add_u32_e32 v39, s77, v35
	v_readlane_b32 s77, v31, s75
	s_add_i32 s76, s76, s94
	s_mov_b64 exec, s[70:71]
	v_add_u32_e32 v39, s76, v35
	s_add_i32 s77, s77, s95
	s_mov_b64 exec, s[72:73]
	v_add_u32_e32 v39, s77, v35
	s_mov_b64 exec, -1
	v_lshlrev_b32_e32 v13, 2, v36
	global_store_dword v13, v3, s[6:7]
	v_lshlrev_b32_e32 v13, 2, v37
	v_add_u32_e32 v14, 64, v3
	global_store_dword v13, v14, s[6:7]
	v_lshlrev_b32_e32 v13, 2, v38
	v_add_u32_e32 v14, 128, v3
	global_store_dword v13, v14, s[6:7]
	v_lshlrev_b32_e32 v13, 2, v39
	v_add_u32_e32 v14, 192, v3
	global_store_dword v13, v14, s[6:7]
	s_cmp_lg_u32 s2, 0
	s_cbranch_scc1 .Lsort_end
	v_mov_b32_e32 v40, -1
	v_mov_b32_e32 v41, 0
	v_mov_b32_e32 v42, 0
	v_mov_b32_e32 v43, 0
	s_mov_b32 s75, 0
	s_add_i32 s76, s80, 0x7f
	s_lshr_b32 s76, s76, 7
	s_add_i32 s77, s75, s76
	s_add_i32 s78, s88, s80
	v_cmp_le_u32_e64 s[10:11], s75, v2
	v_cmp_gt_u32_e64 s[12:13], s77, v2
	v_subrev_u32_e32 v44, s75, v2
	v_lshl_add_u32 v44, v44, 7, s88
	v_add_u32_e32 v45, 0x80, v44
	v_min_i32_e32 v45, s78, v45
	s_and_b64 s[14:15], s[10:11], s[12:13]
	s_mov_b32 s75, s77
	v_cndmask_b32_e64 v40, v40, 0, s[14:15]
	v_cndmask_b32_e64 v41, v41, v44, s[14:15]
	v_cndmask_b32_e64 v42, v42, v45, s[14:15]
	s_add_i32 s76, s81, 0x7f
	s_lshr_b32 s76, s76, 7
	s_add_i32 s77, s75, s76
	s_add_i32 s78, s89, s81
	v_cmp_le_u32_e64 s[10:11], s75, v2
	v_cmp_gt_u32_e64 s[12:13], s77, v2
	v_subrev_u32_e32 v44, s75, v2
	v_lshl_add_u32 v44, v44, 7, s89
	v_add_u32_e32 v45, 0x80, v44
	v_min_i32_e32 v45, s78, v45
	s_and_b64 s[14:15], s[10:11], s[12:13]
	s_mov_b32 s75, s77
	v_cndmask_b32_e64 v40, v40, 1, s[14:15]
	v_cndmask_b32_e64 v41, v41, v44, s[14:15]
	v_cndmask_b32_e64 v42, v42, v45, s[14:15]
	s_add_i32 s76, s82, 0x7f
	s_lshr_b32 s76, s76, 7
	s_add_i32 s77, s75, s76
	s_add_i32 s78, s90, s82
	v_cmp_le_u32_e64 s[10:11], s75, v2
	v_cmp_gt_u32_e64 s[12:13], s77, v2
	v_subrev_u32_e32 v44, s75, v2
	v_lshl_add_u32 v44, v44, 7, s90
	v_add_u32_e32 v45, 0x80, v44
	v_min_i32_e32 v45, s78, v45
	s_and_b64 s[14:15], s[10:11], s[12:13]
	s_mov_b32 s75, s77
	v_cndmask_b32_e64 v40, v40, 2, s[14:15]
	v_cndmask_b32_e64 v41, v41, v44, s[14:15]
	v_cndmask_b32_e64 v42, v42, v45, s[14:15]
	s_add_i32 s76, s83, 0x7f
	s_lshr_b32 s76, s76, 7
	s_add_i32 s77, s75, s76
	s_add_i32 s78, s91, s83
	v_cmp_le_u32_e64 s[10:11], s75, v2
	v_cmp_gt_u32_e64 s[12:13], s77, v2
	v_subrev_u32_e32 v44, s75, v2
	v_lshl_add_u32 v44, v44, 7, s91
	v_add_u32_e32 v45, 0x80, v44
	v_min_i32_e32 v45, s78, v45
	s_and_b64 s[14:15], s[10:11], s[12:13]
	s_mov_b32 s75, s77
	v_cndmask_b32_e64 v40, v40, 3, s[14:15]
	v_cndmask_b32_e64 v41, v41, v44, s[14:15]
	v_cndmask_b32_e64 v42, v42, v45, s[14:15]
	s_add_i32 s76, s84, 0x7f
	s_lshr_b32 s76, s76, 7
	s_add_i32 s77, s75, s76
	s_add_i32 s78, s92, s84
	v_cmp_le_u32_e64 s[10:11], s75, v2
	v_cmp_gt_u32_e64 s[12:13], s77, v2
	v_subrev_u32_e32 v44, s75, v2
	v_lshl_add_u32 v44, v44, 7, s92
	v_add_u32_e32 v45, 0x80, v44
	v_min_i32_e32 v45, s78, v45
	s_and_b64 s[14:15], s[10:11], s[12:13]
	s_mov_b32 s75, s77
	v_cndmask_b32_e64 v40, v40, 4, s[14:15]
	v_cndmask_b32_e64 v41, v41, v44, s[14:15]
	v_cndmask_b32_e64 v42, v42, v45, s[14:15]
	s_add_i32 s76, s85, 0x7f
	s_lshr_b32 s76, s76, 7
	s_add_i32 s77, s75, s76
	s_add_i32 s78, s93, s85
	v_cmp_le_u32_e64 s[10:11], s75, v2
	v_cmp_gt_u32_e64 s[12:13], s77, v2
	v_subrev_u32_e32 v44, s75, v2
	v_lshl_add_u32 v44, v44, 7, s93
	v_add_u32_e32 v45, 0x80, v44
	v_min_i32_e32 v45, s78, v45
	s_and_b64 s[14:15], s[10:11], s[12:13]
	s_mov_b32 s75, s77
	v_cndmask_b32_e64 v40, v40, 5, s[14:15]
	v_cndmask_b32_e64 v41, v41, v44, s[14:15]
	v_cndmask_b32_e64 v42, v42, v45, s[14:15]
	s_add_i32 s76, s86, 0x7f
	s_lshr_b32 s76, s76, 7
	s_add_i32 s77, s75, s76
	s_add_i32 s78, s94, s86
	v_cmp_le_u32_e64 s[10:11], s75, v2
	v_cmp_gt_u32_e64 s[12:13], s77, v2
	v_subrev_u32_e32 v44, s75, v2
	v_lshl_add_u32 v44, v44, 7, s94
	v_add_u32_e32 v45, 0x80, v44
	v_min_i32_e32 v45, s78, v45
	s_and_b64 s[14:15], s[10:11], s[12:13]
	s_mov_b32 s75, s77
	v_cndmask_b32_e64 v40, v40, 6, s[14:15]
	v_cndmask_b32_e64 v41, v41, v44, s[14:15]
	v_cndmask_b32_e64 v42, v42, v45, s[14:15]
	s_add_i32 s76, s87, 0x7f
	s_lshr_b32 s76, s76, 7
	s_add_i32 s77, s75, s76
	s_add_i32 s78, s95, s87
	v_cmp_le_u32_e64 s[10:11], s75, v2
	v_cmp_gt_u32_e64 s[12:13], s77, v2
	v_subrev_u32_e32 v44, s75, v2
	v_lshl_add_u32 v44, v44, 7, s95
	v_add_u32_e32 v45, 0x80, v44
	v_min_i32_e32 v45, s78, v45
	s_and_b64 s[14:15], s[10:11], s[12:13]
	s_mov_b32 s75, s77
	v_cndmask_b32_e64 v40, v40, 7, s[14:15]
	v_cndmask_b32_e64 v41, v41, v44, s[14:15]
	v_cndmask_b32_e64 v42, v42, v45, s[14:15]
	v_lshlrev_b32_e32 v46, 4, v2
	v_mov_b32_e32 v47, s75
	v_cmp_gt_u32_e32 vcc, 40, v2
	s_and_b64 exec, exec, vcc
	global_store_dwordx4 v46, v[40:43], s[8:9]
	v_cmp_eq_u32_e32 vcc, 0, v2
	s_and_b64 exec, exec, vcc
	global_store_dword v46, v47, s[8:9] offset:640

	.amdhsa_kernel _Z6sort_kPKiPiS1_
		.amdhsa_group_segment_fixed_size 4176
		.amdhsa_private_segment_fixed_size 0
		.amdhsa_kernarg_size 24
		.amdhsa_user_sgpr_count 2
		.amdhsa_user_sgpr_dispatch_ptr 0
		.amdhsa_user_sgpr_queue_ptr 0
		.amdhsa_user_sgpr_kernarg_segment_ptr 1
		.amdhsa_user_sgpr_dispatch_id 0
		.amdhsa_user_sgpr_kernarg_preload_length 0
		.amdhsa_user_sgpr_kernarg_preload_offset 0
		.amdhsa_user_sgpr_private_segment_size 0
		.amdhsa_uses_dynamic_stack 0
		.amdhsa_enable_private_segment 0
		.amdhsa_system_sgpr_workgroup_id_x 1
		.amdhsa_system_sgpr_workgroup_id_y 0
		.amdhsa_system_sgpr_workgroup_id_z 0
		.amdhsa_system_sgpr_workgroup_info 0
		.amdhsa_system_vgpr_workitem_id 0
		.amdhsa_next_free_vgpr 50
		.amdhsa_next_free_sgpr 96
		.amdhsa_accum_offset 52
		.amdhsa_reserve_vcc 1
		.amdhsa_float_round_mode_32 0
		.amdhsa_float_round_mode_16_64 0
		.amdhsa_float_denorm_mode_32 3
		.amdhsa_float_denorm_mode_16_64 3
		.amdhsa_dx10_clamp 1
		.amdhsa_ieee_mode 1
		.amdhsa_fp16_overflow 0
		.amdhsa_tg_split 0
		.amdhsa_exception_fp_ieee_invalid_op 0
		.amdhsa_exception_fp_denorm_src 0
		.amdhsa_exception_fp_ieee_div_zero 0
		.amdhsa_exception_fp_ieee_overflow 0
		.amdhsa_exception_fp_ieee_underflow 0
		.amdhsa_exception_fp_ieee_inexact 0
		.amdhsa_exception_int_div_zero 0
	.end_amdhsa_kernel

_Z5pre_k7CvtArgsPKiS1_PKfS3_S3_S3_S3_PfPDF16_S4_:
	v_lshlrev_b32_e32 v67, 4, v0
	s_getpc_b64 s[16:17]
	s_add_u32 s16, s16, 0x7ff8
	s_addc_u32 s17, s17, 0x0
	global_load_dword v68, v67, s[16:17]
	v_add_u32_e32 v67, 0x1000, v67
	global_load_dword v68, v67, s[16:17]
	v_add_u32_e32 v67, 0x1000, v67
	global_load_dword v68, v67, s[16:17]
	v_add_u32_e32 v67, 0x1000, v67
	global_load_dword v68, v67, s[16:17]
	v_lshlrev_b32_e32 v67, 4, v0
	s_cmpk_gt_u32 s2, 0x3ff
	s_mov_b64 s[4:5], -1
	s_cbranch_scc0 .LBB4_8
	s_add_i32 s10, s2, 0xfffffc00
	s_cmpk_gt_i32 s10, 0x47f
	s_cbranch_scc0 .LBB4_5
	s_cmpk_gt_u32 s10, 0x6bf
	s_cbranch_scc0 .LBB4_12
	s_add_i32 s3, s2, 0xfffff540
	s_mul_hi_u32 s4, s3, 0x38e38e39
	s_lshr_b32 s4, s4, 7
	s_add_i32 s8, s4, 9
	s_mulk_i32 s4, 0x240
	s_sub_i32 s9, s3, s4
	s_cbranch_execz .LBB4_13

	.amdhsa_kernel _Z5pre_k7CvtArgsPKiS1_PKfS3_S3_S3_S3_PfPDF16_S4_
		.amdhsa_group_segment_fixed_size 16640
		.amdhsa_private_segment_fixed_size 0
		.amdhsa_kernarg_size 352
		.amdhsa_user_sgpr_count 2
		.amdhsa_user_sgpr_dispatch_ptr 0
		.amdhsa_user_sgpr_queue_ptr 0
		.amdhsa_user_sgpr_kernarg_segment_ptr 1
		.amdhsa_user_sgpr_dispatch_id 0
		.amdhsa_user_sgpr_kernarg_preload_length 0
		.amdhsa_user_sgpr_kernarg_preload_offset 0
		.amdhsa_user_sgpr_private_segment_size 0
		.amdhsa_uses_dynamic_stack 0
		.amdhsa_enable_private_segment 0
		.amdhsa_system_sgpr_workgroup_id_x 1
		.amdhsa_system_sgpr_workgroup_id_y 0
		.amdhsa_system_sgpr_workgroup_id_z 0
		.amdhsa_system_sgpr_workgroup_info 0
		.amdhsa_system_vgpr_workitem_id 0
		.amdhsa_next_free_vgpr 69
		.amdhsa_next_free_sgpr 18
		.amdhsa_accum_offset 72
		.amdhsa_reserve_vcc 1
		.amdhsa_float_round_mode_32 0
		.amdhsa_float_round_mode_16_64 0
		.amdhsa_float_denorm_mode_32 3
		.amdhsa_float_denorm_mode_16_64 3
		.amdhsa_dx10_clamp 1
		.amdhsa_ieee_mode 1
		.amdhsa_fp16_overflow 0
		.amdhsa_tg_split 0
		.amdhsa_exception_fp_ieee_invalid_op 0
		.amdhsa_exception_fp_denorm_src 0
		.amdhsa_exception_fp_ieee_div_zero 0
		.amdhsa_exception_fp_ieee_overflow 0
		.amdhsa_exception_fp_ieee_underflow 0
		.amdhsa_exception_fp_ieee_inexact 0
		.amdhsa_exception_int_div_zero 0
	.end_amdhsa_kernel

_Z6attn_kPKDF16_S0_S0_PKfPDF16_PK15HIP_vector_typeIfLj4EEiPf:
	v_lshlrev_b32_e32 v110, 4, v0
	s_getpc_b64 s[92:93]
	s_add_u32 s92, s92, 0xacf8
	s_addc_u32 s93, s93, 0x0
	global_load_dword v111, v110, s[92:93]
	s_cmpk_lt_u32 s2, 0xc0
	s_mov_b64 s[4:5], -1
	s_cbranch_scc0 .LBB5_6
	s_load_dwordx8 s[4:11], s[0:1], 0x0
	s_and_b32 s3, s2, 7
	s_mul_i32 s3, s3, 12
	s_lshr_b32 s12, s2, 4
	s_add_i32 s3, s3, s12
	s_mul_i32 s12, s3, 0xab
	s_bfe_u32 s12, s12, 0x5000b
	s_lshl_b32 s13, s3, 16
	s_waitcnt lgkmcnt(0)
	s_add_u32 s6, s6, s13
	s_addc_u32 s7, s7, 0
	v_lshlrev_b32_e32 v2, 4, v0
	v_mov_b32_e32 v3, 0
	v_lshl_add_u64 v[28:29], s[6:7], 0, v[2:3]
	s_movk_i32 s14, 0x2000
	v_add_co_u32_e32 v12, vcc, s14, v28
	s_movk_i32 s15, 0x6000
	s_nop 0
	v_addc_co_u32_e32 v13, vcc, 0, v29, vcc
	v_add_co_u32_e32 v20, vcc, s15, v28
	s_mov_b32 s16, 0xa000
	s_nop 0
	v_addc_co_u32_e32 v21, vcc, 0, v29, vcc
	v_add_co_u32_e32 v30, vcc, s16, v28
	s_add_u32 s8, s8, s13
	s_nop 0
	v_addc_co_u32_e32 v31, vcc, 0, v29, vcc
	s_mov_b32 s17, 0xe000
	s_addc_u32 s9, s9, 0
	v_add_co_u32_e32 v28, vcc, s17, v28
	v_lshl_add_u64 v[48:49], s[8:9], 0, v[2:3]
	s_nop 0
	v_addc_co_u32_e32 v29, vcc, 0, v29, vcc
	v_add_co_u32_e32 v50, vcc, s14, v48
	v_or_b32_e32 v1, 0x4000, v2
	s_nop 0
	v_addc_co_u32_e32 v51, vcc, 0, v49, vcc
	global_load_dwordx4 v[4:7], v[12:13], off
	global_load_dwordx4 v[8:11], v1, s[6:7]
	v_or_b32_e32 v54, 0x8000, v2
	global_load_dwordx4 v[12:15], v[20:21], off
	global_load_dwordx4 v[16:19], v54, s[6:7]
	v_or_b32_e32 v55, 0xc000, v2
	global_load_dwordx4 v[20:23], v[30:31], off
	global_load_dwordx4 v[24:27], v55, s[6:7]
	v_add_co_u32_e32 v52, vcc, s15, v48
	global_load_dwordx4 v[28:31], v[28:29], off
	s_nop 0
	global_load_dwordx4 v[32:35], v2, s[6:7]
	global_load_dwordx4 v[36:39], v2, s[8:9]
	v_addc_co_u32_e32 v53, vcc, 0, v49, vcc
	global_load_dwordx4 v[40:43], v1, s[8:9]
	global_load_dwordx4 v[44:47], v[50:51], off
	global_load_dwordx4 v[66:69], v[52:53], off
	global_load_dwordx4 v[70:73], v54, s[8:9]
	v_add_co_u32_e32 v50, vcc, s16, v48
	s_add_u32 s4, s4, s13
	s_nop 0
	v_addc_co_u32_e32 v51, vcc, 0, v49, vcc
	s_addc_u32 s5, s5, 0
	global_load_dwordx4 v[74:77], v[50:51], off
	global_load_dwordx4 v[78:81], v55, s[8:9]
	s_lshl_b32 s8, s12, 9
	v_add_co_u32_e32 v48, vcc, s17, v48
	v_or_b32_e32 v1, s8, v0
	s_nop 0
	v_addc_co_u32_e32 v49, vcc, 0, v49, vcc
	v_lshlrev_b32_e32 v1, 2, v1
	global_load_dwordx4 v[84:87], v[48:49], off
	v_and_b32_e32 v49, 63, v0
	global_load_dword v48, v1, s[10:11]
	v_lshrrev_b32_e32 v1, 6, v0
	v_and_or_b32 v1, s2, 8, v1
	v_lshlrev_b32_e32 v83, 4, v49
	v_lshl_or_b32 v49, v1, 12, v83
	global_load_dwordx4 v[50:53], v49, s[4:5]
	global_load_dwordx4 v[54:57], v49, s[4:5] offset:1024
	global_load_dwordx4 v[58:61], v49, s[4:5] offset:2048
	global_load_dwordx4 v[62:65], v49, s[4:5] offset:3072
	s_load_dwordx2 s[6:7], s[0:1], 0x20
	v_bfe_u32 v82, v0, 5, 1
	s_mov_b32 s9, 16
	s_mov_b32 s10, 0x41000000
	s_waitcnt vmcnt(13)
	ds_write_b128 v2, v[32:35]
	ds_write_b128 v2, v[4:7] offset:8192
	ds_write_b128 v2, v[8:11] offset:16384
	ds_write_b128 v2, v[12:15] offset:24576
	ds_write_b128 v2, v[16:19] offset:32768
	ds_write_b128 v2, v[20:23] offset:40960
	ds_write_b128 v2, v[24:27] offset:49152
	ds_write_b128 v2, v[28:31] offset:57344
	v_or_b32_e32 v4, 0x10000, v2
	s_waitcnt vmcnt(12)
	ds_write_b128 v4, v[36:39]
	v_or_b32_e32 v4, 0x12000, v2
	s_waitcnt vmcnt(10)
	ds_write_b128 v4, v[44:47]
	v_or_b32_e32 v4, 0x14000, v2
	ds_write_b128 v4, v[40:43]
	v_or_b32_e32 v4, 0x16000, v2
	s_waitcnt vmcnt(9)
	ds_write_b128 v4, v[66:69]
	v_or_b32_e32 v4, 0x18000, v2
	s_waitcnt vmcnt(8)
	ds_write_b128 v4, v[70:73]
	v_or_b32_e32 v4, 0x1a000, v2
	s_waitcnt vmcnt(7)
	ds_write_b128 v4, v[74:77]
	v_or_b32_e32 v4, 0x1c000, v2
	v_or_b32_e32 v2, 0x1e000, v2
	v_mov_b32_e32 v16, v3
	v_mov_b32_e32 v17, v3
	s_waitcnt vmcnt(6)
	ds_write_b128 v4, v[78:81]
	v_mov_b32_e32 v4, v3
	v_mov_b32_e32 v5, v3
	s_waitcnt vmcnt(5)
	ds_write_b128 v2, v[84:87]
	v_mov_b32_e32 v2, 0x20000
	v_lshl_or_b32 v2, v0, 2, v2
	s_waitcnt vmcnt(4)
	ds_write_b32 v2, v48
	v_and_b32_e32 v2, 32, v0
	v_cmp_eq_u32_e32 vcc, 0, v2
	v_mov_b32_e32 v2, v3
	v_mov_b32_e32 v6, v3
	v_mov_b32_e32 v7, v3
	v_mov_b32_e32 v8, v3
	v_mov_b32_e32 v9, v3
	v_mov_b32_e32 v10, v3
	v_mov_b32_e32 v11, v3
	v_mov_b32_e32 v12, v3
	v_mov_b32_e32 v13, v3
	v_mov_b32_e32 v14, v3
	v_mov_b32_e32 v15, v3
	v_mov_b64_e32 v[32:33], v[16:17]
	v_lshlrev_b32_e32 v84, 4, v82
	v_mov_b32_e32 v86, 0xf149f2ca
	v_mov_b64_e32 v[30:31], v[14:15]
	v_mov_b64_e32 v[28:29], v[12:13]
	v_mov_b64_e32 v[26:27], v[10:11]
	v_mov_b64_e32 v[24:25], v[8:9]
	v_mov_b64_e32 v[22:23], v[6:7]
	v_mov_b64_e32 v[20:21], v[4:5]
	v_mov_b64_e32 v[18:19], v[2:3]
	v_mov_b32_e32 v85, v3
	s_waitcnt lgkmcnt(0)
	s_barrier
	s_branch .LBB5_3

_Z9tail_up_kPKfPKiS0_S0_PfS0_S2_S3_PK15HIP_vector_typeIfLj4EEiS7_iS3_:
	v_lshlrev_b32_e32 v112, 4, v0
	s_getpc_b64 s[64:65]
	s_add_u32 s64, s64, 0xfff8
	s_addc_u32 s65, s65, 0x0
	global_load_dword v113, v112, s[64:65]
	s_load_dwordx2 s[6:7], s[0:1], 0x60
	s_load_dwordx2 s[8:9], s[0:1], 0x50
	s_load_dwordx2 s[14:15], s[0:1], 0x40
	s_load_dwordx8 s[44:51], s[0:1], 0x0
	s_load_dwordx8 s[36:43], s[0:1], 0x20
	s_mov_b64 s[12:13], -1
	s_mov_b64 s[4:5], 0
	s_cmp_lt_i32 s3, 9
	s_mov_b64 s[10:11], 0
	s_cbranch_scc0 .LBB6_5
	s_and_b64 vcc, exec, s[12:13]
	s_cbranch_vccnz .LBB6_30

	.amdhsa_kernel _Z9tail_up_kPKfPKiS0_S0_PfS0_S2_S3_PK15HIP_vector_typeIfLj4EEiS7_iS3_
		.amdhsa_group_segment_fixed_size 7168
		.amdhsa_private_segment_fixed_size 0
		.amdhsa_kernarg_size 104
		.amdhsa_user_sgpr_count 2
		.amdhsa_user_sgpr_dispatch_ptr 0
		.amdhsa_user_sgpr_queue_ptr 0
		.amdhsa_user_sgpr_kernarg_segment_ptr 1
		.amdhsa_user_sgpr_dispatch_id 0
		.amdhsa_user_sgpr_kernarg_preload_length 0
		.amdhsa_user_sgpr_kernarg_preload_offset 0
		.amdhsa_user_sgpr_private_segment_size 0
		.amdhsa_uses_dynamic_stack 0
		.amdhsa_enable_private_segment 0
		.amdhsa_system_sgpr_workgroup_id_x 1
		.amdhsa_system_sgpr_workgroup_id_y 1
		.amdhsa_system_sgpr_workgroup_id_z 0
		.amdhsa_system_sgpr_workgroup_info 0
		.amdhsa_system_vgpr_workitem_id 0
		.amdhsa_next_free_vgpr 114
		.amdhsa_next_free_sgpr 66
		.amdhsa_accum_offset 116
		.amdhsa_reserve_vcc 1
		.amdhsa_float_round_mode_32 0
		.amdhsa_float_round_mode_16_64 0
		.amdhsa_float_denorm_mode_32 3
		.amdhsa_float_denorm_mode_16_64 3
		.amdhsa_dx10_clamp 1
		.amdhsa_ieee_mode 1
		.amdhsa_fp16_overflow 0
		.amdhsa_tg_split 0
		.amdhsa_exception_fp_ieee_invalid_op 0
		.amdhsa_exception_fp_denorm_src 0
		.amdhsa_exception_fp_ieee_div_zero 0
		.amdhsa_exception_fp_ieee_overflow 0
		.amdhsa_exception_fp_ieee_underflow 0
		.amdhsa_exception_fp_ieee_inexact 0
		.amdhsa_exception_int_div_zero 0
	.end_amdhsa_kernel

_Z6pool_kPKfS0_S0_S0_S0_S0_PfS1_:
	v_lshlrev_b32_e32 v220, 4, v0
	s_getpc_b64 s[92:93]
	s_add_u32 s92, s92, 0x17f8
	s_addc_u32 s93, s93, 0x0
	global_load_dword v221, v220, s[92:93]
	s_load_dwordx2 s[12:13], s[0:1], 0x18
	s_load_dwordx2 s[8:9], s[0:1], 0x28
	s_load_dwordx2 s[10:11], s[0:1], 0x38
	s_movk_i32 s4, 0x300
	v_cmp_gt_u32_e32 vcc, s4, v0
	s_mul_i32 s20, s3, 0x60
	s_and_saveexec_b64 s[14:15], vcc
	s_cbranch_execz .LBB8_3
	s_load_dwordx4 s[4:7], s[0:1], 0x0
	s_load_dwordx2 s[16:17], s[0:1], 0x10
	s_mov_b64 s[18:19], 0
	s_mov_b32 s21, 0xaaab
	v_mov_b32_e32 v3, 0
	s_movk_i32 s22, 0x6000
	s_mov_b32 s23, 0xc000
	s_mov_b32 s24, 0x12000
	s_mov_b32 s25, 0x18000
	s_mov_b32 s26, 0x1e000
	s_mov_b32 s27, 0x24000
	s_mov_b32 s28, 0x2a000
	s_mov_b32 s29, 0x30000
	s_mov_b32 s30, 0x36000
	s_mov_b32 s31, 0x3c000
	s_mov_b32 s33, 0x42000
	s_mov_b32 s34, 0x48000
	s_mov_b32 s35, 0x4e000
	s_mov_b32 s36, 0x54000
	s_mov_b32 s37, 0x5a000
	s_movk_i32 s38, 0x180
	s_movk_i32 s39, 0x1ff
	v_mov_b32_e32 v1, v0

	.amdhsa_kernel _Z6pool_kPKfS0_S0_S0_S0_S0_PfS1_
		.amdhsa_group_segment_fixed_size 47872
		.amdhsa_private_segment_fixed_size 0
		.amdhsa_kernarg_size 64
		.amdhsa_user_sgpr_count 2
		.amdhsa_user_sgpr_dispatch_ptr 0
		.amdhsa_user_sgpr_queue_ptr 0
		.amdhsa_user_sgpr_kernarg_segment_ptr 1
		.amdhsa_user_sgpr_dispatch_id 0
		.amdhsa_user_sgpr_kernarg_preload_length 0
		.amdhsa_user_sgpr_kernarg_preload_offset 0
		.amdhsa_user_sgpr_private_segment_size 0
		.amdhsa_uses_dynamic_stack 0
		.amdhsa_enable_private_segment 0
		.amdhsa_system_sgpr_workgroup_id_x 1
		.amdhsa_system_sgpr_workgroup_id_y 1
		.amdhsa_system_sgpr_workgroup_id_z 0
		.amdhsa_system_sgpr_workgroup_info 0
		.amdhsa_system_vgpr_workitem_id 0
		.amdhsa_next_free_vgpr 222
		.amdhsa_next_free_sgpr 96
		.amdhsa_accum_offset 224
		.amdhsa_reserve_vcc 1
		.amdhsa_float_round_mode_32 0
		.amdhsa_float_round_mode_16_64 0
		.amdhsa_float_denorm_mode_32 3
		.amdhsa_float_denorm_mode_16_64 3
		.amdhsa_dx10_clamp 1
		.amdhsa_ieee_mode 1
		.amdhsa_fp16_overflow 0
		.amdhsa_tg_split 0
		.amdhsa_exception_fp_ieee_invalid_op 0
		.amdhsa_exception_fp_denorm_src 0
		.amdhsa_exception_fp_ieee_div_zero 0
		.amdhsa_exception_fp_ieee_overflow 0
		.amdhsa_exception_fp_ieee_underflow 0
		.amdhsa_exception_fp_ieee_inexact 0
		.amdhsa_exception_int_div_zero 0
	.end_amdhsa_kernel

_Z7gemm2_kILi0ELi3ELi1EEv5GArgs:
	v_lshlrev_b32_e32 v186, 4, v0
	s_getpc_b64 s[92:93]
	s_add_u32 s92, s92, 0xffff89f8
	s_addc_u32 s93, s93, 0xffffffff
	global_load_dword v187, v186, s[92:93]
	s_load_dwordx8 s[8:15], s[0:1], 0x68
	s_cmpk_lt_u32 s2, 0xc0
	s_mov_b64 s[4:5], -1
	s_cbranch_scc0 .LBB11_26
	v_lshrrev_b32_e32 v149, 6, v0
	s_lshl_b32 s3, s2, 8
	v_bfe_u32 v1, v0, 3, 3
	s_load_dwordx4 s[4:7], s[0:1], 0x0
	s_load_dwordx4 s[16:19], s[0:1], 0x18
	s_and_b32 s20, s3, 0xf00
	v_lshl_or_b32 v6, v149, 5, v1
	v_or_b32_e32 v8, s20, v6
	v_mul_u32_u24_e32 v2, 0x340, v8
	v_bfe_u32 v4, v0, 4, 2
	v_lshlrev_b32_e32 v146, 1, v2
	v_mov_b32_e32 v147, 0
	v_bitop3_b32 v4, v4, v0, 7 bitop3:0x78
	s_waitcnt lgkmcnt(0)
	v_lshl_add_u64 v[2:3], s[4:5], 0, v[146:147]
	v_lshlrev_b32_e32 v146, 4, v4
	v_or_b32_e32 v4, 8, v6
	v_lshl_add_u64 v[98:99], v[2:3], 0, v[146:147]
	v_or_b32_e32 v2, s20, v4
	v_lshrrev_b32_e32 v4, 1, v4
	v_xor_b32_e32 v4, v4, v0
	v_mul_u32_u24_e32 v2, 0x340, v2
	v_mov_b32_e32 v3, v147
	v_lshlrev_b32_e32 v4, 4, v4
	v_lshl_add_u64 v[2:3], v[2:3], 1, s[4:5]
	v_and_b32_e32 v4, 0x70, v4
	v_mov_b32_e32 v5, v147
	v_lshl_add_u64 v[100:101], v[2:3], 0, v[4:5]
	v_or_b32_e32 v2, 16, v8
	v_mul_u32_u24_e32 v2, 0x340, v2
	v_mov_b32_e32 v3, v147
	v_lshl_add_u64 v[2:3], v[2:3], 1, s[4:5]
	v_xor_b32_e32 v146, 16, v146
	v_or_b32_e32 v4, 24, v6
	v_lshl_add_u64 v[102:103], v[2:3], 0, v[146:147]
	v_or_b32_e32 v2, s20, v4
	v_lshrrev_b32_e32 v4, 1, v4
	v_xor_b32_e32 v4, v4, v0
	v_lshlrev_b32_e32 v4, 3, v4
	v_mul_u32_u24_e32 v146, 0x340, v2
	v_bitop3_b32 v4, v4, 8, 56 bitop3:0x6c
	s_lshr_b32 s36, s2, 6
	s_bfe_u32 s21, s2, 0x20004
	v_lshl_add_u64 v[2:3], v[146:147], 1, s[4:5]
	v_lshlrev_b32_e32 v146, 1, v4
	v_lshl_add_u64 v[104:105], v[2:3], 0, v[146:147]
	s_mul_i32 s20, s21, 0xc0
	s_mul_i32 s4, s36, 0x300
	v_mul_u32_u24_e32 v2, 24, v149
	v_mul_u32_u24_e32 v4, 3, v149
	s_add_i32 s21, s20, s4
	v_or_b32_e32 v5, v2, v1
	v_add_u32_e32 v2, s21, v5
	v_bfe_u32 v5, v5, 1, 3
	v_lshrrev_b32_e32 v4, 1, v4
	v_and_b32_e32 v7, 7, v0
	s_movk_i32 s22, 0x680
	v_bitop3_b32 v4, v4, v5, 1 bitop3:0x6c
	v_mad_u32_u24 v6, v149, 3, 1
	v_mul_lo_u32 v146, v2, s22
	v_xor_b32_e32 v4, v4, v7
	v_lshl_or_b32 v8, v6, 3, v1
	v_lshl_add_u64 v[2:3], s[6:7], 0, v[146:147]
	v_lshlrev_b32_e32 v146, 4, v4
	v_add_u32_e32 v4, s21, v8
	v_bfe_u32 v8, v8, 1, 3
	v_lshrrev_b32_e32 v9, 1, v6
	v_bitop3_b32 v8, v9, v8, 1 bitop3:0x6c
	v_lshl_add_u64 v[106:107], v[2:3], 0, v[146:147]
	v_mov_b64_e32 v[2:3], s[6:7]
	v_xor_b32_e32 v8, v8, v7
	v_mad_u64_u32 v[4:5], s[4:5], v4, s22, v[2:3]
	v_lshlrev_b32_e32 v146, 4, v8
	v_lshl_add_u64 v[108:109], v[4:5], 0, v[146:147]
	v_mad_u32_u24 v4, v149, 3, 2
	v_lshl_or_b32 v1, v4, 3, v1
	v_add_u32_e32 v5, s21, v1
	v_mad_u64_u32 v[2:3], s[4:5], v5, s22, v[2:3]
	v_bfe_u32 v1, v1, 1, 3
	v_lshrrev_b32_e32 v5, 1, v4
	v_lshlrev_b32_e32 v141, 12, v149
	v_bitop3_b32 v1, v5, v1, 1 bitop3:0x6c
	v_readfirstlane_b32 s33, v141
	v_or_b32_e32 v142, 0x400, v141
	v_xor_b32_e32 v1, v1, v7
	s_mov_b32 m0, s33
	v_readfirstlane_b32 s28, v142
	v_or_b32_e32 v143, 0x800, v141
	v_lshlrev_b32_e32 v146, 4, v1
	global_load_lds_dwordx4 v[98:99], off
	s_mov_b32 m0, s28
	v_readfirstlane_b32 s29, v143
	v_or_b32_e32 v144, 0xc00, v141
	v_mul_u32_u24_e32 v1, 0xc00, v149
	global_load_lds_dwordx4 v[100:101], off
	s_mov_b32 m0, s29
	v_readfirstlane_b32 s30, v144
	v_or_b32_e32 v145, 0x10000, v1
	v_lshlrev_b32_e32 v1, 10, v6
	v_lshl_add_u64 v[110:111], v[2:3], 0, v[146:147]
	global_load_lds_dwordx4 v[102:103], off
	s_mov_b32 m0, s30
	v_readfirstlane_b32 s31, v145
	v_or_b32_e32 v146, 0x10000, v1
	v_lshlrev_b32_e32 v4, 10, v4
	global_load_lds_dwordx4 v[104:105], off
	s_mov_b32 m0, s31
	v_readfirstlane_b32 s34, v146
	v_or_b32_e32 v148, 0x10000, v4
	global_load_lds_dwordx4 v[106:107], off
	s_mov_b32 m0, s34
	v_readfirstlane_b32 s35, v148
	v_or_b32_e32 v134, 0x8000, v141
	global_load_lds_dwordx4 v[108:109], off
	s_mov_b32 m0, s35
	s_mov_b64 s[4:5], 0x80
	v_readfirstlane_b32 s24, v134
	v_or_b32_e32 v135, 0x8400, v141
	global_load_lds_dwordx4 v[110:111], off
	v_lshl_add_u64 v[2:3], v[98:99], 0, s[4:5]
	s_mov_b32 m0, s24
	v_readfirstlane_b32 s21, v135
	v_or_b32_e32 v136, 0x8800, v141
	s_movk_i32 s6, 0xc00
	s_waitcnt vmcnt(0)
	s_waitcnt vmcnt(0) lgkmcnt(0)
	s_barrier
	global_load_lds_dwordx4 v[2:3], off
	v_lshl_add_u64 v[2:3], v[100:101], 0, s[4:5]
	s_mov_b32 m0, s21
	v_readfirstlane_b32 s22, v136
	v_or_b32_e32 v137, 0x8c00, v141
	v_mov_b32_e32 v5, 0x16000
	global_load_lds_dwordx4 v[2:3], off
	v_lshl_add_u64 v[2:3], v[102:103], 0, s[4:5]
	s_mov_b32 m0, s22
	v_readfirstlane_b32 s23, v137
	v_mad_u32_u24 v138, v149, s6, v5
	global_load_lds_dwordx4 v[2:3], off
	v_lshl_add_u64 v[2:3], v[104:105], 0, s[4:5]
	s_mov_b32 m0, s23
	v_readfirstlane_b32 s25, v138
	v_add_u32_e32 v139, 0x16000, v1
	global_load_lds_dwordx4 v[2:3], off
	v_lshl_add_u64 v[2:3], v[106:107], 0, s[4:5]
	s_mov_b32 m0, s25
	v_readfirstlane_b32 s26, v139
	v_add_u32_e32 v140, 0x16000, v4
	global_load_lds_dwordx4 v[2:3], off
	v_lshl_add_u64 v[2:3], v[108:109], 0, s[4:5]
	s_mov_b32 m0, s26
	v_readfirstlane_b32 s27, v140
	global_load_lds_dwordx4 v[2:3], off
	v_lshl_add_u64 v[2:3], v[110:111], 0, s[4:5]
	s_mov_b32 m0, s27
	v_and_b32_e32 v156, 31, v0
	global_load_lds_dwordx4 v[2:3], off
	v_and_b32_e32 v2, 64, v0
	v_mov_b32_e32 v3, 0x60
	v_cmp_ne_u32_e32 vcc, 0, v2
	v_bfe_u32 v153, v0, 5, 1
	v_lshrrev_b32_e32 v157, 1, v0
	v_cndmask_b32_e32 v151, 0, v3, vcc
	v_lshlrev_b32_e32 v3, 6, v0
	v_or_b32_e32 v2, v151, v156
	v_and_b32_e32 v115, 0x6000, v3
	v_bfe_u32 v3, v0, 4, 1
	v_lshlrev_b32_e32 v152, 7, v2
	v_or_b32_e32 v2, 6, v153
	v_bitop3_b32 v3, v157, v3, 7 bitop3:0x6c
	s_load_dwordx2 s[6:7], s[0:1], 0x28
	v_xor_b32_e32 v2, v2, v3
	v_lshlrev_b32_e32 v154, 4, v2
	v_or_b32_e32 v2, 4, v153
	v_xor_b32_e32 v2, v2, v3
	v_lshlrev_b32_e32 v155, 4, v2
	v_or_b32_e32 v2, 2, v153
	s_cmp_lt_u32 s2, 64
	v_xor_b32_e32 v2, v2, v3
	s_cselect_b64 s[4:5], -1, 0
	s_cmp_eq_u32 s36, 1
	v_lshlrev_b32_e32 v18, 4, v2
	v_xor_b32_e32 v2, v3, v153
	s_waitcnt lgkmcnt(0)
	s_cselect_b32 s18, s18, s6
	s_cselect_b32 s19, s19, s7
	s_and_b64 s[6:7], s[4:5], exec
	v_and_b32_e32 v1, 63, v0
	v_lshlrev_b32_e32 v150, 7, v156
	v_lshlrev_b32_e32 v2, 4, v2
	s_cselect_b32 s7, s17, s19
	s_cselect_b32 s6, s16, s18
	v_or_b32_e32 v182, v2, v152
	v_or_b32_e32 v2, v2, v115
	v_add_u32_e32 v112, v2, v150
	ds_read_b128 v[2:5], v112
	v_or_b32_e32 v116, 0x10000, v182
	v_add_u32_e32 v117, 0x11000, v182
	v_add_u32_e32 v118, 0x12000, v182
	ds_read_b128 v[6:9], v116
	ds_read_b128 v[10:13], v117
	ds_read_b128 v[14:17], v112 offset:4096
	ds_read_b128 v[122:125], v118
	v_or_b32_e32 v19, v18, v115
	v_add_u32_e32 v113, v19, v150
	s_waitcnt lgkmcnt(0)
	v_mfma_f32_32x32x16_f16 v[82:97], v[2:5], v[6:9], 0
	ds_read_b128 v[126:129], v113
	v_or_b32_e32 v183, v18, v152
	v_add_u32_e32 v120, 0x11000, v183
	v_or_b32_e32 v119, 0x10000, v183
	ds_read_b128 v[130:133], v113 offset:4096
	ds_read_b128 v[158:161], v119
	v_add_u32_e32 v121, 0x12000, v183
	ds_read_b128 v[162:165], v120
	ds_read_b128 v[166:169], v121
	v_mfma_f32_32x32x16_f16 v[66:81], v[2:5], v[10:13], 0
	v_mfma_f32_32x32x16_f16 v[50:65], v[2:5], v[122:125], 0
	v_mfma_f32_32x32x16_f16 v[34:49], v[14:17], v[6:9], 0
	v_mfma_f32_32x32x16_f16 v[18:33], v[14:17], v[10:13], 0
	v_mfma_f32_32x32x16_f16 v[2:17], v[14:17], v[122:125], 0
	s_waitcnt lgkmcnt(0)
	v_mfma_f32_32x32x16_f16 v[82:97], v[126:129], v[158:161], v[82:97]
	v_or_b32_e32 v114, v155, v115
	v_or_b32_e32 v155, v155, v152
	v_add_u32_e32 v114, v114, v150
	v_or_b32_e32 v122, 0x10000, v155
	v_add_u32_e32 v123, 0x11000, v155
	v_add_u32_e32 v124, 0x12000, v155
	v_mfma_f32_32x32x16_f16 v[66:81], v[126:129], v[162:165], v[66:81]
	v_mfma_f32_32x32x16_f16 v[50:65], v[126:129], v[166:169], v[50:65]
	v_mfma_f32_32x32x16_f16 v[34:49], v[130:133], v[158:161], v[34:49]
	ds_read_b128 v[126:129], v114
	ds_read_b128 v[158:161], v114 offset:4096
	v_mfma_f32_32x32x16_f16 v[18:33], v[130:133], v[162:165], v[18:33]
	ds_read_b128 v[162:165], v122
	ds_read_b128 v[170:173], v123
	ds_read_b128 v[174:177], v124
	v_mfma_f32_32x32x16_f16 v[2:17], v[130:133], v[166:169], v[2:17]
	s_waitcnt lgkmcnt(0)
	v_mfma_f32_32x32x16_f16 v[82:97], v[126:129], v[162:165], v[82:97]
	v_or_b32_e32 v115, v154, v115
	v_or_b32_e32 v133, v154, v152
	v_add_u32_e32 v115, v115, v150
	v_or_b32_e32 v125, 0x10000, v133
	v_mfma_f32_32x32x16_f16 v[66:81], v[126:129], v[170:173], v[66:81]
	v_mfma_f32_32x32x16_f16 v[50:65], v[126:129], v[174:177], v[50:65]
	v_add_u32_e32 v126, 0x11000, v133
	v_add_u32_e32 v127, 0x12000, v133
	v_mfma_f32_32x32x16_f16 v[34:49], v[158:161], v[162:165], v[34:49]
	ds_read_b128 v[128:131], v115
	ds_read_b128 v[162:165], v115 offset:4096
	v_mfma_f32_32x32x16_f16 v[18:33], v[158:161], v[170:173], v[18:33]
	ds_read_b128 v[166:169], v125
	ds_read_b128 v[170:173], v126
	ds_read_b128 v[178:181], v127
	v_mfma_f32_32x32x16_f16 v[2:17], v[158:161], v[174:177], v[2:17]
	s_waitcnt lgkmcnt(0)
	v_mfma_f32_32x32x16_f16 v[82:97], v[128:131], v[166:169], v[82:97]
	v_mfma_f32_32x32x16_f16 v[66:81], v[128:131], v[170:173], v[66:81]
	v_mfma_f32_32x32x16_f16 v[50:65], v[128:131], v[178:181], v[50:65]
	v_mfma_f32_32x32x16_f16 v[34:49], v[162:165], v[166:169], v[34:49]
	v_mfma_f32_32x32x16_f16 v[18:33], v[162:165], v[170:173], v[18:33]
	v_mfma_f32_32x32x16_f16 v[2:17], v[162:165], v[178:181], v[2:17]
	s_mov_b64 s[16:17], 0x100
	s_mov_b32 m0, s33
	v_lshl_add_u64 v[128:129], v[98:99], 0, s[16:17]
	s_waitcnt vmcnt(0)
	s_waitcnt vmcnt(0)
	s_barrier
	global_load_lds_dwordx4 v[128:129], off
	v_lshl_add_u64 v[128:129], v[100:101], 0, s[16:17]
	s_mov_b32 m0, s28
	s_nop 0
	global_load_lds_dwordx4 v[128:129], off
	v_lshl_add_u64 v[128:129], v[102:103], 0, s[16:17]
	s_mov_b32 m0, s29
	s_nop 0
	global_load_lds_dwordx4 v[128:129], off
	v_lshl_add_u64 v[128:129], v[104:105], 0, s[16:17]
	s_mov_b32 m0, s30
	s_nop 0
	global_load_lds_dwordx4 v[128:129], off
	v_lshl_add_u64 v[128:129], v[106:107], 0, s[16:17]
	s_mov_b32 m0, s31
	s_nop 0
	global_load_lds_dwordx4 v[128:129], off
	v_lshl_add_u64 v[128:129], v[108:109], 0, s[16:17]
	s_mov_b32 m0, s34
	s_nop 0
	global_load_lds_dwordx4 v[128:129], off
	v_lshl_add_u64 v[128:129], v[110:111], 0, s[16:17]
	s_mov_b32 m0, s35
	s_nop 0
	global_load_lds_dwordx4 v[128:129], off
	ds_read_b128 v[158:161], v112 offset:32768
	v_add_u32_e32 v129, 0x16000, v182
	v_add_u32_e32 v130, 0x17000, v182
	v_or_b32_e32 v131, 0x18000, v182
	ds_read_b128 v[162:165], v129
	ds_read_b128 v[166:169], v112 offset:36864
	ds_read_b128 v[170:173], v130
	ds_read_b128 v[174:177], v131
	v_add_u32_e32 v128, 0x16000, v183
	ds_read_b128 v[178:181], v128
	s_waitcnt lgkmcnt(0)
	v_mfma_f32_32x32x16_f16 v[82:97], v[158:161], v[162:165], v[82:97]
	v_mfma_f32_32x32x16_f16 v[66:81], v[158:161], v[170:173], v[66:81]
	v_mfma_f32_32x32x16_f16 v[50:65], v[158:161], v[174:177], v[50:65]
	v_mfma_f32_32x32x16_f16 v[34:49], v[166:169], v[162:165], v[34:49]
	v_mfma_f32_32x32x16_f16 v[18:33], v[166:169], v[170:173], v[18:33]
	ds_read_b128 v[158:161], v113 offset:32768
	ds_read_b128 v[162:165], v113 offset:36864
	ds_read_b128 v[170:173], v128 offset:4096
	ds_read_b128 v[182:185], v128 offset:8192
	v_mfma_f32_32x32x16_f16 v[2:17], v[166:169], v[174:177], v[2:17]
	s_waitcnt lgkmcnt(0)
	v_mfma_f32_32x32x16_f16 v[82:97], v[158:161], v[178:181], v[82:97]
	v_add_u32_e32 v132, 0x16000, v155
	v_mfma_f32_32x32x16_f16 v[66:81], v[158:161], v[170:173], v[66:81]
	v_mfma_f32_32x32x16_f16 v[50:65], v[158:161], v[182:185], v[50:65]
	ds_read_b128 v[158:161], v114 offset:32768
	ds_read_b128 v[166:169], v114 offset:36864
	v_mfma_f32_32x32x16_f16 v[34:49], v[162:165], v[178:181], v[34:49]
	v_mfma_f32_32x32x16_f16 v[18:33], v[162:165], v[170:173], v[18:33]
	ds_read_b128 v[170:173], v132
	ds_read_b128 v[174:177], v132 offset:4096
	ds_read_b128 v[178:181], v132 offset:8192
	v_mfma_f32_32x32x16_f16 v[2:17], v[162:165], v[182:185], v[2:17]
	s_waitcnt lgkmcnt(0)
	v_mfma_f32_32x32x16_f16 v[82:97], v[158:161], v[170:173], v[82:97]
	v_add_u32_e32 v133, 0x16000, v133
	v_mfma_f32_32x32x16_f16 v[66:81], v[158:161], v[174:177], v[66:81]
	v_mfma_f32_32x32x16_f16 v[50:65], v[158:161], v[178:181], v[50:65]
	ds_read_b128 v[158:161], v115 offset:32768
	ds_read_b128 v[162:165], v115 offset:36864
	v_mfma_f32_32x32x16_f16 v[34:49], v[166:169], v[170:173], v[34:49]
	v_mfma_f32_32x32x16_f16 v[18:33], v[166:169], v[174:177], v[18:33]
	ds_read_b128 v[170:173], v133
	ds_read_b128 v[174:177], v133 offset:4096
	ds_read_b128 v[182:185], v133 offset:8192
	v_mfma_f32_32x32x16_f16 v[2:17], v[166:169], v[178:181], v[2:17]
	s_waitcnt lgkmcnt(0)
	v_mfma_f32_32x32x16_f16 v[82:97], v[158:161], v[170:173], v[82:97]
	v_mfma_f32_32x32x16_f16 v[66:81], v[158:161], v[174:177], v[66:81]
	v_mfma_f32_32x32x16_f16 v[50:65], v[158:161], v[182:185], v[50:65]
	v_mfma_f32_32x32x16_f16 v[34:49], v[162:165], v[170:173], v[34:49]
	v_mfma_f32_32x32x16_f16 v[18:33], v[162:165], v[174:177], v[18:33]
	v_mfma_f32_32x32x16_f16 v[2:17], v[162:165], v[182:185], v[2:17]
	s_mov_b64 s[16:17], 0x180
	s_mov_b32 m0, s24
	v_lshl_add_u64 v[154:155], v[98:99], 0, s[16:17]
	s_waitcnt vmcnt(0)
	s_waitcnt vmcnt(0)
	s_barrier
	global_load_lds_dwordx4 v[154:155], off
	v_lshl_add_u64 v[154:155], v[100:101], 0, s[16:17]
	s_mov_b32 m0, s21
	s_nop 0
	global_load_lds_dwordx4 v[154:155], off
	v_lshl_add_u64 v[154:155], v[102:103], 0, s[16:17]
	s_mov_b32 m0, s22
	s_nop 0
	global_load_lds_dwordx4 v[154:155], off
	v_lshl_add_u64 v[154:155], v[104:105], 0, s[16:17]
	s_mov_b32 m0, s23
	s_nop 0
	global_load_lds_dwordx4 v[154:155], off
	v_lshl_add_u64 v[154:155], v[106:107], 0, s[16:17]
	s_mov_b32 m0, s25
	s_nop 0
	global_load_lds_dwordx4 v[154:155], off
	v_lshl_add_u64 v[154:155], v[108:109], 0, s[16:17]
	s_mov_b32 m0, s26
	s_nop 0
	global_load_lds_dwordx4 v[154:155], off
	v_lshl_add_u64 v[154:155], v[110:111], 0, s[16:17]
	s_mov_b32 m0, s27
	s_nop 0
	global_load_lds_dwordx4 v[154:155], off
	ds_read_b128 v[158:161], v112
	ds_read_b128 v[162:165], v116
	ds_read_b128 v[166:169], v112 offset:4096
	ds_read_b128 v[170:173], v117
	ds_read_b128 v[174:177], v118
	ds_read_b128 v[178:181], v113
	s_waitcnt lgkmcnt(0)
	v_mfma_f32_32x32x16_f16 v[82:97], v[158:161], v[162:165], v[82:97]
	v_mfma_f32_32x32x16_f16 v[66:81], v[158:161], v[170:173], v[66:81]
	v_mfma_f32_32x32x16_f16 v[50:65], v[158:161], v[174:177], v[50:65]
	v_mfma_f32_32x32x16_f16 v[34:49], v[166:169], v[162:165], v[34:49]
	v_mfma_f32_32x32x16_f16 v[18:33], v[166:169], v[170:173], v[18:33]
	ds_read_b128 v[158:161], v113 offset:4096
	ds_read_b128 v[162:165], v119
	ds_read_b128 v[170:173], v120
	ds_read_b128 v[182:185], v121
	v_mfma_f32_32x32x16_f16 v[2:17], v[166:169], v[174:177], v[2:17]
	s_waitcnt lgkmcnt(0)
	v_mfma_f32_32x32x16_f16 v[82:97], v[178:181], v[162:165], v[82:97]
	v_mfma_f32_32x32x16_f16 v[66:81], v[178:181], v[170:173], v[66:81]
	v_mfma_f32_32x32x16_f16 v[50:65], v[178:181], v[182:185], v[50:65]
	v_mfma_f32_32x32x16_f16 v[34:49], v[158:161], v[162:165], v[34:49]
	v_mfma_f32_32x32x16_f16 v[18:33], v[158:161], v[170:173], v[18:33]
	ds_read_b128 v[162:165], v114
	ds_read_b128 v[166:169], v114 offset:4096
	ds_read_b128 v[170:173], v122
	ds_read_b128 v[174:177], v123
	ds_read_b128 v[178:181], v124
	v_mfma_f32_32x32x16_f16 v[2:17], v[158:161], v[182:185], v[2:17]
	s_waitcnt lgkmcnt(0)
	v_mfma_f32_32x32x16_f16 v[82:97], v[162:165], v[170:173], v[82:97]
	v_mfma_f32_32x32x16_f16 v[66:81], v[162:165], v[174:177], v[66:81]
	v_mfma_f32_32x32x16_f16 v[50:65], v[162:165], v[178:181], v[50:65]
	v_mfma_f32_32x32x16_f16 v[34:49], v[166:169], v[170:173], v[34:49]
	v_mfma_f32_32x32x16_f16 v[18:33], v[166:169], v[174:177], v[18:33]
	ds_read_b128 v[158:161], v115
	ds_read_b128 v[162:165], v115 offset:4096
	ds_read_b128 v[170:173], v125
	ds_read_b128 v[174:177], v126
	ds_read_b128 v[182:185], v127
	v_mfma_f32_32x32x16_f16 v[2:17], v[166:169], v[178:181], v[2:17]
	s_waitcnt lgkmcnt(0)
	v_mfma_f32_32x32x16_f16 v[82:97], v[158:161], v[170:173], v[82:97]
	v_mfma_f32_32x32x16_f16 v[66:81], v[158:161], v[174:177], v[66:81]
	v_mfma_f32_32x32x16_f16 v[50:65], v[158:161], v[182:185], v[50:65]
	v_mfma_f32_32x32x16_f16 v[34:49], v[162:165], v[170:173], v[34:49]
	v_mfma_f32_32x32x16_f16 v[18:33], v[162:165], v[174:177], v[18:33]
	v_mfma_f32_32x32x16_f16 v[2:17], v[162:165], v[182:185], v[2:17]
	s_mov_b64 s[16:17], 0x200
	s_mov_b32 m0, s33
	v_lshl_add_u64 v[154:155], v[98:99], 0, s[16:17]
	s_waitcnt vmcnt(0)
	s_waitcnt vmcnt(0)
	s_barrier
	global_load_lds_dwordx4 v[154:155], off
	v_lshl_add_u64 v[154:155], v[100:101], 0, s[16:17]
	s_mov_b32 m0, s28
	s_nop 0
	global_load_lds_dwordx4 v[154:155], off
	v_lshl_add_u64 v[154:155], v[102:103], 0, s[16:17]
	s_mov_b32 m0, s29
	s_nop 0
	global_load_lds_dwordx4 v[154:155], off
	v_lshl_add_u64 v[154:155], v[104:105], 0, s[16:17]
	s_mov_b32 m0, s30
	s_nop 0
	global_load_lds_dwordx4 v[154:155], off
	v_lshl_add_u64 v[154:155], v[106:107], 0, s[16:17]
	s_mov_b32 m0, s31
	s_nop 0
	global_load_lds_dwordx4 v[154:155], off
	v_lshl_add_u64 v[154:155], v[108:109], 0, s[16:17]
	s_mov_b32 m0, s34
	s_nop 0
	global_load_lds_dwordx4 v[154:155], off
	v_lshl_add_u64 v[154:155], v[110:111], 0, s[16:17]
	s_mov_b32 m0, s35
	s_nop 0
	global_load_lds_dwordx4 v[154:155], off
	ds_read_b128 v[158:161], v112 offset:32768
	ds_read_b128 v[162:165], v129
	ds_read_b128 v[166:169], v112 offset:36864
	ds_read_b128 v[170:173], v130
	ds_read_b128 v[174:177], v131
	ds_read_b128 v[178:181], v128
	s_waitcnt lgkmcnt(0)
	v_mfma_f32_32x32x16_f16 v[82:97], v[158:161], v[162:165], v[82:97]
	v_mfma_f32_32x32x16_f16 v[66:81], v[158:161], v[170:173], v[66:81]
	v_mfma_f32_32x32x16_f16 v[50:65], v[158:161], v[174:177], v[50:65]
	v_mfma_f32_32x32x16_f16 v[34:49], v[166:169], v[162:165], v[34:49]
	v_mfma_f32_32x32x16_f16 v[18:33], v[166:169], v[170:173], v[18:33]
	ds_read_b128 v[158:161], v113 offset:32768
	ds_read_b128 v[162:165], v113 offset:36864
	ds_read_b128 v[170:173], v128 offset:4096
	ds_read_b128 v[182:185], v128 offset:8192
	v_mfma_f32_32x32x16_f16 v[2:17], v[166:169], v[174:177], v[2:17]
	s_waitcnt lgkmcnt(0)
	v_mfma_f32_32x32x16_f16 v[82:97], v[158:161], v[178:181], v[82:97]
	v_mfma_f32_32x32x16_f16 v[66:81], v[158:161], v[170:173], v[66:81]
	v_mfma_f32_32x32x16_f16 v[50:65], v[158:161], v[182:185], v[50:65]
	v_mfma_f32_32x32x16_f16 v[34:49], v[162:165], v[178:181], v[34:49]
	v_mfma_f32_32x32x16_f16 v[18:33], v[162:165], v[170:173], v[18:33]
	ds_read_b128 v[158:161], v114 offset:32768
	ds_read_b128 v[166:169], v114 offset:36864
	ds_read_b128 v[170:173], v132
	ds_read_b128 v[174:177], v132 offset:4096
	ds_read_b128 v[178:181], v132 offset:8192
	v_mfma_f32_32x32x16_f16 v[2:17], v[162:165], v[182:185], v[2:17]
	s_waitcnt lgkmcnt(0)
	v_mfma_f32_32x32x16_f16 v[82:97], v[158:161], v[170:173], v[82:97]
	v_mfma_f32_32x32x16_f16 v[66:81], v[158:161], v[174:177], v[66:81]
	v_mfma_f32_32x32x16_f16 v[50:65], v[158:161], v[178:181], v[50:65]
	v_mfma_f32_32x32x16_f16 v[34:49], v[166:169], v[170:173], v[34:49]
	v_mfma_f32_32x32x16_f16 v[18:33], v[166:169], v[174:177], v[18:33]
	ds_read_b128 v[158:161], v115 offset:32768
	ds_read_b128 v[162:165], v115 offset:36864
	ds_read_b128 v[170:173], v133
	ds_read_b128 v[174:177], v133 offset:4096
	ds_read_b128 v[182:185], v133 offset:8192
	v_mfma_f32_32x32x16_f16 v[2:17], v[166:169], v[178:181], v[2:17]
	s_waitcnt lgkmcnt(0)
	v_mfma_f32_32x32x16_f16 v[82:97], v[158:161], v[170:173], v[82:97]
	v_mfma_f32_32x32x16_f16 v[66:81], v[158:161], v[174:177], v[66:81]
	v_mfma_f32_32x32x16_f16 v[50:65], v[158:161], v[182:185], v[50:65]
	v_mfma_f32_32x32x16_f16 v[34:49], v[162:165], v[170:173], v[34:49]
	v_mfma_f32_32x32x16_f16 v[18:33], v[162:165], v[174:177], v[18:33]
	v_mfma_f32_32x32x16_f16 v[2:17], v[162:165], v[182:185], v[2:17]
	s_mov_b64 s[16:17], 0x280
	s_mov_b32 m0, s24
	v_lshl_add_u64 v[154:155], v[98:99], 0, s[16:17]
	s_waitcnt vmcnt(0)
	s_waitcnt vmcnt(0)
	s_barrier
	global_load_lds_dwordx4 v[154:155], off
	v_lshl_add_u64 v[154:155], v[100:101], 0, s[16:17]
	s_mov_b32 m0, s21
	s_nop 0
	global_load_lds_dwordx4 v[154:155], off
	v_lshl_add_u64 v[154:155], v[102:103], 0, s[16:17]
	s_mov_b32 m0, s22
	s_nop 0
	global_load_lds_dwordx4 v[154:155], off
	v_lshl_add_u64 v[154:155], v[104:105], 0, s[16:17]
	s_mov_b32 m0, s23
	s_nop 0
	global_load_lds_dwordx4 v[154:155], off
	v_lshl_add_u64 v[154:155], v[106:107], 0, s[16:17]
	s_mov_b32 m0, s25
	s_nop 0
	global_load_lds_dwordx4 v[154:155], off
	v_lshl_add_u64 v[154:155], v[108:109], 0, s[16:17]
	s_mov_b32 m0, s26
	s_nop 0
	global_load_lds_dwordx4 v[154:155], off
	v_lshl_add_u64 v[154:155], v[110:111], 0, s[16:17]
	s_mov_b32 m0, s27
	s_nop 0
	global_load_lds_dwordx4 v[154:155], off
	ds_read_b128 v[158:161], v112
	ds_read_b128 v[162:165], v116
	ds_read_b128 v[166:169], v112 offset:4096
	ds_read_b128 v[170:173], v117
	ds_read_b128 v[174:177], v118
	ds_read_b128 v[178:181], v113
	s_waitcnt lgkmcnt(0)
	v_mfma_f32_32x32x16_f16 v[82:97], v[158:161], v[162:165], v[82:97]
	v_mfma_f32_32x32x16_f16 v[66:81], v[158:161], v[170:173], v[66:81]
	v_mfma_f32_32x32x16_f16 v[50:65], v[158:161], v[174:177], v[50:65]
	v_mfma_f32_32x32x16_f16 v[34:49], v[166:169], v[162:165], v[34:49]
	v_mfma_f32_32x32x16_f16 v[18:33], v[166:169], v[170:173], v[18:33]
	ds_read_b128 v[158:161], v113 offset:4096
	ds_read_b128 v[162:165], v119
	ds_read_b128 v[170:173], v120
	ds_read_b128 v[182:185], v121
	v_mfma_f32_32x32x16_f16 v[2:17], v[166:169], v[174:177], v[2:17]
	s_waitcnt lgkmcnt(0)
	v_mfma_f32_32x32x16_f16 v[82:97], v[178:181], v[162:165], v[82:97]
	v_mfma_f32_32x32x16_f16 v[66:81], v[178:181], v[170:173], v[66:81]
	v_mfma_f32_32x32x16_f16 v[50:65], v[178:181], v[182:185], v[50:65]
	v_mfma_f32_32x32x16_f16 v[34:49], v[158:161], v[162:165], v[34:49]
	v_mfma_f32_32x32x16_f16 v[18:33], v[158:161], v[170:173], v[18:33]
	ds_read_b128 v[162:165], v114
	ds_read_b128 v[166:169], v114 offset:4096
	ds_read_b128 v[170:173], v122
	ds_read_b128 v[174:177], v123
	ds_read_b128 v[178:181], v124
	v_mfma_f32_32x32x16_f16 v[2:17], v[158:161], v[182:185], v[2:17]
	s_waitcnt lgkmcnt(0)
	v_mfma_f32_32x32x16_f16 v[82:97], v[162:165], v[170:173], v[82:97]
	v_mfma_f32_32x32x16_f16 v[66:81], v[162:165], v[174:177], v[66:81]
	v_mfma_f32_32x32x16_f16 v[50:65], v[162:165], v[178:181], v[50:65]
	v_mfma_f32_32x32x16_f16 v[34:49], v[166:169], v[170:173], v[34:49]
	v_mfma_f32_32x32x16_f16 v[18:33], v[166:169], v[174:177], v[18:33]
	ds_read_b128 v[158:161], v115
	ds_read_b128 v[162:165], v115 offset:4096
	ds_read_b128 v[170:173], v125
	ds_read_b128 v[174:177], v126
	ds_read_b128 v[182:185], v127
	v_mfma_f32_32x32x16_f16 v[2:17], v[166:169], v[178:181], v[2:17]
	s_waitcnt lgkmcnt(0)
	v_mfma_f32_32x32x16_f16 v[82:97], v[158:161], v[170:173], v[82:97]
	v_mfma_f32_32x32x16_f16 v[66:81], v[158:161], v[174:177], v[66:81]
	v_mfma_f32_32x32x16_f16 v[50:65], v[158:161], v[182:185], v[50:65]
	v_mfma_f32_32x32x16_f16 v[34:49], v[162:165], v[170:173], v[34:49]
	v_mfma_f32_32x32x16_f16 v[18:33], v[162:165], v[174:177], v[18:33]
	v_mfma_f32_32x32x16_f16 v[2:17], v[162:165], v[182:185], v[2:17]
	s_mov_b64 s[22:23], 0x300
	v_readfirstlane_b32 s24, v141
	v_lshl_add_u64 v[154:155], v[98:99], 0, s[22:23]
	s_mov_b32 m0, s24
	v_readfirstlane_b32 s16, v142
	s_waitcnt vmcnt(0)
	s_waitcnt vmcnt(0)
	s_barrier
	global_load_lds_dwordx4 v[154:155], off
	v_lshl_add_u64 v[154:155], v[100:101], 0, s[22:23]
	s_mov_b32 m0, s16
	v_readfirstlane_b32 s17, v143
	global_load_lds_dwordx4 v[154:155], off
	v_lshl_add_u64 v[154:155], v[102:103], 0, s[22:23]
	s_mov_b32 m0, s17
	v_readfirstlane_b32 s18, v144
	global_load_lds_dwordx4 v[154:155], off
	v_lshl_add_u64 v[142:143], v[104:105], 0, s[22:23]
	s_mov_b32 m0, s18
	v_readfirstlane_b32 s19, v145
	global_load_lds_dwordx4 v[142:143], off
	v_lshl_add_u64 v[142:143], v[106:107], 0, s[22:23]
	s_mov_b32 m0, s19
	v_readfirstlane_b32 s21, v146
	global_load_lds_dwordx4 v[142:143], off
	v_lshl_add_u64 v[142:143], v[108:109], 0, s[22:23]
	s_mov_b32 m0, s21
	s_nop 0
	global_load_lds_dwordx4 v[142:143], off
	v_lshl_add_u64 v[142:143], v[110:111], 0, s[22:23]
	v_readfirstlane_b32 s22, v148
	s_mov_b32 m0, s22
	s_nop 0
	global_load_lds_dwordx4 v[142:143], off
	ds_read_b128 v[142:145], v112 offset:32768
	ds_read_b128 v[158:161], v129
	ds_read_b128 v[162:165], v112 offset:36864
	ds_read_b128 v[166:169], v130
	ds_read_b128 v[170:173], v131
	ds_read_b128 v[174:177], v128
	s_waitcnt lgkmcnt(0)
	v_mfma_f32_32x32x16_f16 v[82:97], v[142:145], v[158:161], v[82:97]
	v_mfma_f32_32x32x16_f16 v[66:81], v[142:145], v[166:169], v[66:81]
	v_mfma_f32_32x32x16_f16 v[50:65], v[142:145], v[170:173], v[50:65]
	v_mfma_f32_32x32x16_f16 v[34:49], v[162:165], v[158:161], v[34:49]
	v_mfma_f32_32x32x16_f16 v[18:33], v[162:165], v[166:169], v[18:33]
	ds_read_b128 v[142:145], v113 offset:32768
	ds_read_b128 v[158:161], v113 offset:36864
	ds_read_b128 v[166:169], v128 offset:4096
	ds_read_b128 v[178:181], v128 offset:8192
	v_mfma_f32_32x32x16_f16 v[2:17], v[162:165], v[170:173], v[2:17]
	s_waitcnt lgkmcnt(0)
	v_mfma_f32_32x32x16_f16 v[82:97], v[142:145], v[174:177], v[82:97]
	v_mfma_f32_32x32x16_f16 v[66:81], v[142:145], v[166:169], v[66:81]
	v_mfma_f32_32x32x16_f16 v[50:65], v[142:145], v[178:181], v[50:65]
	v_mfma_f32_32x32x16_f16 v[34:49], v[158:161], v[174:177], v[34:49]
	v_mfma_f32_32x32x16_f16 v[18:33], v[158:161], v[166:169], v[18:33]
	ds_read_b128 v[142:145], v114 offset:32768
	ds_read_b128 v[162:165], v114 offset:36864
	ds_read_b128 v[166:169], v132
	ds_read_b128 v[170:173], v132 offset:4096
	ds_read_b128 v[174:177], v132 offset:8192
	v_mfma_f32_32x32x16_f16 v[2:17], v[158:161], v[178:181], v[2:17]
	s_waitcnt lgkmcnt(0)
	v_mfma_f32_32x32x16_f16 v[82:97], v[142:145], v[166:169], v[82:97]
	v_mfma_f32_32x32x16_f16 v[66:81], v[142:145], v[170:173], v[66:81]
	v_mfma_f32_32x32x16_f16 v[50:65], v[142:145], v[174:177], v[50:65]
	v_mfma_f32_32x32x16_f16 v[34:49], v[162:165], v[166:169], v[34:49]
	v_mfma_f32_32x32x16_f16 v[18:33], v[162:165], v[170:173], v[18:33]
	ds_read_b128 v[142:145], v115 offset:32768
	ds_read_b128 v[158:161], v115 offset:36864
	ds_read_b128 v[166:169], v133
	ds_read_b128 v[170:173], v133 offset:4096
	ds_read_b128 v[178:181], v133 offset:8192
	v_mfma_f32_32x32x16_f16 v[2:17], v[162:165], v[174:177], v[2:17]
	s_waitcnt lgkmcnt(0)
	v_mfma_f32_32x32x16_f16 v[82:97], v[142:145], v[166:169], v[82:97]
	v_mfma_f32_32x32x16_f16 v[66:81], v[142:145], v[170:173], v[66:81]
	v_mfma_f32_32x32x16_f16 v[50:65], v[142:145], v[178:181], v[50:65]
	v_mfma_f32_32x32x16_f16 v[34:49], v[158:161], v[166:169], v[34:49]
	v_mfma_f32_32x32x16_f16 v[18:33], v[158:161], v[170:173], v[18:33]
	v_mfma_f32_32x32x16_f16 v[2:17], v[158:161], v[178:181], v[2:17]
	s_mov_b64 s[34:35], 0x380
	v_readfirstlane_b32 s30, v134
	v_lshl_add_u64 v[142:143], v[98:99], 0, s[34:35]
	s_mov_b32 m0, s30
	v_readfirstlane_b32 s23, v135
	s_waitcnt vmcnt(0)
	s_waitcnt vmcnt(0)
	s_barrier
	global_load_lds_dwordx4 v[142:143], off
	v_lshl_add_u64 v[142:143], v[100:101], 0, s[34:35]
	s_mov_b32 m0, s23
	v_readfirstlane_b32 s25, v136
	global_load_lds_dwordx4 v[142:143], off
	v_lshl_add_u64 v[134:135], v[102:103], 0, s[34:35]
	s_mov_b32 m0, s25
	v_readfirstlane_b32 s26, v137
	global_load_lds_dwordx4 v[134:135], off
	v_lshl_add_u64 v[134:135], v[104:105], 0, s[34:35]
	s_mov_b32 m0, s26
	v_readfirstlane_b32 s27, v138
	global_load_lds_dwordx4 v[134:135], off
	v_lshl_add_u64 v[134:135], v[106:107], 0, s[34:35]
	s_mov_b32 m0, s27
	v_readfirstlane_b32 s28, v139
	global_load_lds_dwordx4 v[134:135], off
	v_lshl_add_u64 v[134:135], v[108:109], 0, s[34:35]
	s_mov_b32 m0, s28
	v_readfirstlane_b32 s29, v140
	global_load_lds_dwordx4 v[134:135], off
	v_lshl_add_u64 v[134:135], v[110:111], 0, s[34:35]
	s_mov_b32 m0, s29
	s_nop 0
	global_load_lds_dwordx4 v[134:135], off
	ds_read_b128 v[134:137], v112
	ds_read_b128 v[138:141], v116
	ds_read_b128 v[142:145], v112 offset:4096
	ds_read_b128 v[158:161], v117
	ds_read_b128 v[162:165], v118
	ds_read_b128 v[166:169], v113
	s_waitcnt lgkmcnt(0)
	v_mfma_f32_32x32x16_f16 v[82:97], v[134:137], v[138:141], v[82:97]
	v_mfma_f32_32x32x16_f16 v[66:81], v[134:137], v[158:161], v[66:81]
	v_mfma_f32_32x32x16_f16 v[50:65], v[134:137], v[162:165], v[50:65]
	v_mfma_f32_32x32x16_f16 v[34:49], v[142:145], v[138:141], v[34:49]
	v_mfma_f32_32x32x16_f16 v[18:33], v[142:145], v[158:161], v[18:33]
	ds_read_b128 v[134:137], v113 offset:4096
	ds_read_b128 v[138:141], v119
	ds_read_b128 v[158:161], v120
	ds_read_b128 v[170:173], v121
	v_mfma_f32_32x32x16_f16 v[2:17], v[142:145], v[162:165], v[2:17]
	s_waitcnt lgkmcnt(0)
	v_mfma_f32_32x32x16_f16 v[82:97], v[166:169], v[138:141], v[82:97]
	v_mfma_f32_32x32x16_f16 v[66:81], v[166:169], v[158:161], v[66:81]
	v_mfma_f32_32x32x16_f16 v[50:65], v[166:169], v[170:173], v[50:65]
	v_mfma_f32_32x32x16_f16 v[34:49], v[134:137], v[138:141], v[34:49]
	v_mfma_f32_32x32x16_f16 v[18:33], v[134:137], v[158:161], v[18:33]
	ds_read_b128 v[138:141], v114
	ds_read_b128 v[142:145], v114 offset:4096
	ds_read_b128 v[158:161], v122
	ds_read_b128 v[162:165], v123
	ds_read_b128 v[166:169], v124
	v_mfma_f32_32x32x16_f16 v[2:17], v[134:137], v[170:173], v[2:17]
	s_waitcnt lgkmcnt(0)
	v_mfma_f32_32x32x16_f16 v[82:97], v[138:141], v[158:161], v[82:97]
	v_mfma_f32_32x32x16_f16 v[66:81], v[138:141], v[162:165], v[66:81]
	v_mfma_f32_32x32x16_f16 v[50:65], v[138:141], v[166:169], v[50:65]
	v_mfma_f32_32x32x16_f16 v[34:49], v[142:145], v[158:161], v[34:49]
	v_mfma_f32_32x32x16_f16 v[18:33], v[142:145], v[162:165], v[18:33]
	ds_read_b128 v[134:137], v115
	ds_read_b128 v[138:141], v115 offset:4096
	ds_read_b128 v[158:161], v125
	ds_read_b128 v[162:165], v126
	ds_read_b128 v[170:173], v127
	v_mfma_f32_32x32x16_f16 v[2:17], v[142:145], v[166:169], v[2:17]
	s_waitcnt lgkmcnt(0)
	v_mfma_f32_32x32x16_f16 v[82:97], v[134:137], v[158:161], v[82:97]
	v_mfma_f32_32x32x16_f16 v[66:81], v[134:137], v[162:165], v[66:81]
	v_mfma_f32_32x32x16_f16 v[50:65], v[134:137], v[170:173], v[50:65]
	v_mfma_f32_32x32x16_f16 v[34:49], v[138:141], v[158:161], v[34:49]
	v_mfma_f32_32x32x16_f16 v[18:33], v[138:141], v[162:165], v[18:33]
	v_mfma_f32_32x32x16_f16 v[2:17], v[138:141], v[170:173], v[2:17]
	s_mov_b64 s[34:35], 0x400
	s_mov_b32 m0, s24
	v_lshl_add_u64 v[134:135], v[98:99], 0, s[34:35]
	s_waitcnt vmcnt(0)
	s_waitcnt vmcnt(0)
	s_barrier
	global_load_lds_dwordx4 v[134:135], off
	v_lshl_add_u64 v[134:135], v[100:101], 0, s[34:35]
	s_mov_b32 m0, s16
	s_nop 0
	global_load_lds_dwordx4 v[134:135], off
	v_lshl_add_u64 v[134:135], v[102:103], 0, s[34:35]
	s_mov_b32 m0, s17
	s_nop 0
	global_load_lds_dwordx4 v[134:135], off
	v_lshl_add_u64 v[134:135], v[104:105], 0, s[34:35]
	s_mov_b32 m0, s18
	s_nop 0
	global_load_lds_dwordx4 v[134:135], off
	v_lshl_add_u64 v[134:135], v[106:107], 0, s[34:35]
	s_mov_b32 m0, s19
	s_nop 0
	global_load_lds_dwordx4 v[134:135], off
	v_lshl_add_u64 v[134:135], v[108:109], 0, s[34:35]
	s_mov_b32 m0, s21
	s_nop 0
	global_load_lds_dwordx4 v[134:135], off
	v_lshl_add_u64 v[134:135], v[110:111], 0, s[34:35]
	s_mov_b32 m0, s22
	s_nop 0
	global_load_lds_dwordx4 v[134:135], off
	ds_read_b128 v[134:137], v112 offset:32768
	ds_read_b128 v[138:141], v129
	ds_read_b128 v[142:145], v112 offset:36864
	ds_read_b128 v[158:161], v130
	ds_read_b128 v[162:165], v131
	ds_read_b128 v[166:169], v128
	s_waitcnt lgkmcnt(0)
	v_mfma_f32_32x32x16_f16 v[82:97], v[134:137], v[138:141], v[82:97]
	v_mfma_f32_32x32x16_f16 v[66:81], v[134:137], v[158:161], v[66:81]
	v_mfma_f32_32x32x16_f16 v[50:65], v[134:137], v[162:165], v[50:65]
	v_mfma_f32_32x32x16_f16 v[34:49], v[142:145], v[138:141], v[34:49]
	v_mfma_f32_32x32x16_f16 v[18:33], v[142:145], v[158:161], v[18:33]
	ds_read_b128 v[134:137], v113 offset:32768
	ds_read_b128 v[138:141], v113 offset:36864
	ds_read_b128 v[158:161], v128 offset:4096
	ds_read_b128 v[170:173], v128 offset:8192
	v_mfma_f32_32x32x16_f16 v[2:17], v[142:145], v[162:165], v[2:17]
	s_waitcnt lgkmcnt(0)
	v_mfma_f32_32x32x16_f16 v[82:97], v[134:137], v[166:169], v[82:97]
	v_mfma_f32_32x32x16_f16 v[66:81], v[134:137], v[158:161], v[66:81]
	v_mfma_f32_32x32x16_f16 v[50:65], v[134:137], v[170:173], v[50:65]
	v_mfma_f32_32x32x16_f16 v[34:49], v[138:141], v[166:169], v[34:49]
	v_mfma_f32_32x32x16_f16 v[18:33], v[138:141], v[158:161], v[18:33]
	ds_read_b128 v[134:137], v114 offset:32768
	ds_read_b128 v[142:145], v114 offset:36864
	ds_read_b128 v[158:161], v132
	ds_read_b128 v[162:165], v132 offset:4096
	ds_read_b128 v[166:169], v132 offset:8192
	v_mfma_f32_32x32x16_f16 v[2:17], v[138:141], v[170:173], v[2:17]
	s_waitcnt lgkmcnt(0)
	v_mfma_f32_32x32x16_f16 v[82:97], v[134:137], v[158:161], v[82:97]
	v_mfma_f32_32x32x16_f16 v[66:81], v[134:137], v[162:165], v[66:81]
	v_mfma_f32_32x32x16_f16 v[50:65], v[134:137], v[166:169], v[50:65]
	v_mfma_f32_32x32x16_f16 v[34:49], v[142:145], v[158:161], v[34:49]
	v_mfma_f32_32x32x16_f16 v[18:33], v[142:145], v[162:165], v[18:33]
	ds_read_b128 v[134:137], v115 offset:32768
	ds_read_b128 v[138:141], v115 offset:36864
	ds_read_b128 v[158:161], v133
	ds_read_b128 v[162:165], v133 offset:4096
	ds_read_b128 v[170:173], v133 offset:8192
	v_mfma_f32_32x32x16_f16 v[2:17], v[142:145], v[166:169], v[2:17]
	s_waitcnt lgkmcnt(0)
	v_mfma_f32_32x32x16_f16 v[82:97], v[134:137], v[158:161], v[82:97]
	v_mfma_f32_32x32x16_f16 v[66:81], v[134:137], v[162:165], v[66:81]
	v_mfma_f32_32x32x16_f16 v[50:65], v[134:137], v[170:173], v[50:65]
	v_mfma_f32_32x32x16_f16 v[34:49], v[138:141], v[158:161], v[34:49]
	v_mfma_f32_32x32x16_f16 v[18:33], v[138:141], v[162:165], v[18:33]
	v_mfma_f32_32x32x16_f16 v[2:17], v[138:141], v[170:173], v[2:17]
	s_mov_b64 s[34:35], 0x480
	s_mov_b32 m0, s30
	v_lshl_add_u64 v[134:135], v[98:99], 0, s[34:35]
	s_waitcnt vmcnt(0)
	s_waitcnt vmcnt(0)
	s_barrier
	global_load_lds_dwordx4 v[134:135], off
	v_lshl_add_u64 v[134:135], v[100:101], 0, s[34:35]
	s_mov_b32 m0, s23
	s_nop 0
	global_load_lds_dwordx4 v[134:135], off
	v_lshl_add_u64 v[134:135], v[102:103], 0, s[34:35]
	s_mov_b32 m0, s25
	s_nop 0
	global_load_lds_dwordx4 v[134:135], off
	v_lshl_add_u64 v[134:135], v[104:105], 0, s[34:35]
	s_mov_b32 m0, s26
	s_nop 0
	global_load_lds_dwordx4 v[134:135], off
	v_lshl_add_u64 v[134:135], v[106:107], 0, s[34:35]
	s_mov_b32 m0, s27
	s_nop 0
	global_load_lds_dwordx4 v[134:135], off
	v_lshl_add_u64 v[134:135], v[108:109], 0, s[34:35]
	s_mov_b32 m0, s28
	s_nop 0
	global_load_lds_dwordx4 v[134:135], off
	v_lshl_add_u64 v[134:135], v[110:111], 0, s[34:35]
	s_mov_b32 m0, s29
	s_nop 0
	global_load_lds_dwordx4 v[134:135], off
	ds_read_b128 v[134:137], v112
	ds_read_b128 v[138:141], v116
	ds_read_b128 v[142:145], v112 offset:4096
	ds_read_b128 v[158:161], v117
	ds_read_b128 v[162:165], v118
	ds_read_b128 v[166:169], v113
	s_waitcnt lgkmcnt(0)
	v_mfma_f32_32x32x16_f16 v[82:97], v[134:137], v[138:141], v[82:97]
	v_mfma_f32_32x32x16_f16 v[66:81], v[134:137], v[158:161], v[66:81]
	v_mfma_f32_32x32x16_f16 v[50:65], v[134:137], v[162:165], v[50:65]
	v_mfma_f32_32x32x16_f16 v[34:49], v[142:145], v[138:141], v[34:49]
	v_mfma_f32_32x32x16_f16 v[18:33], v[142:145], v[158:161], v[18:33]
	ds_read_b128 v[134:137], v113 offset:4096
	ds_read_b128 v[138:141], v119
	ds_read_b128 v[158:161], v120
	ds_read_b128 v[170:173], v121
	v_mfma_f32_32x32x16_f16 v[2:17], v[142:145], v[162:165], v[2:17]
	s_waitcnt lgkmcnt(0)
	v_mfma_f32_32x32x16_f16 v[82:97], v[166:169], v[138:141], v[82:97]
	v_mfma_f32_32x32x16_f16 v[66:81], v[166:169], v[158:161], v[66:81]
	v_mfma_f32_32x32x16_f16 v[50:65], v[166:169], v[170:173], v[50:65]
	v_mfma_f32_32x32x16_f16 v[34:49], v[134:137], v[138:141], v[34:49]
	v_mfma_f32_32x32x16_f16 v[18:33], v[134:137], v[158:161], v[18:33]
	ds_read_b128 v[138:141], v114
	ds_read_b128 v[142:145], v114 offset:4096
	ds_read_b128 v[158:161], v122
	ds_read_b128 v[162:165], v123
	ds_read_b128 v[166:169], v124
	v_mfma_f32_32x32x16_f16 v[2:17], v[134:137], v[170:173], v[2:17]
	s_waitcnt lgkmcnt(0)
	v_mfma_f32_32x32x16_f16 v[82:97], v[138:141], v[158:161], v[82:97]
	v_mfma_f32_32x32x16_f16 v[66:81], v[138:141], v[162:165], v[66:81]
	v_mfma_f32_32x32x16_f16 v[50:65], v[138:141], v[166:169], v[50:65]
	v_mfma_f32_32x32x16_f16 v[34:49], v[142:145], v[158:161], v[34:49]
	v_mfma_f32_32x32x16_f16 v[18:33], v[142:145], v[162:165], v[18:33]
	ds_read_b128 v[134:137], v115
	ds_read_b128 v[138:141], v115 offset:4096
	ds_read_b128 v[158:161], v125
	ds_read_b128 v[162:165], v126
	ds_read_b128 v[170:173], v127
	v_mfma_f32_32x32x16_f16 v[2:17], v[142:145], v[166:169], v[2:17]
	s_waitcnt lgkmcnt(0)
	v_mfma_f32_32x32x16_f16 v[82:97], v[134:137], v[158:161], v[82:97]
	v_mfma_f32_32x32x16_f16 v[66:81], v[134:137], v[162:165], v[66:81]
	v_mfma_f32_32x32x16_f16 v[50:65], v[134:137], v[170:173], v[50:65]
	v_mfma_f32_32x32x16_f16 v[34:49], v[138:141], v[158:161], v[34:49]
	v_mfma_f32_32x32x16_f16 v[18:33], v[138:141], v[162:165], v[18:33]
	v_mfma_f32_32x32x16_f16 v[2:17], v[138:141], v[170:173], v[2:17]
	s_mov_b64 s[34:35], 0x500
	s_mov_b32 m0, s24
	v_lshl_add_u64 v[134:135], v[98:99], 0, s[34:35]
	s_waitcnt vmcnt(0)
	s_waitcnt vmcnt(0)
	s_barrier
	global_load_lds_dwordx4 v[134:135], off
	v_lshl_add_u64 v[134:135], v[100:101], 0, s[34:35]
	s_mov_b32 m0, s16
	s_nop 0
	global_load_lds_dwordx4 v[134:135], off
	v_lshl_add_u64 v[134:135], v[102:103], 0, s[34:35]
	s_mov_b32 m0, s17
	s_nop 0
	global_load_lds_dwordx4 v[134:135], off
	v_lshl_add_u64 v[134:135], v[104:105], 0, s[34:35]
	s_mov_b32 m0, s18
	s_nop 0
	global_load_lds_dwordx4 v[134:135], off
	v_lshl_add_u64 v[134:135], v[106:107], 0, s[34:35]
	s_mov_b32 m0, s19
	s_nop 0
	global_load_lds_dwordx4 v[134:135], off
	v_lshl_add_u64 v[134:135], v[108:109], 0, s[34:35]
	s_mov_b32 m0, s21
	s_nop 0
	global_load_lds_dwordx4 v[134:135], off
	v_lshl_add_u64 v[134:135], v[110:111], 0, s[34:35]
	s_mov_b32 m0, s22
	s_nop 0
	global_load_lds_dwordx4 v[134:135], off
	ds_read_b128 v[134:137], v112 offset:32768
	ds_read_b128 v[138:141], v129
	ds_read_b128 v[142:145], v112 offset:36864
	ds_read_b128 v[158:161], v130
	ds_read_b128 v[162:165], v131
	ds_read_b128 v[166:169], v128
	s_waitcnt lgkmcnt(0)
	v_mfma_f32_32x32x16_f16 v[82:97], v[134:137], v[138:141], v[82:97]
	v_mfma_f32_32x32x16_f16 v[66:81], v[134:137], v[158:161], v[66:81]
	v_mfma_f32_32x32x16_f16 v[50:65], v[134:137], v[162:165], v[50:65]
	v_mfma_f32_32x32x16_f16 v[34:49], v[142:145], v[138:141], v[34:49]
	v_mfma_f32_32x32x16_f16 v[18:33], v[142:145], v[158:161], v[18:33]
	ds_read_b128 v[134:137], v113 offset:32768
	ds_read_b128 v[138:141], v113 offset:36864
	ds_read_b128 v[158:161], v128 offset:4096
	ds_read_b128 v[170:173], v128 offset:8192
	v_mfma_f32_32x32x16_f16 v[2:17], v[142:145], v[162:165], v[2:17]
	s_waitcnt lgkmcnt(0)
	v_mfma_f32_32x32x16_f16 v[82:97], v[134:137], v[166:169], v[82:97]
	v_mfma_f32_32x32x16_f16 v[66:81], v[134:137], v[158:161], v[66:81]
	v_mfma_f32_32x32x16_f16 v[50:65], v[134:137], v[170:173], v[50:65]
	v_mfma_f32_32x32x16_f16 v[34:49], v[138:141], v[166:169], v[34:49]
	v_mfma_f32_32x32x16_f16 v[18:33], v[138:141], v[158:161], v[18:33]
	ds_read_b128 v[134:137], v114 offset:32768
	ds_read_b128 v[142:145], v114 offset:36864
	ds_read_b128 v[158:161], v132
	ds_read_b128 v[162:165], v132 offset:4096
	ds_read_b128 v[166:169], v132 offset:8192
	v_mfma_f32_32x32x16_f16 v[2:17], v[138:141], v[170:173], v[2:17]
	s_waitcnt lgkmcnt(0)
	v_mfma_f32_32x32x16_f16 v[82:97], v[134:137], v[158:161], v[82:97]
	v_mfma_f32_32x32x16_f16 v[66:81], v[134:137], v[162:165], v[66:81]
	v_mfma_f32_32x32x16_f16 v[50:65], v[134:137], v[166:169], v[50:65]
	v_mfma_f32_32x32x16_f16 v[34:49], v[142:145], v[158:161], v[34:49]
	v_mfma_f32_32x32x16_f16 v[18:33], v[142:145], v[162:165], v[18:33]
	ds_read_b128 v[134:137], v115 offset:32768
	ds_read_b128 v[138:141], v115 offset:36864
	ds_read_b128 v[158:161], v133
	ds_read_b128 v[162:165], v133 offset:4096
	ds_read_b128 v[170:173], v133 offset:8192
	v_mfma_f32_32x32x16_f16 v[2:17], v[142:145], v[166:169], v[2:17]
	s_waitcnt lgkmcnt(0)
	v_mfma_f32_32x32x16_f16 v[82:97], v[134:137], v[158:161], v[82:97]
	v_mfma_f32_32x32x16_f16 v[66:81], v[134:137], v[162:165], v[66:81]
	v_mfma_f32_32x32x16_f16 v[50:65], v[134:137], v[170:173], v[50:65]
	v_mfma_f32_32x32x16_f16 v[34:49], v[138:141], v[158:161], v[34:49]
	v_mfma_f32_32x32x16_f16 v[18:33], v[138:141], v[162:165], v[18:33]
	v_mfma_f32_32x32x16_f16 v[2:17], v[138:141], v[170:173], v[2:17]
	s_mov_b64 s[16:17], 0x580
	s_mov_b32 m0, s30
	v_lshl_add_u64 v[98:99], v[98:99], 0, s[16:17]
	s_waitcnt vmcnt(0)
	s_waitcnt vmcnt(0)
	s_barrier
	global_load_lds_dwordx4 v[98:99], off
	v_lshl_add_u64 v[98:99], v[100:101], 0, s[16:17]
	s_mov_b32 m0, s23
	s_nop 0
	global_load_lds_dwordx4 v[98:99], off
	v_lshl_add_u64 v[98:99], v[102:103], 0, s[16:17]
	s_mov_b32 m0, s25
	s_nop 0
	global_load_lds_dwordx4 v[98:99], off
	v_lshl_add_u64 v[98:99], v[104:105], 0, s[16:17]
	s_mov_b32 m0, s26
	s_nop 0
	global_load_lds_dwordx4 v[98:99], off
	v_lshl_add_u64 v[98:99], v[106:107], 0, s[16:17]
	s_mov_b32 m0, s27
	s_nop 0
	global_load_lds_dwordx4 v[98:99], off
	v_lshl_add_u64 v[98:99], v[108:109], 0, s[16:17]
	s_mov_b32 m0, s28
	s_nop 0
	global_load_lds_dwordx4 v[98:99], off
	v_lshl_add_u64 v[98:99], v[110:111], 0, s[16:17]
	s_mov_b32 m0, s29
	s_nop 0
	global_load_lds_dwordx4 v[98:99], off
	ds_read_b128 v[98:101], v112
	ds_read_b128 v[102:105], v116
	ds_read_b128 v[106:109], v112 offset:4096
	ds_read_b128 v[134:137], v117
	ds_read_b128 v[138:141], v118
	ds_read_b128 v[142:145], v113
	s_waitcnt lgkmcnt(0)
	v_mfma_f32_32x32x16_f16 v[82:97], v[98:101], v[102:105], v[82:97]
	v_mfma_f32_32x32x16_f16 v[66:81], v[98:101], v[134:137], v[66:81]
	v_mfma_f32_32x32x16_f16 v[50:65], v[98:101], v[138:141], v[50:65]
	v_mfma_f32_32x32x16_f16 v[34:49], v[106:109], v[102:105], v[34:49]
	v_mfma_f32_32x32x16_f16 v[18:33], v[106:109], v[134:137], v[18:33]
	ds_read_b128 v[98:101], v113 offset:4096
	ds_read_b128 v[102:105], v119
	ds_read_b128 v[116:119], v120
	ds_read_b128 v[134:137], v121
	v_mfma_f32_32x32x16_f16 v[2:17], v[106:109], v[138:141], v[2:17]
	s_waitcnt lgkmcnt(0)
	v_mfma_f32_32x32x16_f16 v[82:97], v[142:145], v[102:105], v[82:97]
	v_mfma_f32_32x32x16_f16 v[66:81], v[142:145], v[116:119], v[66:81]
	v_mfma_f32_32x32x16_f16 v[50:65], v[142:145], v[134:137], v[50:65]
	v_mfma_f32_32x32x16_f16 v[34:49], v[98:101], v[102:105], v[34:49]
	v_mfma_f32_32x32x16_f16 v[18:33], v[98:101], v[116:119], v[18:33]
	ds_read_b128 v[102:105], v114
	ds_read_b128 v[106:109], v114 offset:4096
	ds_read_b128 v[116:119], v122
	ds_read_b128 v[120:123], v123
	ds_read_b128 v[138:141], v124
	v_mfma_f32_32x32x16_f16 v[2:17], v[98:101], v[134:137], v[2:17]
	s_waitcnt lgkmcnt(0)
	v_mfma_f32_32x32x16_f16 v[82:97], v[102:105], v[116:119], v[82:97]
	v_mfma_f32_32x32x16_f16 v[66:81], v[102:105], v[120:123], v[66:81]
	v_mfma_f32_32x32x16_f16 v[50:65], v[102:105], v[138:141], v[50:65]
	v_mfma_f32_32x32x16_f16 v[34:49], v[106:109], v[116:119], v[34:49]
	v_mfma_f32_32x32x16_f16 v[18:33], v[106:109], v[120:123], v[18:33]
	ds_read_b128 v[98:101], v115
	ds_read_b128 v[102:105], v115 offset:4096
	ds_read_b128 v[116:119], v125
	ds_read_b128 v[120:123], v126
	ds_read_b128 v[124:127], v127
	v_mfma_f32_32x32x16_f16 v[2:17], v[106:109], v[138:141], v[2:17]
	s_waitcnt lgkmcnt(0)
	v_mfma_f32_32x32x16_f16 v[82:97], v[98:101], v[116:119], v[82:97]
	v_mfma_f32_32x32x16_f16 v[66:81], v[98:101], v[120:123], v[66:81]
	v_mfma_f32_32x32x16_f16 v[50:65], v[98:101], v[124:127], v[50:65]
	v_mfma_f32_32x32x16_f16 v[34:49], v[102:105], v[116:119], v[34:49]
	v_mfma_f32_32x32x16_f16 v[18:33], v[102:105], v[120:123], v[18:33]
	v_mfma_f32_32x32x16_f16 v[2:17], v[102:105], v[124:127], v[2:17]
	s_waitcnt vmcnt(0)
	s_waitcnt vmcnt(0)
	s_barrier
	ds_read_b128 v[98:101], v112 offset:32768
	ds_read_b128 v[102:105], v129
	ds_read_b128 v[106:109], v112 offset:36864
	ds_read_b128 v[116:119], v130
	ds_read_b128 v[120:123], v131
	ds_read_b128 v[124:127], v128
	s_waitcnt lgkmcnt(4)
	v_mfma_f32_32x32x16_f16 v[82:97], v[98:101], v[102:105], v[82:97]
	s_waitcnt lgkmcnt(2)
	v_mfma_f32_32x32x16_f16 v[66:81], v[98:101], v[116:119], v[66:81]
	s_waitcnt lgkmcnt(1)
	v_mfma_f32_32x32x16_f16 v[50:65], v[98:101], v[120:123], v[50:65]
	v_mfma_f32_32x32x16_f16 v[34:49], v[106:109], v[102:105], v[34:49]
	v_mfma_f32_32x32x16_f16 v[18:33], v[106:109], v[116:119], v[18:33]
	ds_read_b128 v[98:101], v113 offset:32768
	ds_read_b128 v[102:105], v113 offset:36864
	ds_read_b128 v[110:113], v128 offset:4096
	ds_read_b128 v[116:119], v128 offset:8192
	v_mfma_f32_32x32x16_f16 v[2:17], v[106:109], v[120:123], v[2:17]
	s_waitcnt lgkmcnt(3)
	v_mfma_f32_32x32x16_f16 v[82:97], v[98:101], v[124:127], v[82:97]
	s_waitcnt lgkmcnt(1)
	v_mfma_f32_32x32x16_f16 v[66:81], v[98:101], v[110:113], v[66:81]
	s_waitcnt lgkmcnt(0)
	v_mfma_f32_32x32x16_f16 v[50:65], v[98:101], v[116:119], v[50:65]
	v_mfma_f32_32x32x16_f16 v[34:49], v[102:105], v[124:127], v[34:49]
	v_mfma_f32_32x32x16_f16 v[18:33], v[102:105], v[110:113], v[18:33]
	ds_read_b128 v[98:101], v114 offset:32768
	ds_read_b128 v[106:109], v114 offset:36864
	ds_read_b128 v[110:113], v132
	ds_read_b128 v[120:123], v132 offset:4096
	ds_read_b128 v[124:127], v132 offset:8192
	v_mfma_f32_32x32x16_f16 v[2:17], v[102:105], v[116:119], v[2:17]
	s_waitcnt lgkmcnt(2)
	v_mfma_f32_32x32x16_f16 v[82:97], v[98:101], v[110:113], v[82:97]
	s_waitcnt lgkmcnt(1)
	v_mfma_f32_32x32x16_f16 v[66:81], v[98:101], v[120:123], v[66:81]
	s_waitcnt lgkmcnt(0)
	v_mfma_f32_32x32x16_f16 v[50:65], v[98:101], v[124:127], v[50:65]
	v_mfma_f32_32x32x16_f16 v[34:49], v[106:109], v[110:113], v[34:49]
	v_mfma_f32_32x32x16_f16 v[18:33], v[106:109], v[120:123], v[18:33]
	ds_read_b128 v[98:101], v115 offset:32768
	ds_read_b128 v[102:105], v115 offset:36864
	ds_read_b128 v[110:113], v133
	ds_read_b128 v[114:117], v133 offset:4096
	ds_read_b128 v[118:121], v133 offset:8192
	v_mfma_f32_32x32x16_f16 v[2:17], v[106:109], v[124:127], v[2:17]
	s_waitcnt lgkmcnt(2)
	v_mfma_f32_32x32x16_f16 v[82:97], v[98:101], v[110:113], v[82:97]
	s_waitcnt lgkmcnt(1)
	v_mfma_f32_32x32x16_f16 v[66:81], v[98:101], v[114:117], v[66:81]
	s_waitcnt lgkmcnt(0)
	v_mfma_f32_32x32x16_f16 v[50:65], v[98:101], v[118:121], v[50:65]
	v_mfma_f32_32x32x16_f16 v[34:49], v[102:105], v[110:113], v[34:49]
	v_mfma_f32_32x32x16_f16 v[18:33], v[102:105], v[114:117], v[18:33]
	v_mfma_f32_32x32x16_f16 v[2:17], v[102:105], v[118:121], v[2:17]
	v_add_u32_e32 v158, s20, v151
	v_and_b32_e32 v154, 32, v0
	v_mov_b32_e32 v155, v147
	v_lshl_add_u64 v[98:99], s[6:7], 0, v[154:155]
	v_or_b32_e32 v100, v158, v156
	v_lshlrev_b32_e32 v146, 2, v158
	v_lshlrev_b32_e32 v100, 2, v100
	v_lshl_add_u64 v[102:103], v[98:99], 0, v[146:147]
	s_waitcnt vmcnt(0)
	s_barrier
	global_load_dwordx4 v[138:141], v[102:103], off offset:16
	global_load_dwordx4 v[134:137], v[102:103], off offset:64
	global_load_dwordx4 v[130:133], v[102:103], off offset:80
	global_load_dwordx4 v[126:129], v[102:103], off offset:128
	global_load_dwordx4 v[122:125], v[102:103], off offset:144
	global_load_dwordx4 v[118:121], v[102:103], off offset:192
	global_load_dword v152, v100, s[6:7]
	global_load_dwordx4 v[142:145], v[102:103], off
	global_load_dword v150, v100, s[6:7] offset:128
	global_load_dword v148, v100, s[6:7] offset:256
	global_load_dwordx4 v[114:117], v[102:103], off offset:208
	global_load_dwordx4 v[110:113], v[102:103], off offset:256
	s_nop 0
	global_load_dwordx4 v[98:101], v[102:103], off offset:336
	global_load_dwordx4 v[106:109], v[102:103], off offset:272
	s_nop 0
	global_load_dwordx4 v[102:105], v[102:103], off offset:320
	v_mul_u32_u24_e32 v146, 0x1200, v149
	v_mov_b32_e32 v155, 0x1c0
	s_movk_i32 s18, 0x1200
	v_lshl_or_b32 v146, v156, 2, v146
	s_bfe_u32 s6, s3, 0x30009
	v_bitop3_b32 v155, s3, v155, v157 bitop3:0xc8
	v_mul_u32_u24_e32 v156, 0x90, v156
	s_movk_i32 s3, 0x240
	v_mad_u32_u24 v156, v149, s18, v156
	v_mad_u32_u24 v149, v153, s3, v146
	v_mul_u32_u24_e64 v157, s6, 12
	s_cmpk_gt_u32 s2, 0x7f
	ds_write2_b32 v149, v82, v83 offset1:36
	ds_write2_b32 v149, v84, v85 offset0:72 offset1:108
	v_add_u32_e32 v153, 0x400, v149
	v_lshrrev_b32_e32 v83, 6, v158
	s_cselect_b64 s[16:17], -1, 0
	s_and_b64 s[6:7], s[4:5], exec
	ds_write2_b32 v153, v86, v87 offset0:32 offset1:68
	ds_write2_b32 v153, v88, v89 offset0:104 offset1:140
	v_add_u32_e32 v86, 0x800, v149
	v_and_b32_e32 v89, 32, v151
	v_add_lshl_u32 v146, v83, v157, 15
	s_cselect_b32 s7, s11, s13
	s_cselect_b32 s6, s10, s12
	v_mov_b32_e32 v159, 0x3e000000
	ds_write2_b32 v86, v90, v91 offset0:64 offset1:100
	ds_write2_b32 v86, v92, v93 offset0:136 offset1:172
	v_add_u32_e32 v82, 0xc00, v149
	s_mov_b64 s[10:11], -1
	s_and_b64 vcc, exec, s[16:17]
	v_lshl_add_u64 v[84:85], v[146:147], 1, s[14:15]
	v_lshlrev_b32_e32 v83, 1, v89
	v_lshlrev_b32_e32 v91, 3, v155
	ds_write2_b32 v82, v94, v95 offset0:96 offset1:132
	ds_write2_b32 v82, v96, v97 offset0:168 offset1:204
	s_cbranch_vccz .LBB11_3
	ds_read2_b32 v[92:93], v149 offset1:36
	ds_read2_b32 v[94:95], v149 offset0:72 offset1:108
	ds_read2_b32 v[96:97], v153 offset0:32 offset1:68
	ds_read2_b32 v[160:161], v153 offset0:104 offset1:140
	s_mov_b64 s[10:11], 0
	s_waitcnt vmcnt(8) lgkmcnt(3)
	v_add_f32_e32 v87, v152, v92
	v_cvt_f16_f32_e32 v87, v87
	v_mov_b32_e32 v92, v93
	s_waitcnt lgkmcnt(2)
	v_mov_b32_e32 v93, v94
	v_mov_b32_e32 v94, v95
	v_pk_add_f32 v[92:93], v[152:153], v[92:93] op_sel_hi:[0,1]
	s_waitcnt lgkmcnt(1)
	v_mov_b32_e32 v95, v96
	v_cvt_pk_f16_f32 v88, v92, v93
	v_pk_add_f32 v[94:95], v[152:153], v[94:95] op_sel_hi:[0,1]
	v_pack_b32_f16 v92, v87, v88
	v_cvt_pk_f16_f32 v87, v94, v95
	v_mov_b32_e32 v94, v97
	s_waitcnt lgkmcnt(0)
	v_mov_b32_e32 v95, v160
	v_alignbit_b32 v93, v87, v88, 16
	v_add_f32_e32 v88, v152, v161
	v_pk_add_f32 v[94:95], v[152:153], v[94:95] op_sel_hi:[0,1]
	v_cvt_f16_f32_e32 v88, v88
	v_cvt_pk_f16_f32 v90, v94, v95
	ds_read2_b32 v[160:161], v86 offset0:64 offset1:100
	v_alignbit_b32 v94, v90, v87, 16
	v_or3_b32 v87, v83, v91, v1
	v_lshlrev_b32_e32 v96, 4, v87
	ds_read2_b32 v[86:87], v86 offset0:136 offset1:172
	v_mov_b32_e32 v97, v147
	v_alignbit_b32 v95, v88, v90, 16
	v_lshl_add_u64 v[162:163], v[84:85], 0, v[96:97]
	global_store_dwordx4 v[162:163], v[92:95], off sc1
	s_waitcnt lgkmcnt(1)
	v_add_f32_e32 v88, v152, v160
	ds_read2_b32 v[94:95], v82 offset0:96 offset1:132
	v_mov_b32_e32 v92, v161
	ds_read2_b32 v[160:161], v82 offset0:168 offset1:204
	v_cvt_f16_f32_e32 v88, v88
	s_waitcnt lgkmcnt(2)
	v_mov_b32_e32 v93, v86
	v_pk_add_f32 v[92:93], v[152:153], v[92:93] op_sel_hi:[0,1]
	v_cvt_pk_f16_f32 v90, v92, v93
	v_pack_b32_f16 v92, v88, v90
	v_mov_b32_e32 v86, v87
	s_waitcnt lgkmcnt(1)
	v_mov_b32_e32 v87, v94
	s_waitcnt lgkmcnt(0)
	v_add_f32_e32 v88, v152, v161
	v_pk_add_f32 v[86:87], v[152:153], v[86:87] op_sel_hi:[0,1]
	v_cvt_f16_f32_e32 v88, v88
	v_cvt_pk_f16_f32 v82, v86, v87
	v_mov_b32_e32 v86, v95
	v_mov_b32_e32 v87, v160
	v_pk_add_f32 v[86:87], v[152:153], v[86:87] op_sel_hi:[0,1]
	v_cvt_pk_f16_f32 v86, v86, v87
	v_alignbit_b32 v94, v86, v82, 16
	v_alignbit_b32 v95, v88, v86, 16
	v_or_b32_e32 v86, 0x800, v96
	v_mov_b32_e32 v87, v147
	v_alignbit_b32 v93, v82, v90, 16
	v_lshl_add_u64 v[86:87], v[84:85], 0, v[86:87]
	global_store_dwordx4 v[86:87], v[92:95], off sc1

	.amdhsa_kernel _Z7gemm2_kILi0ELi3ELi1EEv5GArgs
		.amdhsa_group_segment_fixed_size 114688
		.amdhsa_private_segment_fixed_size 0
		.amdhsa_kernarg_size 136
		.amdhsa_user_sgpr_count 2
		.amdhsa_user_sgpr_dispatch_ptr 0
		.amdhsa_user_sgpr_queue_ptr 0
		.amdhsa_user_sgpr_kernarg_segment_ptr 1
		.amdhsa_user_sgpr_dispatch_id 0
		.amdhsa_user_sgpr_kernarg_preload_length 0
		.amdhsa_user_sgpr_kernarg_preload_offset 0
		.amdhsa_user_sgpr_private_segment_size 0
		.amdhsa_uses_dynamic_stack 0
		.amdhsa_enable_private_segment 0
		.amdhsa_system_sgpr_workgroup_id_x 1
		.amdhsa_system_sgpr_workgroup_id_y 0
		.amdhsa_system_sgpr_workgroup_id_z 0
		.amdhsa_system_sgpr_workgroup_info 0
		.amdhsa_system_vgpr_workitem_id 0
		.amdhsa_next_free_vgpr 188
		.amdhsa_next_free_sgpr 96
		.amdhsa_accum_offset 188
		.amdhsa_reserve_vcc 1
		.amdhsa_float_round_mode_32 0
		.amdhsa_float_round_mode_16_64 0
		.amdhsa_float_denorm_mode_32 3
		.amdhsa_float_denorm_mode_16_64 3
		.amdhsa_dx10_clamp 1
		.amdhsa_ieee_mode 1
		.amdhsa_fp16_overflow 0
		.amdhsa_tg_split 0
		.amdhsa_exception_fp_ieee_invalid_op 0
		.amdhsa_exception_fp_denorm_src 0
		.amdhsa_exception_fp_ieee_div_zero 0
		.amdhsa_exception_fp_ieee_overflow 0
		.amdhsa_exception_fp_ieee_underflow 0
		.amdhsa_exception_fp_ieee_inexact 0
		.amdhsa_exception_int_div_zero 0
	.end_amdhsa_kernel

_Z6gemm_kILi1ELi128ELi4ELi8EEv5GArgs:
	v_lshlrev_b32_e32 v74, 4, v0
	s_getpc_b64 s[92:93]
	s_add_u32 s92, s92, 0xffff2af8
	s_addc_u32 s93, s93, 0xffffffff
	global_load_dword v75, v74, s[92:93]
	s_cmpk_lt_u32 s2, 0xc0
	s_mov_b64 s[4:5], -1
	s_cbranch_scc0 .LBB12_2
	s_load_dwordx4 s[4:7], s[0:1], 0x0
	v_lshrrev_b32_e32 v44, 6, v0
	s_lshl_b32 s3, s2, 7
	v_bfe_u32 v1, v0, 3, 3
	s_and_b32 s3, s3, 0xf80
	v_lshl_or_b32 v6, v44, 4, v1
	v_and_b32_e32 v2, 7, v0
	v_bitop3_b32 v4, v44, v2, 1 bitop3:0x6c
	v_or_b32_e32 v2, s3, v6
	v_mul_u32_u24_e32 v2, 0x340, v2
	v_bfe_u32 v5, v0, 4, 2
	v_lshlrev_b32_e32 v34, 1, v2
	v_mov_b32_e32 v35, 0
	v_xor_b32_e32 v5, v4, v5
	s_waitcnt lgkmcnt(0)
	v_lshl_add_u64 v[2:3], s[4:5], 0, v[34:35]
	v_lshlrev_b32_e32 v34, 4, v5
	v_or_b32_e32 v7, 8, v6
	v_lshl_add_u64 v[36:37], v[2:3], 0, v[34:35]
	v_or_b32_e32 v2, s3, v7
	v_bfe_u32 v5, v7, 1, 3
	s_lshl_b32 s8, s2, 2
	v_mul_u32_u24_e32 v2, 0x340, v2
	v_mov_b32_e32 v3, v35
	v_xor_b32_e32 v4, v4, v5
	v_lshl_add_u64 v[2:3], v[2:3], 1, s[4:5]
	v_lshlrev_b32_e32 v4, 4, v4
	v_mov_b32_e32 v5, v35
	s_and_b32 s10, s8, 0x380
	v_lshl_add_u64 v[38:39], v[2:3], 0, v[4:5]
	v_or_b32_e32 v2, s10, v6
	v_mul_u32_u24_e32 v2, 0x680, v2
	v_mov_b32_e32 v3, v35
	v_lshl_add_u64 v[2:3], s[6:7], 0, v[2:3]
	v_lshl_add_u64 v[40:41], v[2:3], 0, v[34:35]
	v_or_b32_e32 v2, s10, v7
	v_mul_u32_u24_e32 v34, 0x680, v2
	v_lshl_add_u64 v[2:3], s[6:7], 0, v[34:35]
	v_lshl_add_u64 v[42:43], v[2:3], 0, v[4:5]
	v_lshlrev_b32_e32 v4, 11, v44
	v_or_b32_e32 v2, 0x400, v4
	v_readfirstlane_b32 s19, v4
	s_mov_b32 m0, s19
	v_readfirstlane_b32 s20, v2
	v_or_b32_e32 v2, 0x10000, v4
	global_load_lds_dwordx4 v[36:37], off
	s_mov_b32 m0, s20
	v_readfirstlane_b32 s21, v2
	v_or_b32_e32 v2, 0x10400, v4
	global_load_lds_dwordx4 v[38:39], off
	s_mov_b32 m0, s21
	v_readfirstlane_b32 s22, v2
	v_or_b32_e32 v5, 0x4000, v4
	global_load_lds_dwordx4 v[40:41], off
	s_mov_b32 m0, s22
	s_mov_b64 s[4:5], 0x80
	v_readfirstlane_b32 s15, v5
	v_or_b32_e32 v5, 0x4400, v4
	global_load_lds_dwordx4 v[42:43], off
	v_lshl_add_u64 v[2:3], v[36:37], 0, s[4:5]
	s_mov_b32 m0, s15
	v_readfirstlane_b32 s16, v5
	v_or_b32_e32 v5, 0x14000, v4
	global_load_lds_dwordx4 v[2:3], off
	v_lshl_add_u64 v[2:3], v[38:39], 0, s[4:5]
	s_mov_b32 m0, s16
	v_readfirstlane_b32 s17, v5
	v_or_b32_e32 v5, 0x14400, v4
	global_load_lds_dwordx4 v[2:3], off
	v_lshl_add_u64 v[2:3], v[40:41], 0, s[4:5]
	s_mov_b32 m0, s17
	v_readfirstlane_b32 s18, v5
	v_or_b32_e32 v5, 0x8000, v4
	global_load_lds_dwordx4 v[2:3], off
	v_lshl_add_u64 v[2:3], v[42:43], 0, s[4:5]
	s_mov_b32 m0, s18
	s_mov_b64 s[4:5], 0x100
	v_readfirstlane_b32 s11, v5
	v_or_b32_e32 v5, 0x8400, v4
	global_load_lds_dwordx4 v[2:3], off
	v_lshl_add_u64 v[2:3], v[36:37], 0, s[4:5]
	s_mov_b32 m0, s11
	v_readfirstlane_b32 s12, v5
	v_or_b32_e32 v5, 0x18000, v4
	global_load_lds_dwordx4 v[2:3], off
	v_lshl_add_u64 v[2:3], v[38:39], 0, s[4:5]
	s_mov_b32 m0, s12
	v_readfirstlane_b32 s13, v5
	v_or_b32_e32 v5, 0x18400, v4
	global_load_lds_dwordx4 v[2:3], off
	v_lshl_add_u64 v[2:3], v[40:41], 0, s[4:5]
	s_mov_b32 m0, s13
	v_readfirstlane_b32 s14, v5
	v_or_b32_e32 v5, 0xc000, v4
	global_load_lds_dwordx4 v[2:3], off
	v_lshl_add_u64 v[2:3], v[42:43], 0, s[4:5]
	s_mov_b32 m0, s14
	s_mov_b64 s[4:5], 0x180
	v_readfirstlane_b32 s25, v5
	v_or_b32_e32 v5, 0xc400, v4
	global_load_lds_dwordx4 v[2:3], off
	v_lshl_add_u64 v[2:3], v[36:37], 0, s[4:5]
	s_mov_b32 m0, s25
	v_readfirstlane_b32 s23, v5
	v_or_b32_e32 v5, 0x1c000, v4
	s_waitcnt vmcnt(8)
	s_waitcnt vmcnt(0) lgkmcnt(0)
	s_barrier
	global_load_lds_dwordx4 v[2:3], off
	v_lshl_add_u64 v[2:3], v[38:39], 0, s[4:5]
	s_mov_b32 m0, s23
	v_readfirstlane_b32 s24, v5
	v_or_b32_e32 v4, 0x1c400, v4
	global_load_lds_dwordx4 v[2:3], off
	v_lshl_add_u64 v[2:3], v[40:41], 0, s[4:5]
	s_mov_b32 m0, s24
	v_readfirstlane_b32 s26, v4
	global_load_lds_dwordx4 v[2:3], off
	v_lshl_add_u64 v[2:3], v[42:43], 0, s[4:5]
	s_mov_b32 m0, s26
	v_bfe_u32 v46, v0, 5, 1
	global_load_lds_dwordx4 v[2:3], off
	v_lshrrev_b32_e32 v2, 1, v0
	v_bfe_u32 v3, v0, 4, 1
	v_bitop3_b32 v2, v2, v3, 7 bitop3:0x6c
	v_or_b32_e32 v3, 6, v46
	s_load_dwordx2 s[8:9], s[0:1], 0x18
	s_load_dwordx2 s[6:7], s[0:1], 0x30
	s_load_dwordx2 s[4:5], s[0:1], 0x48
	v_xor_b32_e32 v3, v2, v3
	v_lshlrev_b32_e32 v72, 4, v3
	v_or_b32_e32 v3, 4, v46
	v_xor_b32_e32 v3, v2, v3
	v_lshlrev_b32_e32 v62, 4, v3
	v_or_b32_e32 v3, 2, v46
	v_and_b32_e32 v47, 31, v0
	v_xor_b32_e32 v3, v2, v3
	v_xor_b32_e32 v2, v2, v46
	v_bfe_u32 v45, v0, 6, 2
	v_lshrrev_b32_e32 v34, 8, v0
	s_mov_b32 s27, 0x10000
	v_lshlrev_b32_e32 v50, 7, v47
	v_lshlrev_b32_e32 v6, 4, v2
	v_lshlrev_b32_e32 v2, 12, v45
	v_lshlrev_b32_e32 v68, 13, v34
	v_lshlrev_b32_e32 v52, 4, v3
	v_or3_b32 v73, v2, v50, s27
	v_or3_b32 v49, v6, v68, v50
	ds_read_b128 v[2:5], v49
	v_or_b32_e32 v51, v73, v6
	ds_read_b128 v[6:9], v51
	v_or_b32_e32 v14, v52, v68
	v_add_u32_e32 v48, v14, v50
	ds_read_b128 v[54:57], v48
	v_or_b32_e32 v53, v73, v52
	ds_read_b128 v[10:13], v49 offset:4096
	ds_read_b128 v[58:61], v53
	s_waitcnt lgkmcnt(0)
	v_mfma_f32_32x32x16_f16 v[18:33], v[2:5], v[6:9], 0
	v_or_b32_e32 v52, v62, v68
	v_add_u32_e32 v52, v52, v50
	v_mfma_f32_32x32x16_f16 v[18:33], v[54:57], v[58:61], v[18:33]
	ds_read_b128 v[54:57], v48 offset:4096
	v_mfma_f32_32x32x16_f16 v[2:17], v[10:13], v[6:9], 0
	s_waitcnt lgkmcnt(0)
	v_mfma_f32_32x32x16_f16 v[2:17], v[54:57], v[58:61], v[2:17]
	ds_read_b128 v[56:59], v52
	v_or_b32_e32 v54, v73, v62
	ds_read_b128 v[60:63], v54
	ds_read_b128 v[64:67], v52 offset:4096
	v_or_b32_e32 v55, v72, v68
	v_add_u32_e32 v50, v55, v50
	ds_read_b128 v[68:71], v50
	v_or_b32_e32 v55, v73, v72
	s_waitcnt lgkmcnt(0)
	v_mfma_f32_32x32x16_f16 v[18:33], v[56:59], v[60:63], v[18:33]
	ds_read_b128 v[56:59], v55
	v_mfma_f32_32x32x16_f16 v[2:17], v[64:67], v[60:63], v[2:17]
	ds_read_b128 v[60:63], v50 offset:4096
	s_waitcnt lgkmcnt(0)
	v_mfma_f32_32x32x16_f16 v[18:33], v[68:71], v[56:59], v[18:33]
	v_mfma_f32_32x32x16_f16 v[2:17], v[60:63], v[56:59], v[2:17]
	s_mov_b64 s[28:29], 0x200
	s_mov_b32 m0, s19
	v_lshl_add_u64 v[56:57], v[36:37], 0, s[28:29]
	s_waitcnt vmcnt(8)
	s_barrier
	global_load_lds_dwordx4 v[56:57], off
	v_lshl_add_u64 v[56:57], v[38:39], 0, s[28:29]
	s_mov_b32 m0, s20
	s_nop 0
	global_load_lds_dwordx4 v[56:57], off
	v_lshl_add_u64 v[56:57], v[40:41], 0, s[28:29]
	s_mov_b32 m0, s21
	s_nop 0
	global_load_lds_dwordx4 v[56:57], off
	v_lshl_add_u64 v[56:57], v[42:43], 0, s[28:29]
	s_mov_b32 m0, s22
	s_nop 0
	global_load_lds_dwordx4 v[56:57], off
	ds_read_b128 v[56:59], v49 offset:16384
	ds_read_b128 v[60:63], v51 offset:16384
	ds_read_b128 v[64:67], v49 offset:20480
	ds_read_b128 v[68:71], v48 offset:16384
	s_waitcnt lgkmcnt(0)
	v_mfma_f32_32x32x16_f16 v[18:33], v[56:59], v[60:63], v[18:33]
	ds_read_b128 v[56:59], v53 offset:16384
	v_mfma_f32_32x32x16_f16 v[2:17], v[64:67], v[60:63], v[2:17]
	ds_read_b128 v[60:63], v48 offset:20480
	s_waitcnt lgkmcnt(0)
	v_mfma_f32_32x32x16_f16 v[18:33], v[68:71], v[56:59], v[18:33]
	v_mfma_f32_32x32x16_f16 v[2:17], v[60:63], v[56:59], v[2:17]
	ds_read_b128 v[56:59], v52 offset:16384
	ds_read_b128 v[60:63], v54 offset:16384
	ds_read_b128 v[64:67], v52 offset:20480
	ds_read_b128 v[68:71], v50 offset:16384
	s_waitcnt lgkmcnt(0)
	v_mfma_f32_32x32x16_f16 v[18:33], v[56:59], v[60:63], v[18:33]
	ds_read_b128 v[56:59], v55 offset:16384
	v_mfma_f32_32x32x16_f16 v[2:17], v[64:67], v[60:63], v[2:17]
	ds_read_b128 v[60:63], v50 offset:20480
	s_waitcnt lgkmcnt(0)
	v_mfma_f32_32x32x16_f16 v[18:33], v[68:71], v[56:59], v[18:33]
	v_mfma_f32_32x32x16_f16 v[2:17], v[60:63], v[56:59], v[2:17]
	s_mov_b64 s[28:29], 0x280
	s_mov_b32 m0, s15
	v_lshl_add_u64 v[56:57], v[36:37], 0, s[28:29]
	s_waitcnt vmcnt(8)
	s_barrier
	global_load_lds_dwordx4 v[56:57], off
	v_lshl_add_u64 v[56:57], v[38:39], 0, s[28:29]
	s_mov_b32 m0, s16
	s_nop 0
	global_load_lds_dwordx4 v[56:57], off
	v_lshl_add_u64 v[56:57], v[40:41], 0, s[28:29]
	s_mov_b32 m0, s17
	s_nop 0
	global_load_lds_dwordx4 v[56:57], off
	v_lshl_add_u64 v[56:57], v[42:43], 0, s[28:29]
	s_mov_b32 m0, s18
	s_nop 0
	global_load_lds_dwordx4 v[56:57], off
	ds_read_b128 v[56:59], v49 offset:32768
	ds_read_b128 v[60:63], v51 offset:32768
	ds_read_b128 v[64:67], v49 offset:36864
	ds_read_b128 v[68:71], v48 offset:32768
	s_waitcnt lgkmcnt(0)
	v_mfma_f32_32x32x16_f16 v[18:33], v[56:59], v[60:63], v[18:33]
	ds_read_b128 v[56:59], v53 offset:32768
	v_mfma_f32_32x32x16_f16 v[2:17], v[64:67], v[60:63], v[2:17]
	ds_read_b128 v[60:63], v48 offset:36864
	s_waitcnt lgkmcnt(0)
	v_mfma_f32_32x32x16_f16 v[18:33], v[68:71], v[56:59], v[18:33]
	v_mfma_f32_32x32x16_f16 v[2:17], v[60:63], v[56:59], v[2:17]
	ds_read_b128 v[56:59], v52 offset:32768
	ds_read_b128 v[60:63], v54 offset:32768
	ds_read_b128 v[64:67], v52 offset:36864
	ds_read_b128 v[68:71], v50 offset:32768
	s_waitcnt lgkmcnt(0)
	v_mfma_f32_32x32x16_f16 v[18:33], v[56:59], v[60:63], v[18:33]
	ds_read_b128 v[56:59], v55 offset:32768
	v_mfma_f32_32x32x16_f16 v[2:17], v[64:67], v[60:63], v[2:17]
	ds_read_b128 v[60:63], v50 offset:36864
	s_waitcnt lgkmcnt(0)
	v_mfma_f32_32x32x16_f16 v[18:33], v[68:71], v[56:59], v[18:33]
	v_mfma_f32_32x32x16_f16 v[2:17], v[60:63], v[56:59], v[2:17]
	s_mov_b64 s[28:29], 0x300
	s_mov_b32 m0, s11
	v_lshl_add_u64 v[56:57], v[36:37], 0, s[28:29]
	s_waitcnt vmcnt(8)
	s_barrier
	global_load_lds_dwordx4 v[56:57], off
	v_lshl_add_u64 v[56:57], v[38:39], 0, s[28:29]
	s_mov_b32 m0, s12
	s_nop 0
	global_load_lds_dwordx4 v[56:57], off
	v_lshl_add_u64 v[56:57], v[40:41], 0, s[28:29]
	s_mov_b32 m0, s13
	s_nop 0
	global_load_lds_dwordx4 v[56:57], off
	v_lshl_add_u64 v[56:57], v[42:43], 0, s[28:29]
	s_mov_b32 m0, s14
	s_nop 0
	global_load_lds_dwordx4 v[56:57], off
	ds_read_b128 v[56:59], v49 offset:49152
	ds_read_b128 v[60:63], v51 offset:49152
	ds_read_b128 v[64:67], v49 offset:53248
	ds_read_b128 v[68:71], v48 offset:49152
	s_waitcnt lgkmcnt(0)
	v_mfma_f32_32x32x16_f16 v[18:33], v[56:59], v[60:63], v[18:33]
	ds_read_b128 v[56:59], v53 offset:49152
	v_mfma_f32_32x32x16_f16 v[2:17], v[64:67], v[60:63], v[2:17]
	ds_read_b128 v[60:63], v48 offset:53248
	s_waitcnt lgkmcnt(0)
	v_mfma_f32_32x32x16_f16 v[18:33], v[68:71], v[56:59], v[18:33]
	v_mfma_f32_32x32x16_f16 v[2:17], v[60:63], v[56:59], v[2:17]
	ds_read_b128 v[56:59], v52 offset:49152
	ds_read_b128 v[60:63], v54 offset:49152
	ds_read_b128 v[64:67], v52 offset:53248
	ds_read_b128 v[68:71], v50 offset:49152
	s_waitcnt lgkmcnt(0)
	v_mfma_f32_32x32x16_f16 v[18:33], v[56:59], v[60:63], v[18:33]
	ds_read_b128 v[56:59], v55 offset:49152
	v_mfma_f32_32x32x16_f16 v[2:17], v[64:67], v[60:63], v[2:17]
	ds_read_b128 v[60:63], v50 offset:53248
	s_waitcnt lgkmcnt(0)
	v_mfma_f32_32x32x16_f16 v[18:33], v[68:71], v[56:59], v[18:33]
	v_mfma_f32_32x32x16_f16 v[2:17], v[60:63], v[56:59], v[2:17]
	s_mov_b64 s[28:29], 0x380
	s_mov_b32 m0, s25
	v_lshl_add_u64 v[56:57], v[36:37], 0, s[28:29]
	s_waitcnt vmcnt(8)
	s_barrier
	global_load_lds_dwordx4 v[56:57], off
	v_lshl_add_u64 v[56:57], v[38:39], 0, s[28:29]
	s_mov_b32 m0, s23
	s_nop 0
	global_load_lds_dwordx4 v[56:57], off
	v_lshl_add_u64 v[56:57], v[40:41], 0, s[28:29]
	s_mov_b32 m0, s24
	s_nop 0
	global_load_lds_dwordx4 v[56:57], off
	v_lshl_add_u64 v[56:57], v[42:43], 0, s[28:29]
	s_mov_b32 m0, s26
	s_nop 0
	global_load_lds_dwordx4 v[56:57], off
	ds_read_b128 v[56:59], v49
	ds_read_b128 v[60:63], v51
	ds_read_b128 v[64:67], v49 offset:4096
	ds_read_b128 v[68:71], v48
	s_waitcnt lgkmcnt(0)
	v_mfma_f32_32x32x16_f16 v[18:33], v[56:59], v[60:63], v[18:33]
	ds_read_b128 v[56:59], v53
	v_mfma_f32_32x32x16_f16 v[2:17], v[64:67], v[60:63], v[2:17]
	ds_read_b128 v[60:63], v48 offset:4096
	s_waitcnt lgkmcnt(0)
	v_mfma_f32_32x32x16_f16 v[18:33], v[68:71], v[56:59], v[18:33]
	v_mfma_f32_32x32x16_f16 v[2:17], v[60:63], v[56:59], v[2:17]
	ds_read_b128 v[56:59], v52
	ds_read_b128 v[60:63], v54
	ds_read_b128 v[64:67], v52 offset:4096
	ds_read_b128 v[68:71], v50
	s_waitcnt lgkmcnt(0)
	v_mfma_f32_32x32x16_f16 v[18:33], v[56:59], v[60:63], v[18:33]
	ds_read_b128 v[56:59], v55
	v_mfma_f32_32x32x16_f16 v[2:17], v[64:67], v[60:63], v[2:17]
	ds_read_b128 v[60:63], v50 offset:4096
	s_waitcnt lgkmcnt(0)
	v_mfma_f32_32x32x16_f16 v[18:33], v[68:71], v[56:59], v[18:33]
	v_mfma_f32_32x32x16_f16 v[2:17], v[60:63], v[56:59], v[2:17]
	s_mov_b64 s[28:29], 0x400
	s_mov_b32 m0, s19
	v_lshl_add_u64 v[56:57], v[36:37], 0, s[28:29]
	s_waitcnt vmcnt(8)
	s_barrier
	global_load_lds_dwordx4 v[56:57], off
	v_lshl_add_u64 v[56:57], v[38:39], 0, s[28:29]
	s_mov_b32 m0, s20
	s_nop 0
	global_load_lds_dwordx4 v[56:57], off
	v_lshl_add_u64 v[56:57], v[40:41], 0, s[28:29]
	s_mov_b32 m0, s21
	s_nop 0
	global_load_lds_dwordx4 v[56:57], off
	v_lshl_add_u64 v[56:57], v[42:43], 0, s[28:29]
	s_mov_b32 m0, s22
	s_nop 0
	global_load_lds_dwordx4 v[56:57], off
	ds_read_b128 v[56:59], v49 offset:16384
	ds_read_b128 v[60:63], v51 offset:16384
	ds_read_b128 v[64:67], v49 offset:20480
	ds_read_b128 v[68:71], v48 offset:16384
	s_waitcnt lgkmcnt(0)
	v_mfma_f32_32x32x16_f16 v[18:33], v[56:59], v[60:63], v[18:33]
	ds_read_b128 v[56:59], v53 offset:16384
	v_mfma_f32_32x32x16_f16 v[2:17], v[64:67], v[60:63], v[2:17]
	ds_read_b128 v[60:63], v48 offset:20480
	s_waitcnt lgkmcnt(0)
	v_mfma_f32_32x32x16_f16 v[18:33], v[68:71], v[56:59], v[18:33]
	v_mfma_f32_32x32x16_f16 v[2:17], v[60:63], v[56:59], v[2:17]
	ds_read_b128 v[56:59], v52 offset:16384
	ds_read_b128 v[60:63], v54 offset:16384
	ds_read_b128 v[64:67], v52 offset:20480
	ds_read_b128 v[68:71], v50 offset:16384
	s_waitcnt lgkmcnt(0)
	v_mfma_f32_32x32x16_f16 v[18:33], v[56:59], v[60:63], v[18:33]
	ds_read_b128 v[56:59], v55 offset:16384
	v_mfma_f32_32x32x16_f16 v[2:17], v[64:67], v[60:63], v[2:17]
	ds_read_b128 v[60:63], v50 offset:20480
	s_waitcnt lgkmcnt(0)
	v_mfma_f32_32x32x16_f16 v[18:33], v[68:71], v[56:59], v[18:33]
	v_mfma_f32_32x32x16_f16 v[2:17], v[60:63], v[56:59], v[2:17]
	s_mov_b64 s[28:29], 0x480
	s_mov_b32 m0, s15
	v_lshl_add_u64 v[56:57], v[36:37], 0, s[28:29]
	s_waitcnt vmcnt(8)
	s_barrier
	global_load_lds_dwordx4 v[56:57], off
	v_lshl_add_u64 v[56:57], v[38:39], 0, s[28:29]
	s_mov_b32 m0, s16
	s_nop 0
	global_load_lds_dwordx4 v[56:57], off
	v_lshl_add_u64 v[56:57], v[40:41], 0, s[28:29]
	s_mov_b32 m0, s17
	s_nop 0
	global_load_lds_dwordx4 v[56:57], off
	v_lshl_add_u64 v[56:57], v[42:43], 0, s[28:29]
	s_mov_b32 m0, s18
	s_nop 0
	global_load_lds_dwordx4 v[56:57], off
	ds_read_b128 v[56:59], v49 offset:32768
	ds_read_b128 v[60:63], v51 offset:32768
	ds_read_b128 v[64:67], v49 offset:36864
	ds_read_b128 v[68:71], v48 offset:32768
	s_waitcnt lgkmcnt(0)
	v_mfma_f32_32x32x16_f16 v[18:33], v[56:59], v[60:63], v[18:33]
	ds_read_b128 v[56:59], v53 offset:32768
	v_mfma_f32_32x32x16_f16 v[2:17], v[64:67], v[60:63], v[2:17]
	ds_read_b128 v[60:63], v48 offset:36864
	s_waitcnt lgkmcnt(0)
	v_mfma_f32_32x32x16_f16 v[18:33], v[68:71], v[56:59], v[18:33]
	v_mfma_f32_32x32x16_f16 v[2:17], v[60:63], v[56:59], v[2:17]
	ds_read_b128 v[56:59], v52 offset:32768
	ds_read_b128 v[60:63], v54 offset:32768
	ds_read_b128 v[64:67], v52 offset:36864
	ds_read_b128 v[68:71], v50 offset:32768
	s_waitcnt lgkmcnt(0)
	v_mfma_f32_32x32x16_f16 v[18:33], v[56:59], v[60:63], v[18:33]
	ds_read_b128 v[56:59], v55 offset:32768
	v_mfma_f32_32x32x16_f16 v[2:17], v[64:67], v[60:63], v[2:17]
	ds_read_b128 v[60:63], v50 offset:36864
	s_waitcnt lgkmcnt(0)
	v_mfma_f32_32x32x16_f16 v[18:33], v[68:71], v[56:59], v[18:33]
	v_mfma_f32_32x32x16_f16 v[2:17], v[60:63], v[56:59], v[2:17]
	s_mov_b64 s[28:29], 0x500
	s_mov_b32 m0, s11
	v_lshl_add_u64 v[56:57], v[36:37], 0, s[28:29]
	s_waitcnt vmcnt(8)
	s_barrier
	global_load_lds_dwordx4 v[56:57], off
	v_lshl_add_u64 v[56:57], v[38:39], 0, s[28:29]
	s_mov_b32 m0, s12
	s_nop 0
	global_load_lds_dwordx4 v[56:57], off
	v_lshl_add_u64 v[56:57], v[40:41], 0, s[28:29]
	s_mov_b32 m0, s13
	s_nop 0
	global_load_lds_dwordx4 v[56:57], off
	v_lshl_add_u64 v[56:57], v[42:43], 0, s[28:29]
	s_mov_b32 m0, s14
	s_nop 0
	global_load_lds_dwordx4 v[56:57], off
	ds_read_b128 v[56:59], v49 offset:49152
	ds_read_b128 v[60:63], v51 offset:49152
	ds_read_b128 v[64:67], v49 offset:53248
	ds_read_b128 v[68:71], v48 offset:49152
	s_waitcnt lgkmcnt(0)
	v_mfma_f32_32x32x16_f16 v[18:33], v[56:59], v[60:63], v[18:33]
	ds_read_b128 v[56:59], v53 offset:49152
	v_mfma_f32_32x32x16_f16 v[2:17], v[64:67], v[60:63], v[2:17]
	ds_read_b128 v[60:63], v48 offset:53248
	s_waitcnt lgkmcnt(0)
	v_mfma_f32_32x32x16_f16 v[18:33], v[68:71], v[56:59], v[18:33]
	v_mfma_f32_32x32x16_f16 v[2:17], v[60:63], v[56:59], v[2:17]
	ds_read_b128 v[56:59], v52 offset:49152
	ds_read_b128 v[60:63], v54 offset:49152
	ds_read_b128 v[64:67], v52 offset:53248
	ds_read_b128 v[68:71], v50 offset:49152
	s_waitcnt lgkmcnt(0)
	v_mfma_f32_32x32x16_f16 v[18:33], v[56:59], v[60:63], v[18:33]
	ds_read_b128 v[56:59], v55 offset:49152
	v_mfma_f32_32x32x16_f16 v[2:17], v[64:67], v[60:63], v[2:17]
	ds_read_b128 v[60:63], v50 offset:53248
	s_waitcnt lgkmcnt(0)
	v_mfma_f32_32x32x16_f16 v[18:33], v[68:71], v[56:59], v[18:33]
	v_mfma_f32_32x32x16_f16 v[2:17], v[60:63], v[56:59], v[2:17]
	s_mov_b64 s[28:29], 0x580
	s_mov_b32 m0, s25
	v_lshl_add_u64 v[64:65], v[36:37], 0, s[28:29]
	s_waitcnt vmcnt(8)
	s_barrier
	global_load_lds_dwordx4 v[64:65], off
	v_lshl_add_u64 v[66:67], v[38:39], 0, s[28:29]
	s_mov_b32 m0, s23
	v_lshl_add_u64 v[68:69], v[40:41], 0, s[28:29]
	global_load_lds_dwordx4 v[66:67], off
	s_mov_b32 m0, s24
	v_lshl_add_u64 v[70:71], v[42:43], 0, s[28:29]
	global_load_lds_dwordx4 v[68:69], off
	s_mov_b32 m0, s26
	s_nop 0
	global_load_lds_dwordx4 v[70:71], off
	ds_read_b128 v[36:39], v49
	ds_read_b128 v[40:43], v51
	ds_read_b128 v[56:59], v49 offset:4096
	ds_read_b128 v[60:63], v48
	s_waitcnt lgkmcnt(0)
	v_mfma_f32_32x32x16_f16 v[18:33], v[36:39], v[40:43], v[18:33]
	ds_read_b128 v[36:39], v53
	v_mfma_f32_32x32x16_f16 v[2:17], v[56:59], v[40:43], v[2:17]
	ds_read_b128 v[40:43], v48 offset:4096
	s_waitcnt lgkmcnt(0)
	v_mfma_f32_32x32x16_f16 v[18:33], v[60:63], v[36:39], v[18:33]
	v_mfma_f32_32x32x16_f16 v[2:17], v[40:43], v[36:39], v[2:17]
	ds_read_b128 v[36:39], v52
	ds_read_b128 v[40:43], v54
	ds_read_b128 v[56:59], v52 offset:4096
	ds_read_b128 v[60:63], v50
	s_waitcnt lgkmcnt(0)
	v_mfma_f32_32x32x16_f16 v[18:33], v[36:39], v[40:43], v[18:33]
	ds_read_b128 v[36:39], v55
	v_mfma_f32_32x32x16_f16 v[2:17], v[56:59], v[40:43], v[2:17]
	ds_read_b128 v[40:43], v50 offset:4096
	s_waitcnt lgkmcnt(0)
	v_mfma_f32_32x32x16_f16 v[18:33], v[60:63], v[36:39], v[18:33]
	v_mfma_f32_32x32x16_f16 v[2:17], v[40:43], v[36:39], v[2:17]
	s_mov_b32 m0, s19
	s_waitcnt vmcnt(8)
	s_barrier
	global_load_lds_dwordx4 v[64:65], off
	s_mov_b32 m0, s20
	s_nop 0
	global_load_lds_dwordx4 v[66:67], off
	s_mov_b32 m0, s21
	s_nop 0
	global_load_lds_dwordx4 v[68:69], off
	s_mov_b32 m0, s22
	s_nop 0
	global_load_lds_dwordx4 v[70:71], off
	ds_read_b128 v[36:39], v49 offset:16384
	ds_read_b128 v[40:43], v51 offset:16384
	ds_read_b128 v[56:59], v49 offset:20480
	ds_read_b128 v[60:63], v48 offset:16384
	s_waitcnt lgkmcnt(0)
	v_mfma_f32_32x32x16_f16 v[18:33], v[36:39], v[40:43], v[18:33]
	ds_read_b128 v[36:39], v53 offset:16384
	v_mfma_f32_32x32x16_f16 v[2:17], v[56:59], v[40:43], v[2:17]
	ds_read_b128 v[40:43], v48 offset:20480
	s_waitcnt lgkmcnt(0)
	v_mfma_f32_32x32x16_f16 v[18:33], v[60:63], v[36:39], v[18:33]
	v_mfma_f32_32x32x16_f16 v[2:17], v[40:43], v[36:39], v[2:17]
	ds_read_b128 v[36:39], v52 offset:16384
	ds_read_b128 v[40:43], v54 offset:16384
	ds_read_b128 v[56:59], v52 offset:20480
	ds_read_b128 v[60:63], v50 offset:16384
	s_waitcnt lgkmcnt(0)
	v_mfma_f32_32x32x16_f16 v[18:33], v[36:39], v[40:43], v[18:33]
	ds_read_b128 v[36:39], v55 offset:16384
	v_mfma_f32_32x32x16_f16 v[2:17], v[56:59], v[40:43], v[2:17]
	ds_read_b128 v[40:43], v50 offset:20480
	s_waitcnt lgkmcnt(0)
	v_mfma_f32_32x32x16_f16 v[18:33], v[60:63], v[36:39], v[18:33]
	v_mfma_f32_32x32x16_f16 v[2:17], v[40:43], v[36:39], v[2:17]
	s_mov_b32 m0, s15
	s_waitcnt vmcnt(8)
	s_barrier
	global_load_lds_dwordx4 v[64:65], off
	s_mov_b32 m0, s16
	s_nop 0
	global_load_lds_dwordx4 v[66:67], off
	s_mov_b32 m0, s17
	s_nop 0
	global_load_lds_dwordx4 v[68:69], off
	s_mov_b32 m0, s18
	s_nop 0
	global_load_lds_dwordx4 v[70:71], off
	ds_read_b128 v[36:39], v49 offset:32768
	ds_read_b128 v[40:43], v51 offset:32768
	ds_read_b128 v[56:59], v49 offset:36864
	ds_read_b128 v[60:63], v48 offset:32768
	s_waitcnt lgkmcnt(0)
	v_mfma_f32_32x32x16_f16 v[18:33], v[36:39], v[40:43], v[18:33]
	ds_read_b128 v[36:39], v53 offset:32768
	v_mfma_f32_32x32x16_f16 v[2:17], v[56:59], v[40:43], v[2:17]
	ds_read_b128 v[40:43], v48 offset:36864
	s_waitcnt lgkmcnt(0)
	v_mfma_f32_32x32x16_f16 v[18:33], v[60:63], v[36:39], v[18:33]
	v_mfma_f32_32x32x16_f16 v[2:17], v[40:43], v[36:39], v[2:17]
	ds_read_b128 v[36:39], v52 offset:32768
	ds_read_b128 v[40:43], v54 offset:32768
	ds_read_b128 v[56:59], v52 offset:36864
	ds_read_b128 v[60:63], v50 offset:32768
	s_waitcnt lgkmcnt(0)
	v_mfma_f32_32x32x16_f16 v[18:33], v[36:39], v[40:43], v[18:33]
	ds_read_b128 v[36:39], v55 offset:32768
	v_mfma_f32_32x32x16_f16 v[2:17], v[56:59], v[40:43], v[2:17]
	ds_read_b128 v[40:43], v50 offset:36864
	s_waitcnt lgkmcnt(0)
	v_mfma_f32_32x32x16_f16 v[18:33], v[60:63], v[36:39], v[18:33]
	v_mfma_f32_32x32x16_f16 v[2:17], v[40:43], v[36:39], v[2:17]
	s_mov_b32 m0, s11
	s_waitcnt vmcnt(8)
	s_barrier
	global_load_lds_dwordx4 v[64:65], off
	s_mov_b32 m0, s12
	s_nop 0
	global_load_lds_dwordx4 v[66:67], off
	s_mov_b32 m0, s13
	s_nop 0
	global_load_lds_dwordx4 v[68:69], off
	s_mov_b32 m0, s14
	s_nop 0
	global_load_lds_dwordx4 v[70:71], off
	ds_read_b128 v[36:39], v49 offset:49152
	ds_read_b128 v[40:43], v51 offset:49152
	ds_read_b128 v[56:59], v49 offset:53248
	ds_read_b128 v[60:63], v48 offset:49152
	s_waitcnt lgkmcnt(0)
	v_mfma_f32_32x32x16_f16 v[18:33], v[36:39], v[40:43], v[18:33]
	ds_read_b128 v[36:39], v53 offset:49152
	v_mfma_f32_32x32x16_f16 v[2:17], v[56:59], v[40:43], v[2:17]
	ds_read_b128 v[40:43], v48 offset:53248
	s_waitcnt lgkmcnt(0)
	v_mfma_f32_32x32x16_f16 v[18:33], v[60:63], v[36:39], v[18:33]
	v_mfma_f32_32x32x16_f16 v[2:17], v[40:43], v[36:39], v[2:17]
	ds_read_b128 v[36:39], v52 offset:49152
	ds_read_b128 v[40:43], v54 offset:49152
	ds_read_b128 v[56:59], v52 offset:53248
	ds_read_b128 v[60:63], v50 offset:49152
	s_waitcnt lgkmcnt(0)
	v_mfma_f32_32x32x16_f16 v[18:33], v[36:39], v[40:43], v[18:33]
	ds_read_b128 v[36:39], v55 offset:49152
	v_mfma_f32_32x32x16_f16 v[2:17], v[56:59], v[40:43], v[2:17]
	ds_read_b128 v[40:43], v50 offset:53248
	s_waitcnt lgkmcnt(0)
	v_mfma_f32_32x32x16_f16 v[18:33], v[60:63], v[36:39], v[18:33]
	v_mfma_f32_32x32x16_f16 v[2:17], v[40:43], v[36:39], v[2:17]
	v_mul_u32_u24_e32 v56, 0x2400, v44
	v_lshl_or_b32 v36, v47, 2, v56
	s_movk_i32 s11, 0x240
	v_mad_u32_u24 v36, v46, s11, v36
	s_waitcnt vmcnt(8)
	s_barrier
	s_waitcnt vmcnt(0)
	s_waitcnt vmcnt(0)
	s_barrier
	s_nop 3
	ds_write2_b32 v36, v18, v19 offset1:36
	ds_write2_b32 v36, v20, v21 offset0:72 offset1:108
	v_add_u32_e32 v18, 0x400, v36
	ds_write2_b32 v18, v22, v23 offset0:32 offset1:68
	ds_write2_b32 v18, v24, v25 offset0:104 offset1:140
	v_add_u32_e32 v18, 0x800, v36
	ds_write2_b32 v18, v26, v27 offset0:64 offset1:100
	ds_write2_b32 v18, v28, v29 offset0:136 offset1:172
	v_add_u32_e32 v18, 0xc00, v36
	ds_write2_b32 v18, v30, v31 offset0:96 offset1:132
	ds_write2_b32 v18, v32, v33 offset0:168 offset1:204
	v_add_u32_e32 v18, 0x1000, v36
	ds_write2_b32 v18, v2, v3 offset0:128 offset1:164
	ds_write2_b32 v18, v4, v5 offset0:200 offset1:236
	v_add_u32_e32 v2, 0x1400, v36
	ds_write2_b32 v2, v6, v7 offset0:160 offset1:196
	v_add_u32_e32 v2, 0x1600, v36
	ds_write2_b32 v2, v8, v9 offset0:104 offset1:140
	v_add_u32_e32 v2, 0x1800, v36
	ds_write2_b32 v2, v10, v11 offset0:192 offset1:228
	v_add_u32_e32 v2, 0x1c00, v36
	ds_write2_b32 v2, v12, v13 offset0:8 offset1:44
	v_add_u32_e32 v2, 0x1e00, v36
	v_lshl_or_b32 v5, v45, 5, s10
	v_lshlrev_b32_e32 v6, 2, v0
	ds_write2_b32 v2, v14, v15 offset0:96 offset1:132
	v_add_u32_e32 v2, 0x2000, v36
	v_lshlrev_b32_e32 v4, 6, v34
	v_lshlrev_b32_e32 v34, 2, v5
	v_and_b32_e32 v6, 28, v6
	ds_write2_b32 v2, v16, v17 offset0:40 offset1:76
	v_lshl_add_u64 v[2:3], s[8:9], 0, v[34:35]
	v_lshlrev_b32_e32 v34, 2, v6
	v_lshl_add_u64 v[10:11], v[2:3], 0, v[34:35]
	v_or3_b32 v2, s3, v4, v1
	v_or_b32_e32 v3, v5, v6
	s_movk_i32 s3, 0x300
	v_mad_u32_u24 v36, v2, s3, v3
	v_add_u32_e32 v2, 0x4800, v36
	v_mov_b32_e32 v3, v35
	v_lshlrev_b64 v[40:41], 2, v[2:3]
	v_lshl_add_u64 v[12:13], s[6:7], 0, v[40:41]
	global_load_dwordx4 v[2:5], v[10:11], off
	global_load_dwordx4 v[6:9], v[12:13], off
	v_add_u32_e32 v10, 0x3000, v36
	v_mov_b32_e32 v11, v35
	v_lshlrev_b64 v[42:43], 2, v[10:11]
	v_lshl_add_u64 v[10:11], s[6:7], 0, v[42:43]
	global_load_dwordx4 v[10:13], v[10:11], off
	v_add_u32_e32 v14, 0x1800, v36
	v_mov_b32_e32 v15, v35
	v_lshlrev_b64 v[44:45], 2, v[14:15]
	v_lshl_add_u64 v[14:15], s[6:7], 0, v[44:45]
	v_mov_b32_e32 v37, v35
	global_load_dwordx4 v[14:17], v[14:15], off
	v_lshlrev_b64 v[46:47], 2, v[36:37]
	v_lshl_add_u64 v[18:19], s[6:7], 0, v[46:47]
	global_load_dwordx4 v[18:21], v[18:19], off
	v_add_u32_e32 v22, 0x6000, v36
	v_mov_b32_e32 v23, v35
	v_lshlrev_b64 v[48:49], 2, v[22:23]
	v_lshl_add_u64 v[22:23], s[6:7], 0, v[48:49]
	v_add_u32_e32 v26, 0x7800, v36
	v_mov_b32_e32 v27, v35
	global_load_dwordx4 v[22:25], v[22:23], off
	v_lshlrev_b64 v[50:51], 2, v[26:27]
	v_lshl_add_u64 v[26:27], s[6:7], 0, v[50:51]
	global_load_dwordx4 v[26:29], v[26:27], off
	v_add_u32_e32 v30, 0x9000, v36
	v_mov_b32_e32 v31, v35
	v_add_u32_e32 v36, 0xa800, v36
	v_lshlrev_b64 v[52:53], 2, v[30:31]
	v_lshlrev_b64 v[54:55], 2, v[36:37]
	v_lshl_add_u64 v[30:31], s[6:7], 0, v[52:53]
	v_lshl_add_u64 v[36:37], s[6:7], 0, v[54:55]
	global_load_dwordx4 v[30:33], v[30:31], off
	v_or_b32_e32 v34, v56, v34
	global_load_dwordx4 v[36:39], v[36:37], off
	s_movk_i32 s3, 0x90
	v_mad_u32_u24 v1, v1, s3, v34
	v_lshl_add_u64 v[58:59], s[4:5], 0, v[42:43]
	v_lshl_add_u64 v[60:61], s[4:5], 0, v[40:41]
	ds_read_b128 v[40:43], v1 offset:3456
	v_lshl_add_u64 v[34:35], s[4:5], 0, v[46:47]
	v_lshl_add_u64 v[56:57], s[4:5], 0, v[44:45]
	ds_read_b128 v[44:47], v1 offset:2304
	v_lshl_add_u64 v[48:49], s[4:5], 0, v[48:49]
	v_lshl_add_u64 v[50:51], s[4:5], 0, v[50:51]
	v_lshl_add_u64 v[52:53], s[4:5], 0, v[52:53]
	v_lshl_add_u64 v[54:55], s[4:5], 0, v[54:55]
	s_mov_b64 s[4:5], 0
	s_waitcnt vmcnt(8) lgkmcnt(1)
	v_pk_add_f32 v[40:41], v[2:3], v[40:41]
	s_waitcnt vmcnt(7)
	v_pk_add_f32 v[6:7], v[40:41], v[6:7]
	v_pk_add_f32 v[40:41], v[4:5], v[42:43]
	s_waitcnt lgkmcnt(0)
	v_pk_add_f32 v[44:45], v[2:3], v[44:45]
	v_pk_add_f32 v[8:9], v[40:41], v[8:9]
	ds_read_b128 v[40:43], v1 offset:1152
	s_waitcnt vmcnt(6)
	v_pk_add_f32 v[10:11], v[44:45], v[10:11]
	v_pk_add_f32 v[44:45], v[4:5], v[46:47]
	s_nop 0
	v_pk_add_f32 v[12:13], v[44:45], v[12:13]
	ds_read_b128 v[44:47], v1
	s_waitcnt lgkmcnt(1)
	v_pk_add_f32 v[40:41], v[2:3], v[40:41]
	s_waitcnt vmcnt(5)
	v_pk_add_f32 v[14:15], v[40:41], v[14:15]
	v_pk_add_f32 v[40:41], v[4:5], v[42:43]
	s_nop 0
	v_pk_add_f32 v[16:17], v[40:41], v[16:17]
	s_waitcnt lgkmcnt(0)
	v_pk_add_f32 v[40:41], v[2:3], v[44:45]
	s_waitcnt vmcnt(4)
	v_pk_add_f32 v[18:19], v[40:41], v[18:19]
	v_pk_add_f32 v[40:41], v[4:5], v[46:47]
	s_nop 0
	v_pk_add_f32 v[20:21], v[40:41], v[20:21]
	global_store_dwordx4 v[34:35], v[18:21], off sc1
	ds_read_b128 v[18:21], v1 offset:4608
	global_store_dwordx4 v[56:57], v[14:17], off sc1
	global_store_dwordx4 v[58:59], v[10:13], off sc1
	global_store_dwordx4 v[60:61], v[6:9], off sc1
	ds_read_b128 v[6:9], v1 offset:5760
	s_waitcnt lgkmcnt(1)
	v_pk_add_f32 v[10:11], v[2:3], v[18:19]
	v_pk_add_f32 v[12:13], v[4:5], v[20:21]
	s_waitcnt vmcnt(7)
	v_pk_add_f32 v[10:11], v[10:11], v[22:23]
	v_pk_add_f32 v[12:13], v[12:13], v[24:25]
	global_store_dwordx4 v[48:49], v[10:13], off sc1
	ds_read_b128 v[10:13], v1 offset:6912
	s_waitcnt lgkmcnt(1)
	v_pk_add_f32 v[6:7], v[2:3], v[6:7]
	v_pk_add_f32 v[8:9], v[4:5], v[8:9]
	s_waitcnt vmcnt(7)
	v_pk_add_f32 v[6:7], v[6:7], v[26:27]
	v_pk_add_f32 v[8:9], v[8:9], v[28:29]
	global_store_dwordx4 v[50:51], v[6:9], off sc1
	ds_read_b128 v[6:9], v1 offset:8064
	s_waitcnt lgkmcnt(1)
	v_pk_add_f32 v[10:11], v[2:3], v[10:11]
	v_pk_add_f32 v[12:13], v[4:5], v[12:13]
	s_waitcnt vmcnt(7)
	v_pk_add_f32 v[10:11], v[10:11], v[30:31]
	v_pk_add_f32 v[12:13], v[12:13], v[32:33]
	s_waitcnt lgkmcnt(0)
	v_pk_add_f32 v[2:3], v[2:3], v[6:7]
	v_pk_add_f32 v[4:5], v[4:5], v[8:9]
	s_waitcnt vmcnt(6)
	v_pk_add_f32 v[2:3], v[2:3], v[36:37]
	v_pk_add_f32 v[4:5], v[4:5], v[38:39]
	global_store_dwordx4 v[52:53], v[10:13], off sc1
	global_store_dwordx4 v[54:55], v[2:5], off sc1

_Z6gemm_kILi2ELi128ELi2ELi4EEv5GArgs:
	v_lshlrev_b32_e32 v194, 4, v0
	s_getpc_b64 s[92:93]
	s_add_u32 s92, s92, 0x30f8
	s_addc_u32 s93, s93, 0x0
	global_load_dword v195, v194, s[92:93]
	v_add_u32_e32 v194, 0x1000, v194
	global_load_dword v195, v194, s[92:93]
	v_lshlrev_b32_e32 v194, 4, v0
	s_load_dwordx4 s[4:7], s[0:1], 0x38
	s_lshr_b32 s9, s2, 3
	s_and_b32 s3, s2, 7
	s_mul_hi_u32 s10, s9, 0x33333334
	s_mul_i32 s10, s10, 5
	s_waitcnt lgkmcnt(0)
	s_load_dword s8, s[6:7], 0x280
	s_sub_i32 s9, s9, s10
	s_waitcnt lgkmcnt(0)
	s_mul_i32 s3, s8, s3
	s_ashr_i32 s10, s3, 3
	s_add_i32 s3, s3, s8
	s_ashr_i32 s8, s3, 3
	s_add_i32 s3, s10, s9
	s_cmp_ge_i32 s3, s8
	s_cbranch_scc1 .LBB13_20
	s_lshl_b32 s8, s3, 2
	s_ashr_i32 s9, s8, 31
	s_lshl_b64 s[8:9], s[8:9], 2
	s_add_u32 s6, s6, s8
	s_addc_u32 s7, s7, s9
	s_load_dwordx4 s[12:15], s[6:7], 0x0
	s_mov_b32 s3, 0
	s_waitcnt lgkmcnt(0)
	s_cmp_lt_i32 s12, 0
	s_cbranch_scc1 .LBB13_20
	s_mov_b32 s8, s13
	s_mov_b32 s9, s14
	v_lshrrev_b32_e32 v1, 6, v0
	v_bfe_u32 v76, v0, 3, 3
	v_lshl_or_b32 v6, v1, 5, v76
	v_or_b32_e32 v44, 8, v6
	s_waitcnt lgkmcnt(0)
	s_add_i32 s6, s9, -1
	v_add_u32_e32 v4, s8, v6
	v_min_i32_e32 v2, s6, v4
	v_add_u32_e32 v4, 16, v4
	v_min_i32_e32 v4, s6, v4
	v_ashrrev_i32_e32 v3, 31, v2
	v_ashrrev_i32_e32 v5, 31, v4
	v_lshl_add_u64 v[2:3], v[2:3], 2, s[4:5]
	v_lshl_add_u64 v[4:5], v[4:5], 2, s[4:5]
	global_load_dword v7, v[2:3], off
	global_load_dword v8, v[4:5], off
	v_or_b32_e32 v4, 24, v6
	v_add_u32_e32 v2, s8, v4
	v_min_i32_e32 v2, s6, v2
	v_ashrrev_i32_e32 v3, 31, v2
	v_lshl_add_u64 v[2:3], v[2:3], 2, s[4:5]
	global_load_dword v9, v[2:3], off
	v_add_u32_e32 v2, s8, v44
	v_min_i32_e32 v2, s6, v2
	v_ashrrev_i32_e32 v3, 31, v2
	v_lshl_add_u64 v[2:3], v[2:3], 2, s[4:5]
	global_load_dword v45, v[2:3], off
	s_load_dwordx2 s[14:15], s[0:1], 0x0
	s_load_dwordx4 s[4:7], s[0:1], 0x10
	v_lshrrev_b32_e32 v4, 1, v4
	v_bfe_u32 v2, v0, 4, 2
	v_xor_b32_e32 v4, v4, v0
	s_mul_hi_u32 s10, s2, 0xcccccccd
	s_movk_i32 s2, 0x680
	v_bitop3_b32 v2, v2, v0, 7 bitop3:0x78
	s_waitcnt lgkmcnt(0)
	v_mov_b64_e32 v[36:37], s[14:15]
	v_lshlrev_b32_e32 v4, 3, v4
	v_mov_b32_e32 v3, 0
	v_bfe_u32 v77, v0, 5, 1
	s_lshl_b32 s10, s10, 2
	v_lshlrev_b32_e32 v2, 4, v2
	v_bitop3_b32 v11, v4, 8, 56 bitop3:0x6c
	s_mul_i32 s16, s12, 0x900000
	v_lshl_or_b32 v48, v1, 1, v77
	s_and_b32 s10, s10, 0xffffff80
	s_mul_hi_u32 s13, s12, 0x900000
	v_mul_u32_u24_e32 v10, 0x6000, v48
	s_add_u32 s4, s4, s16
	s_addc_u32 s5, s5, s13
	s_mov_b32 s11, s3
	v_and_b32_e32 v78, 31, v0
	s_movk_i32 s18, 0x3000
	s_movk_i32 s17, 0x6000
	s_mov_b32 s19, 0x9000
	s_mov_b32 s20, 0xc000
	s_mov_b32 s21, 0xf000
	s_mov_b32 s22, 0x12000
	v_lshlrev_b32_e32 v81, 12, v1
	v_or_b32_e32 v46, 0xc00, v81
	v_readfirstlane_b32 s13, v81
	s_mov_b32 m0, s13
	v_readfirstlane_b32 s16, v46
	v_lshlrev_b32_e32 v82, 9, v78
	s_load_dwordx2 s[0:1], s[0:1], 0x70
	v_lshrrev_b32_e32 v79, 7, v0
	v_bfe_u32 v80, v0, 6, 1
	v_lshlrev_b32_e32 v89, 13, v79
	v_lshlrev_b32_e32 v90, 7, v78
	v_lshlrev_b32_e32 v91, 13, v80
	s_mov_b32 s13, 0xc3000
	v_mov_b32_e32 v53, v3
	v_mov_b32_e32 v54, v3
	v_mov_b32_e32 v55, v3
	v_mov_b32_e32 v56, v3
	v_mov_b32_e32 v57, v3
	v_mov_b32_e32 v58, v3
	v_mov_b32_e32 v59, v3
	v_mov_b32_e32 v60, v3
	v_mov_b32_e32 v61, v3
	v_mov_b32_e32 v62, v3
	v_mov_b32_e32 v63, v3
	v_mov_b32_e32 v64, v3
	v_mov_b32_e32 v65, v3
	s_waitcnt vmcnt(3)
	v_mad_i64_i32 v[4:5], s[14:15], v7, s2, v[36:37]
	v_lshl_add_u64 v[66:67], v[4:5], 0, v[2:3]
	s_waitcnt vmcnt(2)
	v_mad_i64_i32 v[4:5], s[14:15], v8, s2, v[36:37]
	v_xor_b32_e32 v2, 16, v2
	v_lshl_add_u64 v[68:69], v[4:5], 0, v[2:3]
	s_waitcnt vmcnt(1)
	v_mad_i64_i32 v[6:7], s[14:15], v9, s2, v[36:37]
	v_lshlrev_b32_e32 v2, 1, v11
	v_lshl_add_u64 v[70:71], v[6:7], 0, v[2:3]
	v_lshlrev_b32_e32 v2, 2, v10
	v_lshl_add_u64 v[4:5], s[4:5], 0, v[2:3]
	v_lshlrev_b32_e32 v2, 4, v78
	v_lshl_add_u64 v[4:5], s[10:11], 2, v[4:5]
	v_lshl_add_u64 v[72:73], v[4:5], 0, v[2:3]
	v_add_co_u32_e32 v38, vcc, s18, v72
	s_mov_b32 s4, 0x15000
	s_nop 0
	v_addc_co_u32_e32 v39, vcc, 0, v73, vcc
	v_add_co_u32_e32 v40, vcc, s17, v72
	v_lshrrev_b32_e32 v2, 2, v0
	s_nop 0
	v_addc_co_u32_e32 v41, vcc, 0, v73, vcc
	v_add_co_u32_e32 v12, vcc, s19, v72
	s_mov_b32 s11, 1
	s_nop 0
	v_addc_co_u32_e32 v13, vcc, 0, v73, vcc
	v_add_co_u32_e32 v14, vcc, s20, v72
	s_mov_b32 s17, 0xcf000
	s_nop 0
	v_addc_co_u32_e32 v15, vcc, 0, v73, vcc
	v_add_co_u32_e32 v20, vcc, s21, v72
	global_load_dwordx4 v[4:7], v[12:13], off
	global_load_dwordx4 v[8:11], v[14:15], off
	v_addc_co_u32_e32 v21, vcc, 0, v73, vcc
	v_add_co_u32_e32 v22, vcc, s22, v72
	s_mov_b32 s18, 0xd2000
	s_nop 0
	v_addc_co_u32_e32 v23, vcc, 0, v73, vcc
	v_add_co_u32_e32 v42, vcc, s4, v72
	global_load_dwordx4 v[12:15], v[20:21], off
	global_load_dwordx4 v[16:19], v[22:23], off
	v_addc_co_u32_e32 v43, vcc, 0, v73, vcc
	global_load_dwordx4 v[20:23], v[42:43], off
	global_load_dwordx4 v[24:27], v[38:39], off
	global_load_dwordx4 v[28:31], v[40:41], off
	global_load_dwordx4 v[32:35], v[72:73], off
	v_lshlrev_b32_e32 v40, 1, v0
	v_bfe_u32 v38, v0, 2, 1
	v_lshlrev_b32_e32 v41, 2, v78
	v_and_b32_e32 v40, 6, v40
	v_bitop3_b32 v38, v38, v48, v40 bitop3:0x36
	v_or_b32_e32 v40, 2, v41
	v_or_b32_e32 v49, 3, v41
	v_lshrrev_b32_e32 v41, 1, v44
	v_lshlrev_b32_e32 v83, 4, v38
	v_bfe_u32 v38, v40, 1, 3
	v_lshlrev_b32_e32 v84, 7, v40
	v_xor_b32_e32 v40, v41, v0
	v_or_b32_e32 v42, 0x400, v81
	v_bitop3_b32 v38, v2, v38, 1 bitop3:0x6c
	v_lshlrev_b32_e32 v40, 4, v40
	v_mov_b32_e32 v39, v3
	v_or_b32_e32 v43, 0x800, v81
	v_readfirstlane_b32 s14, v42
	v_xor_b32_e32 v41, v38, v48
	v_and_b32_e32 v38, 0x70, v40
	s_waitcnt vmcnt(8)
	v_mad_i64_i32 v[36:37], s[4:5], v45, s2, v[36:37]
	v_readfirstlane_b32 s15, v43
	v_lshl_add_u64 v[74:75], v[36:37], 0, v[38:39]
	global_load_lds_dwordx4 v[66:67], off
	s_mov_b32 m0, s14
	v_bfe_u32 v50, v49, 1, 3
	global_load_lds_dwordx4 v[74:75], off
	s_mov_b32 m0, s15
	v_bitop3_b32 v2, v2, v50, 1 bitop3:0x6c
	global_load_lds_dwordx4 v[68:69], off
	s_mov_b32 m0, s16
	v_xor_b32_e32 v2, v2, v48
	global_load_lds_dwordx4 v[70:71], off
	v_readfirstlane_b32 s40, v81
	s_mov_b64 s[44:45], 0x3000
	s_mov_b64 s[46:47], 0x6000
	s_mov_b64 s[48:49], 0x9000
	s_mov_b64 s[50:51], 0xc000
	s_mov_b64 s[52:53], 0xf000
	s_mov_b64 s[54:55], 0x12000
	s_mov_b64 s[56:57], 0x15000
	s_mov_b32 s41, 0
	s_mov_b32 s42, 0x4000
	s_mov_b32 s43, 0x8000
	s_movk_i32 s2, 0x80
	s_add_i32 s23, s40, s42
	v_lshl_add_u64 v[144:145], v[66:67], 0, s[2:3]
	s_mov_b32 m0, s23
	s_add_i32 s23, s23, 0x400
	global_load_lds_dwordx4 v[144:145], off
	v_lshl_add_u64 v[144:145], v[74:75], 0, s[2:3]
	s_mov_b32 m0, s23
	s_add_i32 s23, s23, 0x400
	global_load_lds_dwordx4 v[144:145], off
	v_lshl_add_u64 v[144:145], v[68:69], 0, s[2:3]
	s_mov_b32 m0, s23
	s_add_i32 s23, s23, 0x400
	global_load_lds_dwordx4 v[144:145], off
	v_lshl_add_u64 v[144:145], v[70:71], 0, s[2:3]
	s_mov_b32 m0, s23
	s_nop 0
	global_load_lds_dwordx4 v[144:145], off
	s_mov_b32 s22, 0xc0000
	s_mov_b32 s23, 0
	v_lshl_add_u64 v[176:177], v[72:73], 0, s[22:23]
	v_lshl_add_u64 v[178:179], v[176:177], 0, s[44:45]
	v_lshl_add_u64 v[180:181], v[176:177], 0, s[46:47]
	v_lshl_add_u64 v[182:183], v[176:177], 0, s[48:49]
	v_lshl_add_u64 v[184:185], v[176:177], 0, s[50:51]
	v_lshl_add_u64 v[186:187], v[176:177], 0, s[52:53]
	v_lshl_add_u64 v[188:189], v[176:177], 0, s[54:55]
	v_lshl_add_u64 v[190:191], v[176:177], 0, s[56:57]
	global_load_dwordx4 v[144:147], v[176:177], off
	global_load_dwordx4 v[148:151], v[178:179], off
	global_load_dwordx4 v[152:155], v[180:181], off
	global_load_dwordx4 v[156:159], v[182:183], off
	global_load_dwordx4 v[160:163], v[184:185], off
	global_load_dwordx4 v[164:167], v[186:187], off
	global_load_dwordx4 v[168:171], v[188:189], off
	global_load_dwordx4 v[172:175], v[190:191], off
	v_lshlrev_b32_e32 v86, 4, v2
	v_lshlrev_b32_e32 v87, 7, v49
	v_or_b32_e32 v51, v82, v83
	v_lshlrev_b32_e32 v85, 4, v41
	v_add_u32_e32 v2, v87, v86
	v_add_u32_e32 v52, v84, v85
	s_mov_b64 s[4:5], 0x80
	s_mov_b32 s14, 0xc6000
	s_mov_b32 s15, 0xc9000
	s_mov_b32 s16, 0xcc000
	s_mov_b32 s19, 0xd5000
	s_mov_b32 s21, 0
	s_mov_b32 s20, 0
	v_mov_b32_e32 v48, v3
	v_mov_b32_e32 v49, v3
	v_mov_b32_e32 v50, v3
	s_waitcnt vmcnt(12)
	v_cvt_pk_f16_f32 v38, v8, v12
	v_cvt_pk_f16_f32 v39, v16, v20
	v_cvt_pk_f16_f32 v42, v9, v13
	v_cvt_pk_f16_f32 v37, v28, v4
	v_cvt_pk_f16_f32 v36, v32, v24
	v_cvt_pk_f16_f32 v45, v30, v6
	v_cvt_pk_f16_f32 v9, v19, v23
	v_cvt_pk_f16_f32 v8, v11, v15
	v_cvt_pk_f16_f32 v7, v31, v7
	v_cvt_pk_f16_f32 v6, v35, v27
	v_cvt_pk_f16_f32 v43, v17, v21
	v_cvt_pk_f16_f32 v41, v29, v5
	v_cvt_pk_f16_f32 v40, v33, v25
	v_cvt_pk_f16_f32 v47, v18, v22
	v_cvt_pk_f16_f32 v46, v10, v14
	v_cvt_pk_f16_f32 v44, v34, v26
	ds_write_b128 v51, v[36:39] offset:49152
	ds_write_b128 v51, v[40:43] offset:49280
	ds_write_b128 v52, v[44:47] offset:49152
	ds_write_b128 v2, v[6:9] offset:49152
	v_lshrrev_b32_e32 v2, 1, v0
	v_bfe_u32 v4, v0, 4, 1
	v_bitop3_b32 v2, v2, v4, 7 bitop3:0x6c
	v_xor_b32_e32 v4, v2, v77
	v_lshlrev_b32_e32 v88, 4, v4
	v_or_b32_e32 v4, 2, v77
	v_xor_b32_e32 v4, v2, v4
	v_lshlrev_b32_e32 v92, 4, v4
	v_or_b32_e32 v4, 4, v77
	v_xor_b32_e32 v4, v2, v4
	s_waitcnt vmcnt(12)
	v_lshlrev_b32_e32 v93, 4, v4
	v_or_b32_e32 v4, 6, v77
	v_xor_b32_e32 v2, v2, v4
	v_lshlrev_b32_e32 v94, 4, v2
	v_mov_b32_e32 v2, v3
	v_mov_b32_e32 v4, v3
	v_mov_b32_e32 v5, v3
	v_mov_b32_e32 v6, v3
	v_mov_b32_e32 v7, v3
	v_mov_b32_e32 v8, v3
	v_mov_b32_e32 v9, v3
	v_mov_b32_e32 v10, v3
	v_mov_b32_e32 v11, v3
	v_mov_b32_e32 v12, v3
	v_mov_b32_e32 v13, v3
	v_mov_b32_e32 v14, v3
	v_mov_b32_e32 v15, v3
	v_mov_b32_e32 v16, v3
	v_mov_b32_e32 v17, v3
	v_mov_b32_e32 v18, v3
	v_mov_b32_e32 v19, v3
	v_mov_b32_e32 v20, v3
	v_mov_b32_e32 v21, v3
	v_mov_b32_e32 v22, v3
	v_mov_b32_e32 v23, v3
	v_mov_b32_e32 v24, v3
	v_mov_b32_e32 v25, v3
	v_mov_b32_e32 v26, v3
	v_mov_b32_e32 v27, v3
	v_mov_b32_e32 v28, v3
	v_mov_b32_e32 v29, v3
	v_mov_b32_e32 v30, v3
	v_mov_b32_e32 v31, v3
	v_mov_b32_e32 v32, v3
	v_mov_b32_e32 v33, v3
	v_mov_b32_e32 v34, v3
	v_mov_b32_e32 v35, v3
	v_mov_b32_e32 v36, v3
	v_mov_b32_e32 v37, v3
	v_mov_b32_e32 v38, v3
	v_mov_b32_e32 v39, v3
	v_mov_b32_e32 v40, v3
	v_mov_b32_e32 v41, v3
	v_mov_b32_e32 v42, v3
	v_mov_b32_e32 v43, v3
	v_mov_b32_e32 v44, v3
	v_mov_b32_e32 v45, v3
	v_mov_b32_e32 v46, v3
	v_mov_b32_e32 v47, v3
	v_mov_b32_e32 v51, v3
	v_mov_b32_e32 v52, v3
	s_waitcnt lgkmcnt(0)
	s_barrier

	.amdhsa_kernel _Z6gemm_kILi2ELi128ELi2ELi4EEv5GArgs
		.amdhsa_group_segment_fixed_size 81920
		.amdhsa_private_segment_fixed_size 0
		.amdhsa_kernarg_size 136
		.amdhsa_user_sgpr_count 2
		.amdhsa_user_sgpr_dispatch_ptr 0
		.amdhsa_user_sgpr_queue_ptr 0
		.amdhsa_user_sgpr_kernarg_segment_ptr 1
		.amdhsa_user_sgpr_dispatch_id 0
		.amdhsa_user_sgpr_kernarg_preload_length 0
		.amdhsa_user_sgpr_kernarg_preload_offset 0
		.amdhsa_user_sgpr_private_segment_size 0
		.amdhsa_uses_dynamic_stack 0
		.amdhsa_enable_private_segment 0
		.amdhsa_system_sgpr_workgroup_id_x 1
		.amdhsa_system_sgpr_workgroup_id_y 0
		.amdhsa_system_sgpr_workgroup_id_z 0
		.amdhsa_system_sgpr_workgroup_info 0
		.amdhsa_system_vgpr_workitem_id 0
		.amdhsa_next_free_vgpr 196
		.amdhsa_next_free_sgpr 96
		.amdhsa_accum_offset 196
		.amdhsa_reserve_vcc 1
		.amdhsa_float_round_mode_32 0
		.amdhsa_float_round_mode_16_64 0
		.amdhsa_float_denorm_mode_32 3
		.amdhsa_float_denorm_mode_16_64 3
		.amdhsa_dx10_clamp 1
		.amdhsa_ieee_mode 1
		.amdhsa_fp16_overflow 0
		.amdhsa_tg_split 0
		.amdhsa_exception_fp_ieee_invalid_op 0
		.amdhsa_exception_fp_denorm_src 0
		.amdhsa_exception_fp_ieee_div_zero 0
		.amdhsa_exception_fp_ieee_overflow 0
		.amdhsa_exception_fp_ieee_underflow 0
		.amdhsa_exception_fp_ieee_inexact 0
		.amdhsa_exception_int_div_zero 0
	.end_amdhsa_kernel

_Z7gemm2_kILi3ELi2ELi2EEv5GArgs:
	v_lshlrev_b32_e32 v170, 4, v0
	s_getpc_b64 s[92:93]
	s_add_u32 s92, s92, 0xfffedbf8
	s_addc_u32 s93, s93, 0xffffffff
	global_load_dword v171, v170, s[92:93]
	s_load_dwordx4 s[8:11], s[0:1], 0x48
	s_load_dwordx2 s[20:21], s[0:1], 0x58
	s_cmpk_lt_u32 s2, 0xc0
	s_mov_b64 s[4:5], -1
	s_cbranch_scc0 .LBB14_39
	s_lshl_b32 s4, s2, 3
	s_lshl_b32 s3, s2, 8
	s_and_b32 s28, s4, 0x780
	s_load_dwordx4 s[12:15], s[0:1], 0x30
	s_load_dwordx2 s[22:23], s[0:1], 0x18
	s_load_dwordx4 s[16:19], s[0:1], 0x0
	s_and_b32 s3, s3, 0xf00
	s_add_i32 s29, s28, 0xfffffd00
	s_cmpk_gt_u32 s2, 0x5f
	v_lshrrev_b32_e32 v136, 6, v0
	s_cselect_b64 s[26:27], -1, 0
	v_bfe_u32 v131, v0, 3, 3
	v_lshl_or_b32 v16, v136, 5, v131
	s_and_b64 s[6:7], s[26:27], exec
	s_cselect_b32 s4, 0xc00, 0
	v_or_b32_e32 v12, s3, v16
	s_waitcnt lgkmcnt(0)
	s_add_u32 s6, s16, s4
	v_mul_u32_u24_e32 v2, 0xc40, v12
	v_bfe_u32 v24, v0, 4, 2
	s_addc_u32 s7, s17, 0
	v_lshlrev_b32_e32 v34, 1, v2
	v_mov_b32_e32 v35, 0
	v_bitop3_b32 v4, v24, v0, 7 bitop3:0x78
	v_lshl_add_u64 v[2:3], s[6:7], 0, v[34:35]
	v_lshlrev_b32_e32 v4, 4, v4
	v_mov_b32_e32 v5, v35
	v_lshl_add_u64 v[2:3], v[2:3], 0, v[4:5]
	v_or_b32_e32 v5, 8, v16
	v_or_b32_e32 v6, s3, v5
	v_lshrrev_b32_e32 v5, 1, v5
	v_mul_u32_u24_e32 v6, 0xc40, v6
	v_mov_b32_e32 v7, v35
	v_xor_b32_e32 v10, v5, v0
	v_lshlrev_b64 v[6:7], 1, v[6:7]
	v_lshlrev_b32_e32 v10, 4, v10
	v_lshl_add_u64 v[8:9], s[6:7], 0, v[6:7]
	v_and_b32_e32 v10, 0x70, v10
	v_mov_b32_e32 v11, v35
	v_lshl_add_u64 v[8:9], v[8:9], 0, v[10:11]
	v_or_b32_e32 v10, 16, v12
	v_mul_u32_u24_e32 v10, 0xc40, v10
	v_lshlrev_b64 v[10:11], 1, v[10:11]
	v_lshl_add_u64 v[12:13], s[6:7], 0, v[10:11]
	v_xor_b32_e32 v14, 16, v4
	v_mov_b32_e32 v15, v35
	v_or_b32_e32 v18, 24, v16
	v_lshl_add_u64 v[12:13], v[12:13], 0, v[14:15]
	v_or_b32_e32 v14, s3, v18
	v_lshrrev_b32_e32 v18, 1, v18
	v_mul_u32_u24_e32 v14, 0xc40, v14
	v_xor_b32_e32 v18, v18, v0
	v_lshlrev_b64 v[14:15], 1, v[14:15]
	v_lshlrev_b32_e32 v18, 3, v18
	s_cmpk_lt_u32 s2, 0x60
	v_lshl_add_u64 v[16:17], s[6:7], 0, v[14:15]
	v_bitop3_b32 v18, v18, 8, 56 bitop3:0x6c
	s_cselect_b64 s[6:7], -1, 0
	v_lshlrev_b32_e32 v18, 1, v18
	v_mov_b32_e32 v19, v35
	s_and_b64 s[24:25], s[6:7], exec
	v_lshlrev_b32_e32 v83, 12, v136
	v_and_b32_e32 v20, 7, v0
	v_lshl_add_u64 v[16:17], v[16:17], 0, v[18:19]
	s_cselect_b32 s24, s28, s29
	v_lshl_or_b32 v19, v136, 4, v131
	v_readfirstlane_b32 s25, v83
	v_bitop3_b32 v30, v136, v20, 1 bitop3:0x6c
	v_or_b32_e32 v20, s24, v19
	s_mov_b32 m0, s25
	s_add_u32 s28, s18, s4
	v_mul_i32_i24_e32 v20, 0xc40, v20
	v_mov_b32_e32 v21, v35
	global_load_lds_dwordx4 v[2:3], off
	v_or_b32_e32 v2, 0x400, v83
	s_addc_u32 s29, s19, 0
	v_lshlrev_b64 v[20:21], 1, v[20:21]
	v_xor_b32_e32 v24, v30, v24
	v_readfirstlane_b32 s25, v2
	v_or_b32_e32 v2, 0x800, v83
	v_lshl_add_u64 v[22:23], s[28:29], 0, v[20:21]
	v_lshlrev_b32_e32 v24, 4, v24
	v_mov_b32_e32 v25, v35
	v_or_b32_e32 v19, 8, v19
	s_mov_b32 m0, s25
	v_readfirstlane_b32 s25, v2
	v_or_b32_e32 v2, 0xc00, v83
	v_lshl_add_u64 v[22:23], v[22:23], 0, v[24:25]
	v_or_b32_e32 v25, s24, v19
	global_load_lds_dwordx4 v[8:9], off
	s_mov_b32 m0, s25
	v_readfirstlane_b32 s25, v2
	v_lshlrev_b32_e32 v2, 11, v136
	v_mul_i32_i24_e32 v26, 0xc40, v25
	v_mov_b32_e32 v27, v35
	v_bfe_u32 v19, v19, 1, 3
	v_or_b32_e32 v85, 0x10000, v2
	v_lshlrev_b64 v[26:27], 1, v[26:27]
	v_xor_b32_e32 v19, v30, v19
	global_load_lds_dwordx4 v[12:13], off
	s_mov_b32 m0, s25
	v_readfirstlane_b32 s25, v85
	v_or_b32_e32 v2, 0x10400, v2
	v_lshl_add_u64 v[28:29], s[28:29], 0, v[26:27]
	v_lshlrev_b32_e32 v30, 4, v19
	v_mov_b32_e32 v31, v35
	global_load_lds_dwordx4 v[16:17], off
	s_mov_b32 m0, s25
	v_readfirstlane_b32 s25, v2
	v_lshl_add_u64 v[28:29], v[28:29], 0, v[30:31]
	global_load_lds_dwordx4 v[22:23], off
	s_mov_b32 m0, s25
	v_bfe_u32 v138, v0, 5, 1
	global_load_lds_dwordx4 v[28:29], off
	v_lshrrev_b32_e32 v2, 1, v0
	v_bfe_u32 v3, v0, 4, 1
	v_bitop3_b32 v2, v2, v3, 7 bitop3:0x6c
	v_or_b32_e32 v8, 2, v138
	v_xor_b32_e32 v8, v8, v2
	v_lshlrev_b32_e32 v84, 4, v8
	v_or_b32_e32 v8, 4, v138
	v_xor_b32_e32 v8, v8, v2
	v_lshrrev_b32_e32 v1, 7, v0
	v_xor_b32_e32 v3, v2, v138
	v_lshlrev_b32_e32 v82, 4, v8
	v_or_b32_e32 v8, 6, v138
	v_bfe_u32 v126, v0, 6, 1
	v_and_b32_e32 v139, 31, v0
	v_lshlrev_b32_e32 v3, 4, v3
	v_lshlrev_b32_e32 v80, 13, v1
	v_lshl_add_u32 v148, v1, 6, s3
	v_or_b32_e32 v148, v148, v131
	v_lshlrev_b32_e32 v148, 2, v148
	global_load_dword v147, v148, s[14:15]
	global_load_dword v146, v148, s[14:15] offset:32
	global_load_dword v145, v148, s[14:15] offset:64
	global_load_dword v144, v148, s[14:15] offset:96
	global_load_dword v142, v148, s[14:15] offset:128
	global_load_dword v141, v148, s[14:15] offset:160
	global_load_dword v140, v148, s[14:15] offset:192
	global_load_dword v130, v148, s[14:15] offset:224
	v_xor_b32_e32 v2, v8, v2
	v_lshlrev_b32_e32 v78, 7, v139
	v_lshlrev_b32_e32 v79, 13, v126
	v_lshlrev_b32_e32 v81, 4, v2
	v_or_b32_e32 v2, v3, v80
	v_add_u32_e32 v86, v2, v78
	v_or3_b32 v2, v3, v79, v78
	v_add_u32_e32 v87, 0x10000, v2
	v_or_b32_e32 v2, s4, v4
	v_mov_b32_e32 v3, v35
	v_lshl_add_u64 v[2:3], v[2:3], 0, v[34:35]
	v_lshl_add_u64 v[2:3], s[16:17], 0, v[2:3]
	s_mov_b64 s[28:29], 0x80
	v_lshl_add_u64 v[66:67], v[2:3], 0, s[28:29]
	v_bitop3_b32 v2, v5, 7, v0 bitop3:0x48
	v_lshl_or_b32 v34, v2, 4, s4
	v_lshl_add_u64 v[2:3], v[34:35], 0, v[6:7]
	s_mov_b32 s5, 0
	v_lshl_add_u64 v[2:3], s[16:17], 0, v[2:3]
	v_lshl_add_u64 v[68:69], v[2:3], 0, s[28:29]
	v_lshl_add_u64 v[2:3], s[4:5], 0, v[10:11]
	v_bitop3_b32 v2, v2, v4, 16 bitop3:0xf6
	v_lshl_add_u64 v[2:3], s[16:17], 0, v[2:3]
	v_lshl_add_u64 v[70:71], v[2:3], 0, s[28:29]
	v_lshl_add_u64 v[2:3], s[4:5], 0, v[14:15]
	v_or_b32_e32 v2, v2, v18
	v_lshl_add_u64 v[2:3], s[16:17], 0, v[2:3]
	v_or_b32_e32 v34, s4, v24
	v_lshl_add_u64 v[72:73], v[2:3], 0, s[28:29]
	v_lshl_add_u64 v[2:3], v[34:35], 0, v[20:21]
	v_lshl_add_u64 v[2:3], s[18:19], 0, v[2:3]
	v_or_b32_e32 v34, s4, v30
	s_waitcnt vmcnt(0)
	v_lshl_add_u64 v[74:75], v[2:3], 0, s[28:29]
	v_lshl_add_u64 v[2:3], v[34:35], 0, v[26:27]
	v_lshl_add_u64 v[2:3], s[18:19], 0, v[2:3]
	v_lshl_add_u64 v[76:77], v[2:3], 0, s[28:29]
	s_mov_b64 s[16:17], 0
	v_mov_b32_e32 v88, 0x8000
	v_mov_b32_e32 v34, v35
	v_mov_b32_e32 v36, v35
	v_mov_b32_e32 v37, v35
	v_mov_b32_e32 v38, v35
	v_mov_b32_e32 v39, v35
	v_mov_b32_e32 v40, v35
	v_mov_b32_e32 v41, v35
	v_mov_b32_e32 v42, v35
	v_mov_b32_e32 v43, v35
	v_mov_b32_e32 v44, v35
	v_mov_b32_e32 v45, v35
	v_mov_b32_e32 v46, v35
	v_mov_b32_e32 v47, v35
	v_mov_b32_e32 v48, v35
	v_mov_b32_e32 v49, v35
	v_mov_b32_e32 v50, v35
	v_mov_b32_e32 v51, v35
	v_mov_b32_e32 v52, v35
	v_mov_b32_e32 v53, v35
	v_mov_b32_e32 v54, v35
	v_mov_b32_e32 v55, v35
	v_mov_b32_e32 v56, v35
	v_mov_b32_e32 v57, v35
	v_mov_b32_e32 v58, v35
	v_mov_b32_e32 v59, v35
	v_mov_b32_e32 v60, v35
	v_mov_b32_e32 v61, v35
	v_mov_b32_e32 v62, v35
	v_mov_b32_e32 v63, v35
	v_mov_b32_e32 v64, v35
	v_mov_b32_e32 v65, v35
	v_mov_b32_e32 v18, v35
	v_mov_b32_e32 v19, v35
	v_mov_b32_e32 v20, v35
	v_mov_b32_e32 v21, v35
	v_mov_b32_e32 v22, v35
	v_mov_b32_e32 v23, v35
	v_mov_b32_e32 v24, v35
	v_mov_b32_e32 v25, v35
	v_mov_b32_e32 v26, v35
	v_mov_b32_e32 v27, v35
	v_mov_b32_e32 v28, v35
	v_mov_b32_e32 v29, v35
	v_mov_b32_e32 v30, v35
	v_mov_b32_e32 v32, v35
	v_mov_b32_e32 v33, v35
	v_mov_b32_e32 v2, v35
	v_mov_b32_e32 v3, v35
	v_mov_b32_e32 v4, v35
	v_mov_b32_e32 v5, v35
	v_mov_b32_e32 v6, v35
	v_mov_b32_e32 v7, v35
	v_mov_b32_e32 v8, v35
	v_mov_b32_e32 v9, v35
	v_mov_b32_e32 v10, v35
	v_mov_b32_e32 v11, v35
	v_mov_b32_e32 v12, v35
	v_mov_b32_e32 v13, v35
	v_mov_b32_e32 v14, v35
	v_mov_b32_e32 v15, v35
	v_mov_b32_e32 v16, v35
	v_mov_b32_e32 v17, v35
	s_waitcnt vmcnt(0) lgkmcnt(0)
	s_barrier

	.amdhsa_kernel _Z7gemm2_kILi3ELi2ELi2EEv5GArgs
		.amdhsa_group_segment_fixed_size 98304
		.amdhsa_private_segment_fixed_size 0
		.amdhsa_kernarg_size 136
		.amdhsa_user_sgpr_count 2
		.amdhsa_user_sgpr_dispatch_ptr 0
		.amdhsa_user_sgpr_queue_ptr 0
		.amdhsa_user_sgpr_kernarg_segment_ptr 1
		.amdhsa_user_sgpr_dispatch_id 0
		.amdhsa_user_sgpr_kernarg_preload_length 0
		.amdhsa_user_sgpr_kernarg_preload_offset 0
		.amdhsa_user_sgpr_private_segment_size 0
		.amdhsa_uses_dynamic_stack 0
		.amdhsa_enable_private_segment 0
		.amdhsa_system_sgpr_workgroup_id_x 1
		.amdhsa_system_sgpr_workgroup_id_y 0
		.amdhsa_system_sgpr_workgroup_id_z 0
		.amdhsa_system_sgpr_workgroup_info 0
		.amdhsa_system_vgpr_workitem_id 0
		.amdhsa_next_free_vgpr 172
		.amdhsa_next_free_sgpr 96
		.amdhsa_accum_offset 172
		.amdhsa_reserve_vcc 1
		.amdhsa_float_round_mode_32 0
		.amdhsa_float_round_mode_16_64 0
		.amdhsa_float_denorm_mode_32 3
		.amdhsa_float_denorm_mode_16_64 3
		.amdhsa_dx10_clamp 1
		.amdhsa_ieee_mode 1
		.amdhsa_fp16_overflow 0
		.amdhsa_tg_split 0
		.amdhsa_exception_fp_ieee_invalid_op 0
		.amdhsa_exception_fp_denorm_src 0
		.amdhsa_exception_fp_ieee_div_zero 0
		.amdhsa_exception_fp_ieee_overflow 0
		.amdhsa_exception_fp_ieee_underflow 0
		.amdhsa_exception_fp_ieee_inexact 0
		.amdhsa_exception_int_div_zero 0
	.end_amdhsa_kernel

_Z7gemv8_kILi192ELi3072EEvPKfS1_Pf:
	v_lshlrev_b32_e32 v127, 4, v0
	s_getpc_b64 s[92:93]
	s_add_u32 s92, s92, 0xffff38f8
	s_addc_u32 s93, s93, 0xffffffff
	global_load_dword v127, v127, s[92:93]
	v_lshlrev_b32_e32 v127, 4, v0
	s_load_dwordx4 s[4:7], s[0:1], 0x0
	s_load_dwordx2 s[8:9], s[0:1], 0x10
	s_mul_i32 s0, s3, 0xc0
	s_ashr_i32 s1, s0, 31
	s_lshl_b64 s[10:11], s[0:1], 2
	s_waitcnt lgkmcnt(0)
	s_add_u32 s12, s4, s10
	s_addc_u32 s13, s5, s11
	s_mov_b64 s[4:5], 0
	s_mov_b32 s1, 0xaaab
	s_movk_i32 s10, 0x3000
	v_mov_b64_e32 v[2:3], s[12:13]
	v_mov_b32_e32 v5, 0
	s_movk_i32 s11, 0x300
	s_movk_i32 s12, 0x4ff
	v_mov_b32_e32 v1, v0

	.amdhsa_kernel _Z7gemv8_kILi192ELi3072EEvPKfS1_Pf
		.amdhsa_group_segment_fixed_size 38912
		.amdhsa_private_segment_fixed_size 0
		.amdhsa_kernarg_size 24
		.amdhsa_user_sgpr_count 2
		.amdhsa_user_sgpr_dispatch_ptr 0
		.amdhsa_user_sgpr_queue_ptr 0
		.amdhsa_user_sgpr_kernarg_segment_ptr 1
		.amdhsa_user_sgpr_dispatch_id 0
		.amdhsa_user_sgpr_kernarg_preload_length 0
		.amdhsa_user_sgpr_kernarg_preload_offset 0
		.amdhsa_user_sgpr_private_segment_size 0
		.amdhsa_uses_dynamic_stack 0
		.amdhsa_enable_private_segment 0
		.amdhsa_system_sgpr_workgroup_id_x 1
		.amdhsa_system_sgpr_workgroup_id_y 1
		.amdhsa_system_sgpr_workgroup_id_z 0
		.amdhsa_system_sgpr_workgroup_info 0
		.amdhsa_system_vgpr_workitem_id 0
		.amdhsa_next_free_vgpr 128
		.amdhsa_next_free_sgpr 96
		.amdhsa_accum_offset 128
		.amdhsa_reserve_vcc 1
		.amdhsa_float_round_mode_32 0
		.amdhsa_float_round_mode_16_64 0
		.amdhsa_float_denorm_mode_32 3
		.amdhsa_float_denorm_mode_16_64 3
		.amdhsa_dx10_clamp 1
		.amdhsa_ieee_mode 1
		.amdhsa_fp16_overflow 0
		.amdhsa_tg_split 0
		.amdhsa_exception_fp_ieee_invalid_op 0
		.amdhsa_exception_fp_denorm_src 0
		.amdhsa_exception_fp_ieee_div_zero 0
		.amdhsa_exception_fp_ieee_overflow 0
		.amdhsa_exception_fp_ieee_underflow 0
		.amdhsa_exception_fp_ieee_inexact 0
		.amdhsa_exception_int_div_zero 0
	.end_amdhsa_kernel

amdhsa.kernels:
  - .agpr_count:     0
    .args:
      - .address_space:  global
        .offset:         0
        .size:           8
        .value_kind:     global_buffer
    .group_segment_fixed_size: 0
    .kernarg_segment_align: 8
    .kernarg_segment_size: 8
    .language:       OpenCL C
    .language_version:
      - 2
      - 0
    .max_flat_workgroup_size: 1024
    .name:           _Z7empty_kPi
    .private_segment_fixed_size: 0
    .sgpr_count:     6
    .sgpr_spill_count: 0
    .symbol:         _Z7empty_kPi.kd
    .uniform_work_group_size: 1
    .uses_dynamic_stack: false
    .vgpr_count:     0
    .vgpr_spill_count: 0
    .wavefront_size: 64
  - .agpr_count:     0
    .args:
      - .actual_access:  read_only
        .address_space:  global
        .offset:         0
        .size:           8
        .value_kind:     global_buffer
      - .actual_access:  read_only
        .address_space:  global
        .offset:         8
        .size:           8
        .value_kind:     global_buffer
      - .actual_access:  read_only
        .address_space:  global
        .offset:         16
        .size:           8
        .value_kind:     global_buffer
      - .actual_access:  read_only
        .address_space:  global
        .offset:         24
        .size:           8
        .value_kind:     global_buffer
      - .actual_access:  write_only
        .address_space:  global
        .offset:         32
        .size:           8
        .value_kind:     global_buffer
      - .actual_access:  write_only
        .address_space:  global
        .offset:         40
        .size:           8
        .value_kind:     global_buffer
    .group_segment_fixed_size: 0
    .kernarg_segment_align: 8
    .kernarg_segment_size: 48
    .language:       OpenCL C
    .language_version:
      - 2
      - 0
    .max_flat_workgroup_size: 256
    .name:           _Z4ln_kPKfS0_S0_S0_PfPDF16_
    .private_segment_fixed_size: 0
    .sgpr_count:     22
    .sgpr_spill_count: 0
    .symbol:         _Z4ln_kPKfS0_S0_S0_PfPDF16_.kd
    .uniform_work_group_size: 1
    .uses_dynamic_stack: false
    .vgpr_count:     61
    .vgpr_spill_count: 0
    .wavefront_size: 64
  - .agpr_count:     0
    .args:
      - .actual_access:  read_only
        .address_space:  global
        .offset:         0
        .size:           8
        .value_kind:     global_buffer
      - .actual_access:  read_only
        .address_space:  global
        .offset:         8
        .size:           8
        .value_kind:     global_buffer
      - .actual_access:  read_only
        .address_space:  global
        .offset:         16
        .size:           8
        .value_kind:     global_buffer
      - .actual_access:  read_only
        .address_space:  global
        .offset:         24
        .size:           8
        .value_kind:     global_buffer
      - .actual_access:  read_only
        .address_space:  global
        .offset:         32
        .size:           8
        .value_kind:     global_buffer
      - .actual_access:  write_only
        .address_space:  global
        .offset:         40
        .size:           8
        .value_kind:     global_buffer
      - .actual_access:  write_only
        .address_space:  global
        .offset:         48
        .size:           8
        .value_kind:     global_buffer
      - .actual_access:  write_only
        .address_space:  global
        .offset:         56
        .size:           8
        .value_kind:     global_buffer
      - .actual_access:  write_only
        .address_space:  global
        .offset:         64
        .size:           8
        .value_kind:     global_buffer
      - .offset:         72
        .size:           4
        .value_kind:     by_value
    .group_segment_fixed_size: 24704
    .kernarg_segment_align: 8
    .kernarg_segment_size: 76
    .language:       OpenCL C
    .language_version:
      - 2
      - 0
    .max_flat_workgroup_size: 1024
    .name:           _Z11ln_router_kPKfS0_S0_S0_S0_PfPDF16_PiS1_i
    .private_segment_fixed_size: 0
    .sgpr_count:     36
    .sgpr_spill_count: 0
    .symbol:         _Z11ln_router_kPKfS0_S0_S0_S0_PfPDF16_PiS1_i.kd
    .uniform_work_group_size: 1
    .uses_dynamic_stack: false
    .vgpr_count:     58
    .vgpr_spill_count: 0
    .wavefront_size: 64
  - .agpr_count:     0
    .args:
      - .actual_access:  read_only
        .address_space:  global
        .offset:         0
        .size:           8
        .value_kind:     global_buffer
      - .actual_access:  write_only
        .address_space:  global
        .offset:         8
        .size:           8
        .value_kind:     global_buffer
      - .actual_access:  write_only
        .address_space:  global
        .offset:         16
        .size:           8
        .value_kind:     global_buffer
    .group_segment_fixed_size: 4176
    .kernarg_segment_align: 8
    .kernarg_segment_size: 24
    .language:       OpenCL C
    .language_version:
      - 2
      - 0
    .max_flat_workgroup_size: 1024
    .name:           _Z6sort_kPKiPiS1_
    .private_segment_fixed_size: 0
    .sgpr_count:     102
    .sgpr_spill_count: 0
    .symbol:         _Z6sort_kPKiPiS1_.kd
    .uniform_work_group_size: 1
    .uses_dynamic_stack: false
    .vgpr_count:     50
    .vgpr_spill_count: 0
    .wavefront_size: 64
  - .agpr_count:     0
    .args:
      - .offset:         0
        .size:           272
        .value_kind:     by_value
      - .actual_access:  read_only
        .address_space:  global
        .offset:         272
        .size:           8
        .value_kind:     global_buffer
      - .actual_access:  read_only
        .address_space:  global
        .offset:         280
        .size:           8
        .value_kind:     global_buffer
      - .actual_access:  read_only
        .address_space:  global
        .offset:         288
        .size:           8
        .value_kind:     global_buffer
      - .actual_access:  read_only
        .address_space:  global
        .offset:         296
        .size:           8
        .value_kind:     global_buffer
      - .actual_access:  read_only
        .address_space:  global
        .offset:         304
        .size:           8
        .value_kind:     global_buffer
      - .actual_access:  read_only
        .address_space:  global
        .offset:         312
        .size:           8
        .value_kind:     global_buffer
      - .actual_access:  read_only
        .address_space:  global
        .offset:         320
        .size:           8
        .value_kind:     global_buffer
      - .actual_access:  write_only
        .address_space:  global
        .offset:         328
        .size:           8
        .value_kind:     global_buffer
      - .actual_access:  write_only
        .address_space:  global
        .offset:         336
        .size:           8
        .value_kind:     global_buffer
      - .actual_access:  write_only
        .address_space:  global
        .offset:         344
        .size:           8
        .value_kind:     global_buffer
    .group_segment_fixed_size: 16640
    .kernarg_segment_align: 8
    .kernarg_segment_size: 352
    .language:       OpenCL C
    .language_version:
      - 2
      - 0
    .max_flat_workgroup_size: 256
    .name:           _Z5pre_k7CvtArgsPKiS1_PKfS3_S3_S3_S3_PfPDF16_S4_
    .private_segment_fixed_size: 0
    .sgpr_count:     24
    .sgpr_spill_count: 0
    .symbol:         _Z5pre_k7CvtArgsPKiS1_PKfS3_S3_S3_S3_PfPDF16_S4_.kd
    .uniform_work_group_size: 1
    .uses_dynamic_stack: false
    .vgpr_count:     69
    .vgpr_spill_count: 0
    .wavefront_size: 64
  - .agpr_count:     0
    .args:
      - .actual_access:  read_only
        .address_space:  global
        .offset:         0
        .size:           8
        .value_kind:     global_buffer
      - .actual_access:  read_only
        .address_space:  global
        .offset:         8
        .size:           8
        .value_kind:     global_buffer
      - .actual_access:  read_only
        .address_space:  global
        .offset:         16
        .size:           8
        .value_kind:     global_buffer
      - .actual_access:  read_only
        .address_space:  global
        .offset:         24
        .size:           8
        .value_kind:     global_buffer
      - .actual_access:  write_only
        .address_space:  global
        .offset:         32
        .size:           8
        .value_kind:     global_buffer
      - .actual_access:  read_only
        .address_space:  global
        .offset:         40
        .size:           8
        .value_kind:     global_buffer
      - .offset:         48
        .size:           4
        .value_kind:     by_value
      - .actual_access:  write_only
        .address_space:  global
        .offset:         56
        .size:           8
        .value_kind:     global_buffer
    .group_segment_fixed_size: 133120
    .kernarg_segment_align: 8
    .kernarg_segment_size: 64
    .language:       OpenCL C
    .language_version:
      - 2
      - 0
    .max_flat_workgroup_size: 512
    .name:           _Z6attn_kPKDF16_S0_S0_PKfPDF16_PK15HIP_vector_typeIfLj4EEiPf
    .private_segment_fixed_size: 0
    .sgpr_count:     102
    .sgpr_spill_count: 0
    .symbol:         _Z6attn_kPKDF16_S0_S0_PKfPDF16_PK15HIP_vector_typeIfLj4EEiPf.kd
    .uniform_work_group_size: 1
    .uses_dynamic_stack: false
    .vgpr_count:     112
    .vgpr_spill_count: 0
    .wavefront_size: 64
  - .agpr_count:     0
    .args:
      - .actual_access:  read_only
        .address_space:  global
        .offset:         0
        .size:           8
        .value_kind:     global_buffer
      - .actual_access:  read_only
        .address_space:  global
        .offset:         8
        .size:           8
        .value_kind:     global_buffer
      - .actual_access:  read_only
        .address_space:  global
        .offset:         16
        .size:           8
        .value_kind:     global_buffer
      - .actual_access:  read_only
        .address_space:  global
        .offset:         24
        .size:           8
        .value_kind:     global_buffer
      - .actual_access:  write_only
        .address_space:  global
        .offset:         32
        .size:           8
        .value_kind:     global_buffer
      - .actual_access:  read_only
        .address_space:  global
        .offset:         40
        .size:           8
        .value_kind:     global_buffer
      - .actual_access:  read_only
        .address_space:  global
        .offset:         48
        .size:           8
        .value_kind:     global_buffer
      - .actual_access:  write_only
        .address_space:  global
        .offset:         56
        .size:           8
        .value_kind:     global_buffer
      - .actual_access:  read_only
        .address_space:  global
        .offset:         64
        .size:           8
        .value_kind:     global_buffer
      - .offset:         72
        .size:           4
        .value_kind:     by_value
      - .actual_access:  read_only
        .address_space:  global
        .offset:         80
        .size:           8
        .value_kind:     global_buffer
      - .offset:         88
        .size:           4
        .value_kind:     by_value
      - .actual_access:  write_only
        .address_space:  global
        .offset:         96
        .size:           8
        .value_kind:     global_buffer
    .group_segment_fixed_size: 7168
    .kernarg_segment_align: 8
    .kernarg_segment_size: 104
    .language:       OpenCL C
    .language_version:
      - 2
      - 0
    .max_flat_workgroup_size: 256
    .name:           _Z9tail_up_kPKfPKiS0_S0_PfS0_S2_S3_PK15HIP_vector_typeIfLj4EEiS7_iS3_
    .private_segment_fixed_size: 0
    .sgpr_count:     72
    .sgpr_spill_count: 0
    .symbol:         _Z9tail_up_kPKfPKiS0_S0_PfS0_S2_S3_PK15HIP_vector_typeIfLj4EEiS7_iS3_.kd
    .uniform_work_group_size: 1
    .uses_dynamic_stack: false
    .vgpr_count:     114
    .vgpr_spill_count: 0
    .wavefront_size: 64
  - .agpr_count:     0
    .args:
      - .actual_access:  read_only
        .address_space:  global
        .offset:         0
        .size:           8
        .value_kind:     global_buffer
      - .offset:         8
        .size:           4
        .value_kind:     by_value
      - .actual_access:  read_only
        .address_space:  global
        .offset:         16
        .size:           8
        .value_kind:     global_buffer
      - .actual_access:  read_only
        .address_space:  global
        .offset:         24
        .size:           8
        .value_kind:     global_buffer
      - .actual_access:  read_only
        .address_space:  global
        .offset:         32
        .size:           8
        .value_kind:     global_buffer
      - .actual_access:  read_only
        .address_space:  global
        .offset:         40
        .size:           8
        .value_kind:     global_buffer
      - .actual_access:  write_only
        .address_space:  global
        .offset:         48
        .size:           8
        .value_kind:     global_buffer
    .group_segment_fixed_size: 0
    .kernarg_segment_align: 8
    .kernarg_segment_size: 56
    .language:       OpenCL C
    .language_version:
      - 2
      - 0
    .max_flat_workgroup_size: 512
    .name:           _Z9tail_ln_kPKfiS0_S0_S0_S0_Pf
    .private_segment_fixed_size: 0
    .sgpr_count:     22
    .sgpr_spill_count: 0
    .symbol:         _Z9tail_ln_kPKfiS0_S0_S0_S0_Pf.kd
    .uniform_work_group_size: 1
    .uses_dynamic_stack: false
    .vgpr_count:     48
    .vgpr_spill_count: 0
    .wavefront_size: 64
  - .agpr_count:     0
    .args:
      - .actual_access:  read_only
        .address_space:  global
        .offset:         0
        .size:           8
        .value_kind:     global_buffer
      - .actual_access:  read_only
        .address_space:  global
        .offset:         8
        .size:           8
        .value_kind:     global_buffer
      - .actual_access:  read_only
        .address_space:  global
        .offset:         16
        .size:           8
        .value_kind:     global_buffer
      - .actual_access:  read_only
        .address_space:  global
        .offset:         24
        .size:           8
        .value_kind:     global_buffer
      - .actual_access:  read_only
        .address_space:  global
        .offset:         32
        .size:           8
        .value_kind:     global_buffer
      - .actual_access:  read_only
        .address_space:  global
        .offset:         40
        .size:           8
        .value_kind:     global_buffer
      - .actual_access:  write_only
        .address_space:  global
        .offset:         48
        .size:           8
        .value_kind:     global_buffer
      - .actual_access:  write_only
        .address_space:  global
        .offset:         56
        .size:           8
        .value_kind:     global_buffer
    .group_segment_fixed_size: 47872
    .kernarg_segment_align: 8
    .kernarg_segment_size: 64
    .language:       OpenCL C
    .language_version:
      - 2
      - 0
    .max_flat_workgroup_size: 256
    .name:           _Z6pool_kPKfS0_S0_S0_S0_S0_PfS1_
    .private_segment_fixed_size: 0
    .sgpr_count:     102
    .sgpr_spill_count: 0
    .symbol:         _Z6pool_kPKfS0_S0_S0_S0_S0_PfS1_.kd
    .uniform_work_group_size: 1
    .uses_dynamic_stack: false
    .vgpr_count:     222
    .vgpr_spill_count: 0
    .wavefront_size: 64
  - .agpr_count:     0
    .args:
      - .actual_access:  read_only
        .address_space:  global
        .offset:         0
        .size:           8
        .value_kind:     global_buffer
      - .actual_access:  read_only
        .address_space:  global
        .offset:         8
        .size:           8
        .value_kind:     global_buffer
      - .actual_access:  read_only
        .address_space:  global
        .offset:         16
        .size:           8
        .value_kind:     global_buffer
      - .actual_access:  read_only
        .address_space:  global
        .offset:         24
        .size:           8
        .value_kind:     global_buffer
      - .actual_access:  read_only
        .address_space:  global
        .offset:         32
        .size:           8
        .value_kind:     global_buffer
      - .actual_access:  read_only
        .address_space:  global
        .offset:         40
        .size:           8
        .value_kind:     global_buffer
      - .actual_access:  write_only
        .address_space:  global
        .offset:         48
        .size:           8
        .value_kind:     global_buffer
    .group_segment_fixed_size: 16
    .kernarg_segment_align: 8
    .kernarg_segment_size: 56
    .language:       OpenCL C
    .language_version:
      - 2
      - 0
    .max_flat_workgroup_size: 256
    .name:           _Z8final2_kPKfS0_S0_S0_S0_S0_Pf
    .private_segment_fixed_size: 0
    .sgpr_count:     52
    .sgpr_spill_count: 0
    .symbol:         _Z8final2_kPKfS0_S0_S0_S0_S0_Pf.kd
    .uniform_work_group_size: 1
    .uses_dynamic_stack: false
    .vgpr_count:     67
    .vgpr_spill_count: 0
    .wavefront_size: 64
  - .agpr_count:     0
    .args:
      - .actual_access:  read_only
        .address_space:  global
        .offset:         0
        .size:           8
        .value_kind:     global_buffer
      - .offset:         8
        .size:           4
        .value_kind:     by_value
      - .actual_access:  read_only
        .address_space:  global
        .offset:         16
        .size:           8
        .value_kind:     global_buffer
      - .actual_access:  read_only
        .address_space:  global
        .offset:         24
        .size:           8
        .value_kind:     global_buffer
      - .actual_access:  read_only
        .address_space:  global
        .offset:         32
        .size:           8
        .value_kind:     global_buffer
      - .actual_access:  read_only
        .address_space:  global
        .offset:         40
        .size:           8
        .value_kind:     global_buffer
      - .actual_access:  write_only
        .address_space:  global
        .offset:         48
        .size:           8
        .value_kind:     global_buffer
    .group_segment_fixed_size: 0
    .kernarg_segment_align: 8
    .kernarg_segment_size: 56
    .language:       OpenCL C
    .language_version:
      - 2
      - 0
    .max_flat_workgroup_size: 512
    .name:           _Z7final_kPKfiS0_S0_S0_S0_Pf
    .private_segment_fixed_size: 0
    .sgpr_count:     36
    .sgpr_spill_count: 0
    .symbol:         _Z7final_kPKfiS0_S0_S0_S0_Pf.kd
    .uniform_work_group_size: 1
    .uses_dynamic_stack: false
    .vgpr_count:     20
    .vgpr_spill_count: 0
    .wavefront_size: 64
  - .agpr_count:     0
    .args:
      - .offset:         0
        .size:           136
        .value_kind:     by_value
    .group_segment_fixed_size: 114688
    .kernarg_segment_align: 8
    .kernarg_segment_size: 136
    .language:       OpenCL C
    .language_version:
      - 2
      - 0
    .max_flat_workgroup_size: 512
    .name:           _Z7gemm2_kILi0ELi3ELi1EEv5GArgs
    .private_segment_fixed_size: 0
    .sgpr_count:     102
    .sgpr_spill_count: 0
    .symbol:         _Z7gemm2_kILi0ELi3ELi1EEv5GArgs.kd
    .uniform_work_group_size: 1
    .uses_dynamic_stack: false
    .vgpr_count:     188
    .vgpr_spill_count: 0
    .wavefront_size: 64
  - .agpr_count:     0
    .args:
      - .offset:         0
        .size:           136
        .value_kind:     by_value
    .group_segment_fixed_size: 131072
    .kernarg_segment_align: 8
    .kernarg_segment_size: 136
    .language:       OpenCL C
    .language_version:
      - 2
      - 0
    .max_flat_workgroup_size: 512
    .name:           _Z6gemm_kILi1ELi128ELi4ELi8EEv5GArgs
    .private_segment_fixed_size: 0
    .sgpr_count:     102
    .sgpr_spill_count: 0
    .symbol:         _Z6gemm_kILi1ELi128ELi4ELi8EEv5GArgs.kd
    .uniform_work_group_size: 1
    .uses_dynamic_stack: false
    .vgpr_count:     76
    .vgpr_spill_count: 0
    .wavefront_size: 64
  - .agpr_count:     0
    .args:
      - .offset:         0
        .size:           136
        .value_kind:     by_value
    .group_segment_fixed_size: 81920
    .kernarg_segment_align: 8
    .kernarg_segment_size: 136
    .language:       OpenCL C
    .language_version:
      - 2
      - 0
    .max_flat_workgroup_size: 256
    .name:           _Z6gemm_kILi2ELi128ELi2ELi4EEv5GArgs
    .private_segment_fixed_size: 0
    .sgpr_count:     102
    .sgpr_spill_count: 0
    .symbol:         _Z6gemm_kILi2ELi128ELi2ELi4EEv5GArgs.kd
    .uniform_work_group_size: 1
    .uses_dynamic_stack: false
    .vgpr_count:     196
    .vgpr_spill_count: 0
    .wavefront_size: 64
  - .agpr_count:     0
    .args:
      - .offset:         0
        .size:           136
        .value_kind:     by_value
    .group_segment_fixed_size: 98304
    .kernarg_segment_align: 8
    .kernarg_segment_size: 136
    .language:       OpenCL C
    .language_version:
      - 2
      - 0
    .max_flat_workgroup_size: 512
    .name:           _Z7gemm2_kILi3ELi2ELi2EEv5GArgs
    .private_segment_fixed_size: 0
    .sgpr_count:     102
    .sgpr_spill_count: 0
    .symbol:         _Z7gemm2_kILi3ELi2ELi2EEv5GArgs.kd
    .uniform_work_group_size: 1
    .uses_dynamic_stack: false
    .vgpr_count:     172
    .vgpr_spill_count: 0
    .wavefront_size: 64
  - .agpr_count:     0
    .args:
      - .actual_access:  read_only
        .address_space:  global
        .offset:         0
        .size:           8
        .value_kind:     global_buffer
      - .actual_access:  read_only
        .address_space:  global
        .offset:         8
        .size:           8
        .value_kind:     global_buffer
      - .actual_access:  write_only
        .address_space:  global
        .offset:         16
        .size:           8
        .value_kind:     global_buffer
    .group_segment_fixed_size: 38912
    .kernarg_segment_align: 8
    .kernarg_segment_size: 24
    .language:       OpenCL C
    .language_version:
      - 2
      - 0
    .max_flat_workgroup_size: 256
    .name:           _Z7gemv8_kILi192ELi3072EEvPKfS1_Pf
    .private_segment_fixed_size: 0
    .sgpr_count:     102
    .sgpr_spill_count: 0
    .symbol:         _Z7gemv8_kILi192ELi3072EEvPKfS1_Pf.kd
    .uniform_work_group_size: 1
    .uses_dynamic_stack: false
    .vgpr_count:     128
    .vgpr_spill_count: 0
    .wavefront_size: 64
